# every s_setprio removed (184 sites), second measurement
# speedup vs baseline: 1.0630x; 1.0630x over previous
.LBB0_120:
	ds_read_b128 v[136:139], v211
	ds_read_b128 v[140:143], v211 offset:1024
	ds_read_b128 v[144:147], v211 offset:2048
	ds_read_b128 v[148:151], v211 offset:3072
	ds_read_b128 v[152:155], v212
	ds_read_b128 v[156:159], v212 offset:1024
	ds_read_b128 v[160:163], v212 offset:2048
	ds_read_b128 v[186:189], v212 offset:3072
	s_add_u32 s41, s15, s18
	s_addc_u32 s42, s24, s19
	s_add_u32 s66, s18, 0x100
	s_addc_u32 s67, s19, 0
	s_cmp_eq_u32 s40, 28
	s_cselect_b64 s[70:71], -1, 0
	s_and_b64 s[2:3], s[70:71], exec
	s_cselect_b32 s69, s5, s42
	s_cselect_b32 s68, s13, s41
	s_cselect_b32 s41, 0, s66
	v_lshl_add_u64 v[198:199], v[132:133], 0, s[18:19]
	s_add_i32 m0, s92, 0xc000
	ds_read_b128 v[190:193], v213
	ds_read_b128 v[194:197], v213 offset:1024
	ds_read_b128 v[214:217], v213 offset:2048
	ds_read_b128 v[218:221], v213 offset:3072
	ds_read_b128 v[222:225], v213 offset:4096
	ds_read_b128 v[226:229], v213 offset:5120
	ds_read_b128 v[230:233], v213 offset:6144
	ds_read_b128 v[234:237], v213 offset:7168
	global_load_lds_dwordx4 v[198:199], off
	v_lshl_add_u64 v[198:199], v[134:135], 0, s[18:19]
	s_add_i32 m0, s92, 0xe000
	s_nop 0
	global_load_lds_dwordx4 v[198:199], off
	s_waitcnt vmcnt(8)
	s_waitcnt lgkmcnt(0)
	s_barrier
	s_waitcnt lgkmcnt(0)
	v_mfma_f32_16x16x32_bf16 v[128:131], v[136:139], v[190:193], v[128:131]
	v_mfma_f32_16x16x32_bf16 v[124:127], v[144:147], v[190:193], v[124:127]
	v_mfma_f32_16x16x32_bf16 v[120:123], v[136:139], v[214:217], v[120:123]
	v_mfma_f32_16x16x32_bf16 v[112:115], v[144:147], v[214:217], v[112:115]
	v_mfma_f32_16x16x32_bf16 v[104:107], v[136:139], v[222:225], v[104:107]
	v_mfma_f32_16x16x32_bf16 v[96:99], v[144:147], v[222:225], v[96:99]
	v_mfma_f32_16x16x32_bf16 v[88:91], v[136:139], v[230:233], v[88:91]
	v_mfma_f32_16x16x32_bf16 v[80:83], v[144:147], v[230:233], v[80:83]
	v_mfma_f32_16x16x32_bf16 v[128:131], v[140:143], v[194:197], v[128:131]
	v_mfma_f32_16x16x32_bf16 v[124:127], v[148:151], v[194:197], v[124:127]
	v_mfma_f32_16x16x32_bf16 v[120:123], v[140:143], v[218:221], v[120:123]
	v_mfma_f32_16x16x32_bf16 v[112:115], v[148:151], v[218:221], v[112:115]
	v_mfma_f32_16x16x32_bf16 v[104:107], v[140:143], v[226:229], v[104:107]
	v_mfma_f32_16x16x32_bf16 v[96:99], v[148:151], v[226:229], v[96:99]
	v_mfma_f32_16x16x32_bf16 v[88:91], v[140:143], v[234:237], v[88:91]
	v_mfma_f32_16x16x32_bf16 v[80:83], v[148:151], v[234:237], v[80:83]
	v_mfma_f32_16x16x32_bf16 v[116:119], v[152:155], v[190:193], v[116:119]
	v_mfma_f32_16x16x32_bf16 v[108:111], v[160:163], v[190:193], v[108:111]
	v_mfma_f32_16x16x32_bf16 v[100:103], v[152:155], v[214:217], v[100:103]
	v_mfma_f32_16x16x32_bf16 v[92:95], v[160:163], v[214:217], v[92:95]
	v_mfma_f32_16x16x32_bf16 v[84:87], v[152:155], v[222:225], v[84:87]
	v_mfma_f32_16x16x32_bf16 v[76:79], v[160:163], v[222:225], v[76:79]
	v_mfma_f32_16x16x32_bf16 v[72:75], v[152:155], v[230:233], v[72:75]
	v_mfma_f32_16x16x32_bf16 v[68:71], v[160:163], v[230:233], v[68:71]
	v_mfma_f32_16x16x32_bf16 v[116:119], v[156:159], v[194:197], v[116:119]
	v_mfma_f32_16x16x32_bf16 v[108:111], v[186:189], v[194:197], v[108:111]
	v_mfma_f32_16x16x32_bf16 v[100:103], v[156:159], v[218:221], v[100:103]
	v_mfma_f32_16x16x32_bf16 v[92:95], v[186:189], v[218:221], v[92:95]
	v_mfma_f32_16x16x32_bf16 v[84:87], v[156:159], v[226:229], v[84:87]
	v_mfma_f32_16x16x32_bf16 v[76:79], v[186:189], v[226:229], v[76:79]
	v_mfma_f32_16x16x32_bf16 v[72:75], v[156:159], v[234:237], v[72:75]
	v_mfma_f32_16x16x32_bf16 v[68:71], v[186:189], v[234:237], v[68:71]
	s_barrier
	s_add_i32 s2, s54, s96
	v_lshl_add_u64 v[198:199], s[68:69], 0, v[166:167]
	s_mov_b32 m0, s2
	ds_read_b128 v[190:193], v213 offset:16384
	ds_read_b128 v[194:197], v213 offset:17408
	ds_read_b128 v[214:217], v213 offset:18432
	ds_read_b128 v[218:221], v213 offset:19456
	ds_read_b128 v[222:225], v213 offset:20480
	ds_read_b128 v[226:229], v213 offset:21504
	ds_read_b128 v[230:233], v213 offset:22528
	ds_read_b128 v[234:237], v213 offset:23552
	global_load_lds_dwordx4 v[198:199], off
	s_add_i32 m0, s2, 0x2000
	s_add_u32 s2, s68, 0x80000
	v_lshl_add_u64 v[238:239], s[68:69], 0, v[170:171]
	s_addc_u32 s3, s69, 0
	s_add_i32 s18, s55, s96
	global_load_lds_dwordx4 v[238:239], off
	v_lshl_add_u64 v[240:241], s[2:3], 0, v[166:167]
	s_mov_b32 m0, s18
	s_nop 0
	global_load_lds_dwordx4 v[240:241], off
	v_lshl_add_u64 v[240:241], s[2:3], 0, v[170:171]
	s_add_i32 m0, s18, 0x2000
	s_and_b64 s[2:3], s[10:11], s[70:71]
	s_and_b64 s[2:3], s[2:3], exec
	s_cselect_b32 s2, s62, s16
	s_cselect_b32 s3, s63, s17
	s_add_u32 s2, s2, s41
	s_addc_u32 s3, s3, 0
	global_load_lds_dwordx4 v[240:241], off
	v_lshl_add_u64 v[240:241], s[2:3], 0, v[164:165]
	s_mov_b32 m0, s92
	v_lshl_add_u64 v[244:245], s[2:3], 0, v[168:169]
	global_load_lds_dwordx4 v[240:241], off
	s_mov_b32 m0, s52
	s_nop 0
	global_load_lds_dwordx4 v[244:245], off
	s_waitcnt vmcnt(8)
	s_waitcnt lgkmcnt(0)
	s_barrier
	s_waitcnt lgkmcnt(0)
	v_mfma_f32_16x16x32_bf16 v[64:67], v[136:139], v[190:193], v[64:67]
	v_mfma_f32_16x16x32_bf16 v[60:63], v[144:147], v[190:193], v[60:63]
	v_mfma_f32_16x16x32_bf16 v[52:55], v[136:139], v[214:217], v[52:55]
	v_mfma_f32_16x16x32_bf16 v[44:47], v[144:147], v[214:217], v[44:47]
	v_mfma_f32_16x16x32_bf16 v[36:39], v[136:139], v[222:225], v[36:39]
	v_mfma_f32_16x16x32_bf16 v[28:31], v[144:147], v[222:225], v[28:31]
	v_mfma_f32_16x16x32_bf16 v[20:23], v[136:139], v[230:233], v[20:23]
	v_mfma_f32_16x16x32_bf16 v[12:15], v[144:147], v[230:233], v[12:15]
	v_mfma_f32_16x16x32_bf16 v[64:67], v[140:143], v[194:197], v[64:67]
	v_mfma_f32_16x16x32_bf16 v[60:63], v[148:151], v[194:197], v[60:63]
	v_mfma_f32_16x16x32_bf16 v[52:55], v[140:143], v[218:221], v[52:55]
	v_mfma_f32_16x16x32_bf16 v[44:47], v[148:151], v[218:221], v[44:47]
	v_mfma_f32_16x16x32_bf16 v[36:39], v[140:143], v[226:229], v[36:39]
	v_mfma_f32_16x16x32_bf16 v[28:31], v[148:151], v[226:229], v[28:31]
	v_mfma_f32_16x16x32_bf16 v[20:23], v[140:143], v[234:237], v[20:23]
	v_mfma_f32_16x16x32_bf16 v[12:15], v[148:151], v[234:237], v[12:15]
	v_mfma_f32_16x16x32_bf16 v[56:59], v[152:155], v[190:193], v[56:59]
	v_mfma_f32_16x16x32_bf16 v[48:51], v[160:163], v[190:193], v[48:51]
	v_mfma_f32_16x16x32_bf16 v[40:43], v[152:155], v[214:217], v[40:43]
	v_mfma_f32_16x16x32_bf16 v[32:35], v[160:163], v[214:217], v[32:35]
	v_mfma_f32_16x16x32_bf16 v[24:27], v[152:155], v[222:225], v[24:27]
	v_mfma_f32_16x16x32_bf16 v[16:19], v[160:163], v[222:225], v[16:19]
	v_mfma_f32_16x16x32_bf16 v[8:11], v[152:155], v[230:233], v[8:11]
	v_mfma_f32_16x16x32_bf16 v[4:7], v[160:163], v[230:233], v[4:7]
	v_mfma_f32_16x16x32_bf16 v[56:59], v[156:159], v[194:197], v[56:59]
	v_mfma_f32_16x16x32_bf16 v[48:51], v[186:189], v[194:197], v[48:51]
	v_mfma_f32_16x16x32_bf16 v[40:43], v[156:159], v[218:221], v[40:43]
	v_mfma_f32_16x16x32_bf16 v[32:35], v[186:189], v[218:221], v[32:35]
	v_mfma_f32_16x16x32_bf16 v[24:27], v[156:159], v[226:229], v[24:27]
	v_mfma_f32_16x16x32_bf16 v[16:19], v[186:189], v[226:229], v[16:19]
	v_mfma_f32_16x16x32_bf16 v[8:11], v[156:159], v[234:237], v[8:11]
	v_mfma_f32_16x16x32_bf16 v[4:7], v[186:189], v[234:237], v[4:7]
	s_barrier
	s_add_i32 s18, 0, 0x18000
	v_add_u32_e32 v3, s18, v209
	s_add_i32 s19, 0, 0x1c000
	ds_read_b128 v[136:139], v3
	ds_read_b128 v[140:143], v3 offset:1024
	ds_read_b128 v[144:147], v3 offset:2048
	ds_read_b128 v[148:151], v3 offset:3072
	v_add_u32_e32 v3, s19, v209
	ds_read_b128 v[152:155], v3
	ds_read_b128 v[156:159], v3 offset:1024
	ds_read_b128 v[160:163], v3 offset:2048
	ds_read_b128 v[186:189], v3 offset:3072
	s_add_u32 s2, s2, 0x80000
	s_addc_u32 s3, s3, 0
	s_mov_b32 m0, s53
	v_lshl_add_u64 v[246:247], s[2:3], 0, v[164:165]
	ds_read_b128 v[190:193], v213 offset:32768
	ds_read_b128 v[194:197], v213 offset:33792
	ds_read_b128 v[214:217], v213 offset:34816
	ds_read_b128 v[218:221], v213 offset:35840
	ds_read_b128 v[222:225], v213 offset:36864
	ds_read_b128 v[226:229], v213 offset:37888
	ds_read_b128 v[230:233], v213 offset:38912
	ds_read_b128 v[234:237], v213 offset:39936
	global_load_lds_dwordx4 v[246:247], off
	v_lshl_add_u64 v[246:247], s[2:3], 0, v[168:169]
	s_mov_b32 m0, s50
	s_nop 0
	global_load_lds_dwordx4 v[246:247], off
	s_waitcnt vmcnt(8)
	s_waitcnt lgkmcnt(0)
	s_barrier
	s_waitcnt lgkmcnt(0)
	v_mfma_f32_16x16x32_bf16 v[128:131], v[136:139], v[190:193], v[128:131]
	v_mfma_f32_16x16x32_bf16 v[124:127], v[144:147], v[190:193], v[124:127]
	v_mfma_f32_16x16x32_bf16 v[120:123], v[136:139], v[214:217], v[120:123]
	v_mfma_f32_16x16x32_bf16 v[112:115], v[144:147], v[214:217], v[112:115]
	v_mfma_f32_16x16x32_bf16 v[104:107], v[136:139], v[222:225], v[104:107]
	v_mfma_f32_16x16x32_bf16 v[96:99], v[144:147], v[222:225], v[96:99]
	v_mfma_f32_16x16x32_bf16 v[88:91], v[136:139], v[230:233], v[88:91]
	v_mfma_f32_16x16x32_bf16 v[80:83], v[144:147], v[230:233], v[80:83]
	v_mfma_f32_16x16x32_bf16 v[128:131], v[140:143], v[194:197], v[128:131]
	v_mfma_f32_16x16x32_bf16 v[124:127], v[148:151], v[194:197], v[124:127]
	v_mfma_f32_16x16x32_bf16 v[120:123], v[140:143], v[218:221], v[120:123]
	v_mfma_f32_16x16x32_bf16 v[112:115], v[148:151], v[218:221], v[112:115]
	v_mfma_f32_16x16x32_bf16 v[104:107], v[140:143], v[226:229], v[104:107]
	v_mfma_f32_16x16x32_bf16 v[96:99], v[148:151], v[226:229], v[96:99]
	v_mfma_f32_16x16x32_bf16 v[88:91], v[140:143], v[234:237], v[88:91]
	v_mfma_f32_16x16x32_bf16 v[80:83], v[148:151], v[234:237], v[80:83]
	v_mfma_f32_16x16x32_bf16 v[116:119], v[152:155], v[190:193], v[116:119]
	v_mfma_f32_16x16x32_bf16 v[108:111], v[160:163], v[190:193], v[108:111]
	v_mfma_f32_16x16x32_bf16 v[100:103], v[152:155], v[214:217], v[100:103]
	v_mfma_f32_16x16x32_bf16 v[92:95], v[160:163], v[214:217], v[92:95]
	v_mfma_f32_16x16x32_bf16 v[84:87], v[152:155], v[222:225], v[84:87]
	v_mfma_f32_16x16x32_bf16 v[76:79], v[160:163], v[222:225], v[76:79]
	v_mfma_f32_16x16x32_bf16 v[72:75], v[152:155], v[230:233], v[72:75]
	v_mfma_f32_16x16x32_bf16 v[68:71], v[160:163], v[230:233], v[68:71]
	v_mfma_f32_16x16x32_bf16 v[116:119], v[156:159], v[194:197], v[116:119]
	v_mfma_f32_16x16x32_bf16 v[108:111], v[186:189], v[194:197], v[108:111]
	v_mfma_f32_16x16x32_bf16 v[100:103], v[156:159], v[218:221], v[100:103]
	v_mfma_f32_16x16x32_bf16 v[92:95], v[186:189], v[218:221], v[92:95]
	v_mfma_f32_16x16x32_bf16 v[84:87], v[156:159], v[226:229], v[84:87]
	v_mfma_f32_16x16x32_bf16 v[76:79], v[186:189], v[226:229], v[76:79]
	v_mfma_f32_16x16x32_bf16 v[72:75], v[156:159], v[234:237], v[72:75]
	v_mfma_f32_16x16x32_bf16 v[68:71], v[186:189], v[234:237], v[68:71]
	s_barrier
	s_add_i32 s2, s18, s96
	v_lshl_add_u64 v[198:199], v[198:199], 0, s[38:39]
	s_mov_b32 m0, s2
	ds_read_b128 v[190:193], v213 offset:49152
	ds_read_b128 v[194:197], v213 offset:50176
	ds_read_b128 v[214:217], v213 offset:51200
	ds_read_b128 v[218:221], v213 offset:52224
	ds_read_b128 v[222:225], v213 offset:53248
	ds_read_b128 v[226:229], v213 offset:54272
	ds_read_b128 v[230:233], v213 offset:55296
	ds_read_b128 v[234:237], v213 offset:56320
	global_load_lds_dwordx4 v[198:199], off
	s_add_i32 m0, s2, 0x2000
	s_add_u32 s2, s68, 0x80080
	v_lshl_add_u64 v[198:199], v[238:239], 0, s[38:39]
	s_addc_u32 s3, s69, 0
	s_add_i32 s18, s19, s96
	global_load_lds_dwordx4 v[198:199], off
	v_lshl_add_u64 v[198:199], s[2:3], 0, v[166:167]
	s_mov_b32 m0, s18
	s_nop 0
	global_load_lds_dwordx4 v[198:199], off
	v_lshl_add_u64 v[198:199], s[2:3], 0, v[170:171]
	s_add_i32 m0, s18, 0x2000
	s_nop 0
	global_load_lds_dwordx4 v[198:199], off
	v_lshl_add_u64 v[198:199], v[240:241], 0, s[38:39]
	s_mov_b32 m0, s56
	s_nop 0
	global_load_lds_dwordx4 v[198:199], off
	v_lshl_add_u64 v[198:199], v[244:245], 0, s[38:39]
	s_mov_b32 m0, s57
	s_nop 0
	global_load_lds_dwordx4 v[198:199], off
	s_waitcnt vmcnt(8)
	s_waitcnt lgkmcnt(0)
	s_barrier
	s_waitcnt lgkmcnt(0)
	v_mfma_f32_16x16x32_bf16 v[64:67], v[136:139], v[190:193], v[64:67]
	v_mfma_f32_16x16x32_bf16 v[60:63], v[144:147], v[190:193], v[60:63]
	v_mfma_f32_16x16x32_bf16 v[52:55], v[136:139], v[214:217], v[52:55]
	v_mfma_f32_16x16x32_bf16 v[44:47], v[144:147], v[214:217], v[44:47]
	v_mfma_f32_16x16x32_bf16 v[36:39], v[136:139], v[222:225], v[36:39]
	v_mfma_f32_16x16x32_bf16 v[28:31], v[144:147], v[222:225], v[28:31]
	v_mfma_f32_16x16x32_bf16 v[20:23], v[136:139], v[230:233], v[20:23]
	v_mfma_f32_16x16x32_bf16 v[12:15], v[144:147], v[230:233], v[12:15]
	v_mfma_f32_16x16x32_bf16 v[64:67], v[140:143], v[194:197], v[64:67]
	v_mfma_f32_16x16x32_bf16 v[60:63], v[148:151], v[194:197], v[60:63]
	v_mfma_f32_16x16x32_bf16 v[52:55], v[140:143], v[218:221], v[52:55]
	v_mfma_f32_16x16x32_bf16 v[44:47], v[148:151], v[218:221], v[44:47]
	v_mfma_f32_16x16x32_bf16 v[36:39], v[140:143], v[226:229], v[36:39]
	v_mfma_f32_16x16x32_bf16 v[28:31], v[148:151], v[226:229], v[28:31]
	v_mfma_f32_16x16x32_bf16 v[20:23], v[140:143], v[234:237], v[20:23]
	v_mfma_f32_16x16x32_bf16 v[12:15], v[148:151], v[234:237], v[12:15]
	v_mfma_f32_16x16x32_bf16 v[56:59], v[152:155], v[190:193], v[56:59]
	v_mfma_f32_16x16x32_bf16 v[48:51], v[160:163], v[190:193], v[48:51]
	v_mfma_f32_16x16x32_bf16 v[40:43], v[152:155], v[214:217], v[40:43]
	v_mfma_f32_16x16x32_bf16 v[32:35], v[160:163], v[214:217], v[32:35]
	v_mfma_f32_16x16x32_bf16 v[24:27], v[152:155], v[222:225], v[24:27]
	v_mfma_f32_16x16x32_bf16 v[16:19], v[160:163], v[222:225], v[16:19]
	v_mfma_f32_16x16x32_bf16 v[8:11], v[152:155], v[230:233], v[8:11]
	v_mfma_f32_16x16x32_bf16 v[4:7], v[160:163], v[230:233], v[4:7]
	v_mfma_f32_16x16x32_bf16 v[56:59], v[156:159], v[194:197], v[56:59]
	v_mfma_f32_16x16x32_bf16 v[48:51], v[186:189], v[194:197], v[48:51]
	v_mfma_f32_16x16x32_bf16 v[40:43], v[156:159], v[218:221], v[40:43]
	v_mfma_f32_16x16x32_bf16 v[32:35], v[186:189], v[218:221], v[32:35]
	v_mfma_f32_16x16x32_bf16 v[24:27], v[156:159], v[226:229], v[24:27]
	v_mfma_f32_16x16x32_bf16 v[16:19], v[186:189], v[226:229], v[16:19]
	v_mfma_f32_16x16x32_bf16 v[8:11], v[156:159], v[234:237], v[8:11]
	v_mfma_f32_16x16x32_bf16 v[4:7], v[186:189], v[234:237], v[4:7]
	s_barrier
	s_add_i32 s40, s40, 2
	s_cmp_gt_u32 s40, 29
	s_mov_b64 s[18:19], s[66:67]
	s_cbranch_scc0 .LBB0_120
	v_readlane_b32 s2, v252, 27
	v_readlane_b32 s3, v252, 28
	s_and_b64 vcc, exec, s[2:3]
	s_cbranch_vccz .LBB0_123
	s_barrier

.LBB0_346:
	ds_read_b128 v[148:151], v1
	ds_read_b128 v[152:155], v1 offset:1024
	ds_read_b128 v[156:159], v1 offset:2048
	ds_read_b128 v[160:163], v1 offset:3072
	ds_read_b128 v[172:175], v145
	ds_read_b128 v[176:179], v145 offset:1024
	ds_read_b128 v[180:183], v145 offset:2048
	ds_read_b128 v[184:187], v145 offset:3072
	s_add_u32 s34, s51, s28
	s_addc_u32 s35, s52, s29
	s_add_u32 s30, s28, 0x100
	s_addc_u32 s31, s29, 0
	s_cmp_eq_u32 s53, 28
	s_cselect_b64 s[36:37], -1, 0
	s_and_b64 s[2:3], s[36:37], exec
	s_cselect_b32 s35, s15, s35
	s_cselect_b32 s34, s17, s34
	s_cselect_b32 s54, 0, s30
	v_lshl_add_u64 v[220:221], v[140:141], 0, s[28:29]
	s_add_i32 m0, s21, 0xc000
	ds_read_b128 v[188:191], v146
	ds_read_b128 v[192:195], v146 offset:1024
	ds_read_b128 v[196:199], v146 offset:2048
	ds_read_b128 v[200:203], v146 offset:3072
	ds_read_b128 v[204:207], v146 offset:4096
	ds_read_b128 v[208:211], v146 offset:5120
	ds_read_b128 v[212:215], v146 offset:6144
	ds_read_b128 v[216:219], v146 offset:7168
	global_load_lds_dwordx4 v[220:221], off
	v_lshl_add_u64 v[220:221], v[142:143], 0, s[28:29]
	s_add_i32 m0, s21, 0xe000
	s_nop 0
	global_load_lds_dwordx4 v[220:221], off
	s_waitcnt vmcnt(8)
	s_waitcnt lgkmcnt(0)
	s_barrier
	s_waitcnt lgkmcnt(0)
	v_mfma_f32_16x16x32_bf16 v[126:129], v[188:191], v[148:151], v[126:129]
	v_mfma_f32_16x16x32_bf16 v[114:117], v[188:191], v[156:159], v[114:117]
	v_mfma_f32_16x16x32_bf16 v[122:125], v[196:199], v[148:151], v[122:125]
	v_mfma_f32_16x16x32_bf16 v[106:109], v[196:199], v[156:159], v[106:109]
	v_mfma_f32_16x16x32_bf16 v[118:121], v[204:207], v[148:151], v[118:121]
	v_mfma_f32_16x16x32_bf16 v[102:105], v[204:207], v[156:159], v[102:105]
	v_mfma_f32_16x16x32_bf16 v[110:113], v[212:215], v[148:151], v[110:113]
	v_mfma_f32_16x16x32_bf16 v[98:101], v[212:215], v[156:159], v[98:101]
	v_mfma_f32_16x16x32_bf16 v[126:129], v[192:195], v[152:155], v[126:129]
	v_mfma_f32_16x16x32_bf16 v[114:117], v[192:195], v[160:163], v[114:117]
	v_mfma_f32_16x16x32_bf16 v[122:125], v[200:203], v[152:155], v[122:125]
	v_mfma_f32_16x16x32_bf16 v[106:109], v[200:203], v[160:163], v[106:109]
	v_mfma_f32_16x16x32_bf16 v[118:121], v[208:211], v[152:155], v[118:121]
	v_mfma_f32_16x16x32_bf16 v[102:105], v[208:211], v[160:163], v[102:105]
	v_mfma_f32_16x16x32_bf16 v[110:113], v[216:219], v[152:155], v[110:113]
	v_mfma_f32_16x16x32_bf16 v[98:101], v[216:219], v[160:163], v[98:101]
	v_mfma_f32_16x16x32_bf16 v[94:97], v[188:191], v[172:175], v[94:97]
	v_mfma_f32_16x16x32_bf16 v[82:85], v[188:191], v[180:183], v[82:85]
	v_mfma_f32_16x16x32_bf16 v[90:93], v[196:199], v[172:175], v[90:93]
	v_mfma_f32_16x16x32_bf16 v[74:77], v[196:199], v[180:183], v[74:77]
	v_mfma_f32_16x16x32_bf16 v[86:89], v[204:207], v[172:175], v[86:89]
	v_mfma_f32_16x16x32_bf16 v[70:73], v[204:207], v[180:183], v[70:73]
	v_mfma_f32_16x16x32_bf16 v[78:81], v[212:215], v[172:175], v[78:81]
	v_mfma_f32_16x16x32_bf16 v[66:69], v[212:215], v[180:183], v[66:69]
	v_mfma_f32_16x16x32_bf16 v[94:97], v[192:195], v[176:179], v[94:97]
	v_mfma_f32_16x16x32_bf16 v[82:85], v[192:195], v[184:187], v[82:85]
	v_mfma_f32_16x16x32_bf16 v[90:93], v[200:203], v[176:179], v[90:93]
	v_mfma_f32_16x16x32_bf16 v[74:77], v[200:203], v[184:187], v[74:77]
	v_mfma_f32_16x16x32_bf16 v[86:89], v[208:211], v[176:179], v[86:89]
	v_mfma_f32_16x16x32_bf16 v[70:73], v[208:211], v[184:187], v[70:73]
	v_mfma_f32_16x16x32_bf16 v[78:81], v[216:219], v[176:179], v[78:81]
	v_mfma_f32_16x16x32_bf16 v[66:69], v[216:219], v[184:187], v[66:69]
	s_barrier
	s_add_i32 s2, s49, s20
	v_lshl_add_u64 v[220:221], s[34:35], 0, v[164:165]
	s_mov_b32 m0, s2
	ds_read_b128 v[188:191], v146 offset:16384
	ds_read_b128 v[192:195], v146 offset:17408
	ds_read_b128 v[196:199], v146 offset:18432
	ds_read_b128 v[200:203], v146 offset:19456
	ds_read_b128 v[204:207], v146 offset:20480
	ds_read_b128 v[208:211], v146 offset:21504
	ds_read_b128 v[212:215], v146 offset:22528
	ds_read_b128 v[216:219], v146 offset:23552
	global_load_lds_dwordx4 v[220:221], off
	s_add_i32 m0, s2, 0x2000
	s_add_u32 s2, s34, 0x80000
	v_lshl_add_u64 v[222:223], s[34:35], 0, v[168:169]
	s_addc_u32 s3, s35, 0
	s_add_i32 s28, s50, s20
	global_load_lds_dwordx4 v[222:223], off
	v_lshl_add_u64 v[224:225], s[2:3], 0, v[164:165]
	s_mov_b32 m0, s28
	s_nop 0
	global_load_lds_dwordx4 v[224:225], off
	v_lshl_add_u64 v[224:225], s[2:3], 0, v[168:169]
	s_add_i32 m0, s28, 0x2000
	s_and_b64 s[2:3], s[6:7], s[36:37]
	s_and_b64 s[2:3], s[2:3], exec
	s_cselect_b32 s2, s18, s26
	s_cselect_b32 s3, s19, s27
	s_add_u32 s2, s2, s54
	s_addc_u32 s3, s3, 0
	global_load_lds_dwordx4 v[224:225], off
	v_lshl_add_u64 v[224:225], s[2:3], 0, v[166:167]
	s_mov_b32 m0, s21
	v_lshl_add_u64 v[226:227], s[2:3], 0, v[170:171]
	global_load_lds_dwordx4 v[224:225], off
	s_mov_b32 m0, s33
	s_nop 0
	global_load_lds_dwordx4 v[226:227], off
	s_waitcnt vmcnt(8)
	s_waitcnt lgkmcnt(0)
	s_barrier
	s_waitcnt lgkmcnt(0)
	v_mfma_f32_16x16x32_bf16 v[62:65], v[188:191], v[148:151], v[62:65]
	v_mfma_f32_16x16x32_bf16 v[50:53], v[188:191], v[156:159], v[50:53]
	v_mfma_f32_16x16x32_bf16 v[58:61], v[196:199], v[148:151], v[58:61]
	v_mfma_f32_16x16x32_bf16 v[42:45], v[196:199], v[156:159], v[42:45]
	v_mfma_f32_16x16x32_bf16 v[54:57], v[204:207], v[148:151], v[54:57]
	v_mfma_f32_16x16x32_bf16 v[38:41], v[204:207], v[156:159], v[38:41]
	v_mfma_f32_16x16x32_bf16 v[46:49], v[212:215], v[148:151], v[46:49]
	v_mfma_f32_16x16x32_bf16 v[34:37], v[212:215], v[156:159], v[34:37]
	v_mfma_f32_16x16x32_bf16 v[62:65], v[192:195], v[152:155], v[62:65]
	v_mfma_f32_16x16x32_bf16 v[50:53], v[192:195], v[160:163], v[50:53]
	v_mfma_f32_16x16x32_bf16 v[58:61], v[200:203], v[152:155], v[58:61]
	v_mfma_f32_16x16x32_bf16 v[42:45], v[200:203], v[160:163], v[42:45]
	v_mfma_f32_16x16x32_bf16 v[54:57], v[208:211], v[152:155], v[54:57]
	v_mfma_f32_16x16x32_bf16 v[38:41], v[208:211], v[160:163], v[38:41]
	v_mfma_f32_16x16x32_bf16 v[46:49], v[216:219], v[152:155], v[46:49]
	v_mfma_f32_16x16x32_bf16 v[34:37], v[216:219], v[160:163], v[34:37]
	v_mfma_f32_16x16x32_bf16 v[30:33], v[188:191], v[172:175], v[30:33]
	v_mfma_f32_16x16x32_bf16 v[18:21], v[188:191], v[180:183], v[18:21]
	v_mfma_f32_16x16x32_bf16 v[26:29], v[196:199], v[172:175], v[26:29]
	v_mfma_f32_16x16x32_bf16 v[10:13], v[196:199], v[180:183], v[10:13]
	v_mfma_f32_16x16x32_bf16 v[22:25], v[204:207], v[172:175], v[22:25]
	v_mfma_f32_16x16x32_bf16 v[6:9], v[204:207], v[180:183], v[6:9]
	v_mfma_f32_16x16x32_bf16 v[14:17], v[212:215], v[172:175], v[14:17]
	v_mfma_f32_16x16x32_bf16 v[2:5], v[212:215], v[180:183], v[2:5]
	v_mfma_f32_16x16x32_bf16 v[30:33], v[192:195], v[176:179], v[30:33]
	v_mfma_f32_16x16x32_bf16 v[18:21], v[192:195], v[184:187], v[18:21]
	v_mfma_f32_16x16x32_bf16 v[26:29], v[200:203], v[176:179], v[26:29]
	v_mfma_f32_16x16x32_bf16 v[10:13], v[200:203], v[184:187], v[10:13]
	v_mfma_f32_16x16x32_bf16 v[22:25], v[208:211], v[176:179], v[22:25]
	v_mfma_f32_16x16x32_bf16 v[6:9], v[208:211], v[184:187], v[6:9]
	v_mfma_f32_16x16x32_bf16 v[14:17], v[216:219], v[176:179], v[14:17]
	v_mfma_f32_16x16x32_bf16 v[2:5], v[216:219], v[184:187], v[2:5]
	s_barrier
	s_add_i32 s28, 0, 0x18000
	v_add_u32_e32 v147, s28, v144
	s_add_i32 s29, 0, 0x1c000
	ds_read_b128 v[148:151], v147
	ds_read_b128 v[152:155], v147 offset:1024
	ds_read_b128 v[156:159], v147 offset:2048
	ds_read_b128 v[160:163], v147 offset:3072
	v_add_u32_e32 v147, s29, v144
	ds_read_b128 v[172:175], v147
	ds_read_b128 v[176:179], v147 offset:1024
	ds_read_b128 v[180:183], v147 offset:2048
	ds_read_b128 v[184:187], v147 offset:3072
	s_add_u32 s2, s2, 0x80000
	s_addc_u32 s3, s3, 0
	s_mov_b32 m0, s38
	v_lshl_add_u64 v[228:229], s[2:3], 0, v[166:167]
	ds_read_b128 v[188:191], v146 offset:32768
	ds_read_b128 v[192:195], v146 offset:33792
	ds_read_b128 v[196:199], v146 offset:34816
	ds_read_b128 v[200:203], v146 offset:35840
	ds_read_b128 v[204:207], v146 offset:36864
	ds_read_b128 v[208:211], v146 offset:37888
	ds_read_b128 v[212:215], v146 offset:38912
	ds_read_b128 v[216:219], v146 offset:39936
	global_load_lds_dwordx4 v[228:229], off
	v_lshl_add_u64 v[228:229], s[2:3], 0, v[170:171]
	s_mov_b32 m0, s39
	s_nop 0
	global_load_lds_dwordx4 v[228:229], off
	s_waitcnt vmcnt(8)
	s_waitcnt lgkmcnt(0)
	s_barrier
	s_waitcnt lgkmcnt(0)
	v_mfma_f32_16x16x32_bf16 v[126:129], v[188:191], v[148:151], v[126:129]
	v_mfma_f32_16x16x32_bf16 v[114:117], v[188:191], v[156:159], v[114:117]
	v_mfma_f32_16x16x32_bf16 v[122:125], v[196:199], v[148:151], v[122:125]
	v_mfma_f32_16x16x32_bf16 v[106:109], v[196:199], v[156:159], v[106:109]
	v_mfma_f32_16x16x32_bf16 v[118:121], v[204:207], v[148:151], v[118:121]
	v_mfma_f32_16x16x32_bf16 v[102:105], v[204:207], v[156:159], v[102:105]
	v_mfma_f32_16x16x32_bf16 v[110:113], v[212:215], v[148:151], v[110:113]
	v_mfma_f32_16x16x32_bf16 v[98:101], v[212:215], v[156:159], v[98:101]
	v_mfma_f32_16x16x32_bf16 v[126:129], v[192:195], v[152:155], v[126:129]
	v_mfma_f32_16x16x32_bf16 v[114:117], v[192:195], v[160:163], v[114:117]
	v_mfma_f32_16x16x32_bf16 v[122:125], v[200:203], v[152:155], v[122:125]
	v_mfma_f32_16x16x32_bf16 v[106:109], v[200:203], v[160:163], v[106:109]
	v_mfma_f32_16x16x32_bf16 v[118:121], v[208:211], v[152:155], v[118:121]
	v_mfma_f32_16x16x32_bf16 v[102:105], v[208:211], v[160:163], v[102:105]
	v_mfma_f32_16x16x32_bf16 v[110:113], v[216:219], v[152:155], v[110:113]
	v_mfma_f32_16x16x32_bf16 v[98:101], v[216:219], v[160:163], v[98:101]
	v_mfma_f32_16x16x32_bf16 v[94:97], v[188:191], v[172:175], v[94:97]
	v_mfma_f32_16x16x32_bf16 v[82:85], v[188:191], v[180:183], v[82:85]
	v_mfma_f32_16x16x32_bf16 v[90:93], v[196:199], v[172:175], v[90:93]
	v_mfma_f32_16x16x32_bf16 v[74:77], v[196:199], v[180:183], v[74:77]
	v_mfma_f32_16x16x32_bf16 v[86:89], v[204:207], v[172:175], v[86:89]
	v_mfma_f32_16x16x32_bf16 v[70:73], v[204:207], v[180:183], v[70:73]
	v_mfma_f32_16x16x32_bf16 v[78:81], v[212:215], v[172:175], v[78:81]
	v_mfma_f32_16x16x32_bf16 v[66:69], v[212:215], v[180:183], v[66:69]
	v_mfma_f32_16x16x32_bf16 v[94:97], v[192:195], v[176:179], v[94:97]
	v_mfma_f32_16x16x32_bf16 v[82:85], v[192:195], v[184:187], v[82:85]
	v_mfma_f32_16x16x32_bf16 v[90:93], v[200:203], v[176:179], v[90:93]
	v_mfma_f32_16x16x32_bf16 v[74:77], v[200:203], v[184:187], v[74:77]
	v_mfma_f32_16x16x32_bf16 v[86:89], v[208:211], v[176:179], v[86:89]
	v_mfma_f32_16x16x32_bf16 v[70:73], v[208:211], v[184:187], v[70:73]
	v_mfma_f32_16x16x32_bf16 v[78:81], v[216:219], v[176:179], v[78:81]
	v_mfma_f32_16x16x32_bf16 v[66:69], v[216:219], v[184:187], v[66:69]
	s_barrier
	s_add_i32 s2, s28, s20
	v_lshl_add_u64 v[220:221], v[220:221], 0, s[10:11]
	s_mov_b32 m0, s2
	ds_read_b128 v[188:191], v146 offset:49152
	ds_read_b128 v[192:195], v146 offset:50176
	ds_read_b128 v[196:199], v146 offset:51200
	ds_read_b128 v[200:203], v146 offset:52224
	ds_read_b128 v[204:207], v146 offset:53248
	ds_read_b128 v[208:211], v146 offset:54272
	ds_read_b128 v[212:215], v146 offset:55296
	ds_read_b128 v[216:219], v146 offset:56320
	global_load_lds_dwordx4 v[220:221], off
	s_add_i32 m0, s2, 0x2000
	s_add_u32 s2, s34, 0x80080
	v_lshl_add_u64 v[220:221], v[222:223], 0, s[10:11]
	s_addc_u32 s3, s35, 0
	s_add_i32 s28, s29, s20
	global_load_lds_dwordx4 v[220:221], off
	v_lshl_add_u64 v[220:221], s[2:3], 0, v[164:165]
	s_mov_b32 m0, s28
	s_nop 0
	global_load_lds_dwordx4 v[220:221], off
	v_lshl_add_u64 v[220:221], s[2:3], 0, v[168:169]
	s_add_i32 m0, s28, 0x2000
	s_nop 0
	global_load_lds_dwordx4 v[220:221], off
	v_lshl_add_u64 v[220:221], v[224:225], 0, s[10:11]
	s_mov_b32 m0, s43
	s_nop 0
	global_load_lds_dwordx4 v[220:221], off
	v_lshl_add_u64 v[220:221], v[226:227], 0, s[10:11]
	s_mov_b32 m0, s48
	s_nop 0
	global_load_lds_dwordx4 v[220:221], off
	s_waitcnt vmcnt(8)
	s_waitcnt lgkmcnt(0)
	s_barrier
	s_waitcnt lgkmcnt(0)
	v_mfma_f32_16x16x32_bf16 v[62:65], v[188:191], v[148:151], v[62:65]
	v_mfma_f32_16x16x32_bf16 v[50:53], v[188:191], v[156:159], v[50:53]
	v_mfma_f32_16x16x32_bf16 v[58:61], v[196:199], v[148:151], v[58:61]
	v_mfma_f32_16x16x32_bf16 v[42:45], v[196:199], v[156:159], v[42:45]
	v_mfma_f32_16x16x32_bf16 v[54:57], v[204:207], v[148:151], v[54:57]
	v_mfma_f32_16x16x32_bf16 v[38:41], v[204:207], v[156:159], v[38:41]
	v_mfma_f32_16x16x32_bf16 v[46:49], v[212:215], v[148:151], v[46:49]
	v_mfma_f32_16x16x32_bf16 v[34:37], v[212:215], v[156:159], v[34:37]
	v_mfma_f32_16x16x32_bf16 v[62:65], v[192:195], v[152:155], v[62:65]
	v_mfma_f32_16x16x32_bf16 v[50:53], v[192:195], v[160:163], v[50:53]
	v_mfma_f32_16x16x32_bf16 v[58:61], v[200:203], v[152:155], v[58:61]
	v_mfma_f32_16x16x32_bf16 v[42:45], v[200:203], v[160:163], v[42:45]
	v_mfma_f32_16x16x32_bf16 v[54:57], v[208:211], v[152:155], v[54:57]
	v_mfma_f32_16x16x32_bf16 v[38:41], v[208:211], v[160:163], v[38:41]
	v_mfma_f32_16x16x32_bf16 v[46:49], v[216:219], v[152:155], v[46:49]
	v_mfma_f32_16x16x32_bf16 v[34:37], v[216:219], v[160:163], v[34:37]
	v_mfma_f32_16x16x32_bf16 v[30:33], v[188:191], v[172:175], v[30:33]
	v_mfma_f32_16x16x32_bf16 v[18:21], v[188:191], v[180:183], v[18:21]
	v_mfma_f32_16x16x32_bf16 v[26:29], v[196:199], v[172:175], v[26:29]
	v_mfma_f32_16x16x32_bf16 v[10:13], v[196:199], v[180:183], v[10:13]
	v_mfma_f32_16x16x32_bf16 v[22:25], v[204:207], v[172:175], v[22:25]
	v_mfma_f32_16x16x32_bf16 v[6:9], v[204:207], v[180:183], v[6:9]
	v_mfma_f32_16x16x32_bf16 v[14:17], v[212:215], v[172:175], v[14:17]
	v_mfma_f32_16x16x32_bf16 v[2:5], v[212:215], v[180:183], v[2:5]
	v_mfma_f32_16x16x32_bf16 v[30:33], v[192:195], v[176:179], v[30:33]
	v_mfma_f32_16x16x32_bf16 v[18:21], v[192:195], v[184:187], v[18:21]
	v_mfma_f32_16x16x32_bf16 v[26:29], v[200:203], v[176:179], v[26:29]
	v_mfma_f32_16x16x32_bf16 v[10:13], v[200:203], v[184:187], v[10:13]
	v_mfma_f32_16x16x32_bf16 v[22:25], v[208:211], v[176:179], v[22:25]
	v_mfma_f32_16x16x32_bf16 v[6:9], v[208:211], v[184:187], v[6:9]
	v_mfma_f32_16x16x32_bf16 v[14:17], v[216:219], v[176:179], v[14:17]
	v_mfma_f32_16x16x32_bf16 v[2:5], v[216:219], v[184:187], v[2:5]
	s_barrier
	s_add_i32 s53, s53, 2
	s_cmp_gt_u32 s53, 29
	s_mov_b64 s[28:29], s[30:31]
	s_cbranch_scc0 .LBB0_346
	s_and_b64 vcc, exec, s[12:13]
	s_cbranch_vccz .LBB0_349
	s_barrier

.LBB0_712:
	ds_read_b128 v[140:143], v205
	ds_read_b128 v[144:147], v205 offset:1024
	ds_read_b128 v[148:151], v205 offset:2048
	ds_read_b128 v[152:155], v205 offset:3072
	ds_read_b128 v[182:185], v207
	ds_read_b128 v[186:189], v207 offset:1024
	ds_read_b128 v[196:199], v207 offset:2048
	ds_read_b128 v[212:215], v207 offset:3072
	s_mov_b64 s[72:73], s[56:57]
	s_add_u32 s2, s69, s72
	s_addc_u32 s74, s70, s73
	s_add_u32 s56, s72, 0x100
	s_addc_u32 s57, s73, 0
	s_cmpk_eq_i32 s72, 0xf00
	s_cselect_b64 s[58:59], -1, 0
	s_and_b64 s[60:61], s[58:59], exec
	s_cselect_b32 s61, s35, s74
	s_cselect_b32 s60, s68, s2
	s_cselect_b32 s2, 0, s56
	v_lshl_add_u64 v[4:5], v[136:137], 0, s[72:73]
	s_add_i32 m0, s42, 0xc000
	ds_read_b128 v[216:219], v210
	ds_read_b128 v[220:223], v210 offset:1024
	ds_read_b128 v[224:227], v210 offset:2048
	ds_read_b128 v[228:231], v210 offset:3072
	ds_read_b128 v[232:235], v210 offset:4096
	ds_read_b128 v[236:239], v210 offset:5120
	ds_read_b128 v[244:247], v210 offset:6144
	ds_read_b128 v[248:251], v210 offset:7168
	global_load_lds_dwordx4 v[4:5], off
	v_lshl_add_u64 v[4:5], v[134:135], 0, s[72:73]
	s_add_i32 m0, s42, 0xe000
	s_nop 0
	global_load_lds_dwordx4 v[4:5], off
	s_waitcnt vmcnt(8)
	s_waitcnt lgkmcnt(0)
	s_barrier
	s_waitcnt lgkmcnt(0)
	v_mfma_f32_16x16x32_bf16 v[130:133], v[140:143], v[216:219], v[130:133]
	v_mfma_f32_16x16x32_bf16 v[126:129], v[148:151], v[216:219], v[126:129]
	v_mfma_f32_16x16x32_bf16 v[114:117], v[140:143], v[224:227], v[114:117]
	v_mfma_f32_16x16x32_bf16 v[110:113], v[148:151], v[224:227], v[110:113]
	v_mfma_f32_16x16x32_bf16 v[98:101], v[140:143], v[232:235], v[98:101]
	v_mfma_f32_16x16x32_bf16 v[94:97], v[148:151], v[232:235], v[94:97]
	v_mfma_f32_16x16x32_bf16 v[82:85], v[140:143], v[244:247], v[82:85]
	v_mfma_f32_16x16x32_bf16 v[78:81], v[148:151], v[244:247], v[78:81]
	v_mfma_f32_16x16x32_bf16 v[130:133], v[144:147], v[220:223], v[130:133]
	v_mfma_f32_16x16x32_bf16 v[126:129], v[152:155], v[220:223], v[126:129]
	v_mfma_f32_16x16x32_bf16 v[114:117], v[144:147], v[228:231], v[114:117]
	v_mfma_f32_16x16x32_bf16 v[110:113], v[152:155], v[228:231], v[110:113]
	v_mfma_f32_16x16x32_bf16 v[98:101], v[144:147], v[236:239], v[98:101]
	v_mfma_f32_16x16x32_bf16 v[94:97], v[152:155], v[236:239], v[94:97]
	v_mfma_f32_16x16x32_bf16 v[82:85], v[144:147], v[248:251], v[82:85]
	v_mfma_f32_16x16x32_bf16 v[78:81], v[152:155], v[248:251], v[78:81]
	v_mfma_f32_16x16x32_bf16 v[122:125], v[182:185], v[216:219], v[122:125]
	v_mfma_f32_16x16x32_bf16 v[118:121], v[196:199], v[216:219], v[118:121]
	v_mfma_f32_16x16x32_bf16 v[106:109], v[182:185], v[224:227], v[106:109]
	v_mfma_f32_16x16x32_bf16 v[102:105], v[196:199], v[224:227], v[102:105]
	v_mfma_f32_16x16x32_bf16 v[90:93], v[182:185], v[232:235], v[90:93]
	v_mfma_f32_16x16x32_bf16 v[86:89], v[196:199], v[232:235], v[86:89]
	v_mfma_f32_16x16x32_bf16 v[74:77], v[182:185], v[244:247], v[74:77]
	v_mfma_f32_16x16x32_bf16 v[70:73], v[196:199], v[244:247], v[70:73]
	v_mfma_f32_16x16x32_bf16 v[122:125], v[186:189], v[220:223], v[122:125]
	v_mfma_f32_16x16x32_bf16 v[118:121], v[212:215], v[220:223], v[118:121]
	v_mfma_f32_16x16x32_bf16 v[106:109], v[186:189], v[228:231], v[106:109]
	v_mfma_f32_16x16x32_bf16 v[102:105], v[212:215], v[228:231], v[102:105]
	v_mfma_f32_16x16x32_bf16 v[90:93], v[186:189], v[236:239], v[90:93]
	v_mfma_f32_16x16x32_bf16 v[86:89], v[212:215], v[236:239], v[86:89]
	v_mfma_f32_16x16x32_bf16 v[74:77], v[186:189], v[248:251], v[74:77]
	v_mfma_f32_16x16x32_bf16 v[70:73], v[212:215], v[248:251], v[70:73]
	s_barrier
	s_add_i32 s72, s63, s15
	v_lshl_add_u64 v[156:157], s[60:61], 0, v[160:161]
	s_mov_b32 m0, s72
	ds_read_b128 v[216:219], v210 offset:16384
	ds_read_b128 v[220:223], v210 offset:17408
	ds_read_b128 v[224:227], v210 offset:18432
	ds_read_b128 v[228:231], v210 offset:19456
	ds_read_b128 v[232:235], v210 offset:20480
	ds_read_b128 v[236:239], v210 offset:21504
	ds_read_b128 v[244:247], v210 offset:22528
	ds_read_b128 v[248:251], v210 offset:23552
	global_load_lds_dwordx4 v[156:157], off
	s_add_i32 m0, s72, 0x2000
	s_add_u32 s72, s60, 0x80000
	v_lshl_add_u64 v[178:179], s[60:61], 0, v[164:165]
	s_addc_u32 s73, s61, 0
	s_add_i32 s74, s64, s15
	global_load_lds_dwordx4 v[178:179], off
	v_lshl_add_u64 v[4:5], s[72:73], 0, v[160:161]
	s_mov_b32 m0, s74
	s_nop 0
	global_load_lds_dwordx4 v[4:5], off
	v_lshl_add_u64 v[4:5], s[72:73], 0, v[164:165]
	s_add_i32 m0, s74, 0x2000
	s_and_b64 s[72:73], s[10:11], s[58:59]
	s_and_b64 s[72:73], s[72:73], exec
	s_cselect_b32 s72, s38, s54
	s_cselect_b32 s73, s39, s55
	s_add_u32 s72, s72, s2
	s_addc_u32 s73, s73, 0
	global_load_lds_dwordx4 v[4:5], off
	v_lshl_add_u64 v[192:193], s[72:73], 0, v[158:159]
	s_mov_b32 m0, s42
	v_lshl_add_u64 v[202:203], s[72:73], 0, v[162:163]
	global_load_lds_dwordx4 v[192:193], off
	s_mov_b32 m0, s43
	s_nop 0
	global_load_lds_dwordx4 v[202:203], off
	s_waitcnt vmcnt(8)
	s_waitcnt lgkmcnt(0)
	s_barrier
	s_waitcnt lgkmcnt(0)
	v_mfma_f32_16x16x32_bf16 v[66:69], v[140:143], v[216:219], v[66:69]
	v_mfma_f32_16x16x32_bf16 v[62:65], v[148:151], v[216:219], v[62:65]
	v_mfma_f32_16x16x32_bf16 v[50:53], v[140:143], v[224:227], v[50:53]
	v_mfma_f32_16x16x32_bf16 v[46:49], v[148:151], v[224:227], v[46:49]
	v_mfma_f32_16x16x32_bf16 v[34:37], v[140:143], v[232:235], v[34:37]
	v_mfma_f32_16x16x32_bf16 v[30:33], v[148:151], v[232:235], v[30:33]
	v_mfma_f32_16x16x32_bf16 v[18:21], v[140:143], v[244:247], v[18:21]
	v_mfma_f32_16x16x32_bf16 v[14:17], v[148:151], v[244:247], v[14:17]
	v_mfma_f32_16x16x32_bf16 v[66:69], v[144:147], v[220:223], v[66:69]
	v_mfma_f32_16x16x32_bf16 v[62:65], v[152:155], v[220:223], v[62:65]
	v_mfma_f32_16x16x32_bf16 v[50:53], v[144:147], v[228:231], v[50:53]
	v_mfma_f32_16x16x32_bf16 v[46:49], v[152:155], v[228:231], v[46:49]
	v_mfma_f32_16x16x32_bf16 v[34:37], v[144:147], v[236:239], v[34:37]
	v_mfma_f32_16x16x32_bf16 v[30:33], v[152:155], v[236:239], v[30:33]
	v_mfma_f32_16x16x32_bf16 v[18:21], v[144:147], v[248:251], v[18:21]
	v_mfma_f32_16x16x32_bf16 v[14:17], v[152:155], v[248:251], v[14:17]
	v_mfma_f32_16x16x32_bf16 v[58:61], v[182:185], v[216:219], v[58:61]
	v_mfma_f32_16x16x32_bf16 v[54:57], v[196:199], v[216:219], v[54:57]
	v_mfma_f32_16x16x32_bf16 v[42:45], v[182:185], v[224:227], v[42:45]
	v_mfma_f32_16x16x32_bf16 v[38:41], v[196:199], v[224:227], v[38:41]
	v_mfma_f32_16x16x32_bf16 v[26:29], v[182:185], v[232:235], v[26:29]
	v_mfma_f32_16x16x32_bf16 v[22:25], v[196:199], v[232:235], v[22:25]
	v_mfma_f32_16x16x32_bf16 v[10:13], v[182:185], v[244:247], v[10:13]
	v_mfma_f32_16x16x32_bf16 v[4:7], v[196:199], v[244:247], v[6:9]
	v_mfma_f32_16x16x32_bf16 v[58:61], v[186:189], v[220:223], v[58:61]
	v_mfma_f32_16x16x32_bf16 v[54:57], v[212:215], v[220:223], v[54:57]
	v_mfma_f32_16x16x32_bf16 v[42:45], v[186:189], v[228:231], v[42:45]
	v_mfma_f32_16x16x32_bf16 v[38:41], v[212:215], v[228:231], v[38:41]
	v_mfma_f32_16x16x32_bf16 v[26:29], v[186:189], v[236:239], v[26:29]
	v_mfma_f32_16x16x32_bf16 v[22:25], v[212:215], v[236:239], v[22:25]
	v_mfma_f32_16x16x32_bf16 v[10:13], v[186:189], v[248:251], v[10:13]
	v_mfma_f32_16x16x32_bf16 v[4:7], v[212:215], v[248:251], v[4:7]
	s_barrier
	s_add_i32 s2, 0, 0x18000
	v_add_u32_e32 v3, s2, v177
	s_add_i32 s74, 0, 0x1c000
	ds_read_b128 v[140:143], v3
	ds_read_b128 v[144:147], v3 offset:1024
	ds_read_b128 v[148:151], v3 offset:2048
	ds_read_b128 v[152:155], v3 offset:3072
	v_add_u32_e32 v3, s74, v177
	ds_read_b128 v[182:185], v3
	ds_read_b128 v[186:189], v3 offset:1024
	ds_read_b128 v[196:199], v3 offset:2048
	ds_read_b128 v[212:215], v3 offset:3072
	s_add_u32 s72, s72, 0x80000
	s_addc_u32 s73, s73, 0
	s_mov_b32 m0, s48
	v_lshl_add_u64 v[8:9], s[72:73], 0, v[158:159]
	ds_read_b128 v[216:219], v210 offset:32768
	ds_read_b128 v[220:223], v210 offset:33792
	ds_read_b128 v[224:227], v210 offset:34816
	ds_read_b128 v[228:231], v210 offset:35840
	ds_read_b128 v[232:235], v210 offset:36864
	ds_read_b128 v[236:239], v210 offset:37888
	ds_read_b128 v[244:247], v210 offset:38912
	ds_read_b128 v[248:251], v210 offset:39936
	global_load_lds_dwordx4 v[8:9], off
	v_lshl_add_u64 v[8:9], s[72:73], 0, v[162:163]
	s_mov_b32 m0, s49
	s_nop 0
	global_load_lds_dwordx4 v[8:9], off
	s_waitcnt vmcnt(8)
	s_waitcnt lgkmcnt(0)
	s_barrier
	s_waitcnt lgkmcnt(0)
	v_mfma_f32_16x16x32_bf16 v[130:133], v[140:143], v[216:219], v[130:133]
	v_mfma_f32_16x16x32_bf16 v[126:129], v[148:151], v[216:219], v[126:129]
	v_mfma_f32_16x16x32_bf16 v[114:117], v[140:143], v[224:227], v[114:117]
	v_mfma_f32_16x16x32_bf16 v[110:113], v[148:151], v[224:227], v[110:113]
	v_mfma_f32_16x16x32_bf16 v[98:101], v[140:143], v[232:235], v[98:101]
	v_mfma_f32_16x16x32_bf16 v[94:97], v[148:151], v[232:235], v[94:97]
	v_mfma_f32_16x16x32_bf16 v[82:85], v[140:143], v[244:247], v[82:85]
	v_mfma_f32_16x16x32_bf16 v[78:81], v[148:151], v[244:247], v[78:81]
	v_mfma_f32_16x16x32_bf16 v[130:133], v[144:147], v[220:223], v[130:133]
	v_mfma_f32_16x16x32_bf16 v[126:129], v[152:155], v[220:223], v[126:129]
	v_mfma_f32_16x16x32_bf16 v[114:117], v[144:147], v[228:231], v[114:117]
	v_mfma_f32_16x16x32_bf16 v[110:113], v[152:155], v[228:231], v[110:113]
	v_mfma_f32_16x16x32_bf16 v[98:101], v[144:147], v[236:239], v[98:101]
	v_mfma_f32_16x16x32_bf16 v[94:97], v[152:155], v[236:239], v[94:97]
	v_mfma_f32_16x16x32_bf16 v[82:85], v[144:147], v[248:251], v[82:85]
	v_mfma_f32_16x16x32_bf16 v[78:81], v[152:155], v[248:251], v[78:81]
	v_mfma_f32_16x16x32_bf16 v[122:125], v[182:185], v[216:219], v[122:125]
	v_mfma_f32_16x16x32_bf16 v[118:121], v[196:199], v[216:219], v[118:121]
	v_mfma_f32_16x16x32_bf16 v[106:109], v[182:185], v[224:227], v[106:109]
	v_mfma_f32_16x16x32_bf16 v[102:105], v[196:199], v[224:227], v[102:105]
	v_mfma_f32_16x16x32_bf16 v[90:93], v[182:185], v[232:235], v[90:93]
	v_mfma_f32_16x16x32_bf16 v[86:89], v[196:199], v[232:235], v[86:89]
	v_mfma_f32_16x16x32_bf16 v[74:77], v[182:185], v[244:247], v[74:77]
	v_mfma_f32_16x16x32_bf16 v[70:73], v[196:199], v[244:247], v[70:73]
	v_mfma_f32_16x16x32_bf16 v[122:125], v[186:189], v[220:223], v[122:125]
	v_mfma_f32_16x16x32_bf16 v[118:121], v[212:215], v[220:223], v[118:121]
	v_mfma_f32_16x16x32_bf16 v[106:109], v[186:189], v[228:231], v[106:109]
	v_mfma_f32_16x16x32_bf16 v[102:105], v[212:215], v[228:231], v[102:105]
	v_mfma_f32_16x16x32_bf16 v[90:93], v[186:189], v[236:239], v[90:93]
	v_mfma_f32_16x16x32_bf16 v[86:89], v[212:215], v[236:239], v[86:89]
	v_mfma_f32_16x16x32_bf16 v[74:77], v[186:189], v[248:251], v[74:77]
	v_mfma_f32_16x16x32_bf16 v[70:73], v[212:215], v[248:251], v[70:73]
	s_barrier
	s_add_i32 s2, s2, s15
	v_lshl_add_u64 v[8:9], v[156:157], 0, s[28:29]
	s_mov_b32 m0, s2
	ds_read_b128 v[216:219], v210 offset:49152
	ds_read_b128 v[220:223], v210 offset:50176
	ds_read_b128 v[224:227], v210 offset:51200
	ds_read_b128 v[228:231], v210 offset:52224
	ds_read_b128 v[232:235], v210 offset:53248
	ds_read_b128 v[236:239], v210 offset:54272
	ds_read_b128 v[244:247], v210 offset:55296
	ds_read_b128 v[248:251], v210 offset:56320
	global_load_lds_dwordx4 v[8:9], off
	s_add_i32 m0, s2, 0x2000
	s_add_u32 s60, s60, 0x80080
	v_lshl_add_u64 v[8:9], v[178:179], 0, s[28:29]
	s_addc_u32 s61, s61, 0
	s_add_i32 s2, s74, s15
	global_load_lds_dwordx4 v[8:9], off
	v_lshl_add_u64 v[8:9], s[60:61], 0, v[160:161]
	s_mov_b32 m0, s2
	s_nop 0
	global_load_lds_dwordx4 v[8:9], off
	v_lshl_add_u64 v[8:9], s[60:61], 0, v[164:165]
	s_add_i32 m0, s2, 0x2000
	s_nop 0
	global_load_lds_dwordx4 v[8:9], off
	v_lshl_add_u64 v[8:9], v[192:193], 0, s[28:29]
	s_mov_b32 m0, s51
	s_nop 0
	global_load_lds_dwordx4 v[8:9], off
	v_lshl_add_u64 v[8:9], v[202:203], 0, s[28:29]
	s_mov_b32 m0, s52
	s_nop 0
	global_load_lds_dwordx4 v[8:9], off
	s_waitcnt vmcnt(8)
	s_waitcnt lgkmcnt(0)
	s_barrier
	s_waitcnt lgkmcnt(0)
	v_mfma_f32_16x16x32_bf16 v[66:69], v[140:143], v[216:219], v[66:69]
	v_mfma_f32_16x16x32_bf16 v[62:65], v[148:151], v[216:219], v[62:65]
	v_mfma_f32_16x16x32_bf16 v[50:53], v[140:143], v[224:227], v[50:53]
	v_mfma_f32_16x16x32_bf16 v[46:49], v[148:151], v[224:227], v[46:49]
	v_mfma_f32_16x16x32_bf16 v[34:37], v[140:143], v[232:235], v[34:37]
	v_mfma_f32_16x16x32_bf16 v[30:33], v[148:151], v[232:235], v[30:33]
	v_mfma_f32_16x16x32_bf16 v[18:21], v[140:143], v[244:247], v[18:21]
	v_mfma_f32_16x16x32_bf16 v[14:17], v[148:151], v[244:247], v[14:17]
	v_mfma_f32_16x16x32_bf16 v[66:69], v[144:147], v[220:223], v[66:69]
	v_mfma_f32_16x16x32_bf16 v[62:65], v[152:155], v[220:223], v[62:65]
	v_mfma_f32_16x16x32_bf16 v[50:53], v[144:147], v[228:231], v[50:53]
	v_mfma_f32_16x16x32_bf16 v[46:49], v[152:155], v[228:231], v[46:49]
	v_mfma_f32_16x16x32_bf16 v[34:37], v[144:147], v[236:239], v[34:37]
	v_mfma_f32_16x16x32_bf16 v[30:33], v[152:155], v[236:239], v[30:33]
	v_mfma_f32_16x16x32_bf16 v[18:21], v[144:147], v[248:251], v[18:21]
	v_mfma_f32_16x16x32_bf16 v[14:17], v[152:155], v[248:251], v[14:17]
	v_mfma_f32_16x16x32_bf16 v[58:61], v[182:185], v[216:219], v[58:61]
	v_mfma_f32_16x16x32_bf16 v[54:57], v[196:199], v[216:219], v[54:57]
	v_mfma_f32_16x16x32_bf16 v[42:45], v[182:185], v[224:227], v[42:45]
	v_mfma_f32_16x16x32_bf16 v[38:41], v[196:199], v[224:227], v[38:41]
	v_mfma_f32_16x16x32_bf16 v[26:29], v[182:185], v[232:235], v[26:29]
	v_mfma_f32_16x16x32_bf16 v[22:25], v[196:199], v[232:235], v[22:25]
	v_mfma_f32_16x16x32_bf16 v[8:11], v[182:185], v[244:247], v[10:13]
	v_mfma_f32_16x16x32_bf16 v[4:7], v[196:199], v[244:247], v[4:7]
	v_mfma_f32_16x16x32_bf16 v[58:61], v[186:189], v[220:223], v[58:61]
	v_mfma_f32_16x16x32_bf16 v[54:57], v[212:215], v[220:223], v[54:57]
	v_mfma_f32_16x16x32_bf16 v[42:45], v[186:189], v[228:231], v[42:45]
	v_mfma_f32_16x16x32_bf16 v[38:41], v[212:215], v[228:231], v[38:41]
	v_mfma_f32_16x16x32_bf16 v[26:29], v[186:189], v[236:239], v[26:29]
	v_mfma_f32_16x16x32_bf16 v[22:25], v[212:215], v[236:239], v[22:25]
	v_mfma_f32_16x16x32_bf16 v[10:13], v[186:189], v[248:251], v[8:11]
	v_mfma_f32_16x16x32_bf16 v[6:9], v[212:215], v[248:251], v[4:7]
	s_barrier
	s_add_i32 s2, s71, 4
	s_and_b32 s2, s2, 6
	s_cmp_lg_u32 s2, 0
	s_cselect_b64 s[60:61], -1, 0
	s_or_b64 s[58:59], s[58:59], s[60:61]
	s_and_b64 vcc, exec, s[58:59]
	s_cbranch_vccnz .LBB0_711
	ds_read2st64_b32 v[4:5], v138 offset1:1
	ds_read2st64_b32 v[140:141], v138 offset0:2 offset1:3
	ds_read2st64_b32 v[142:143], v138 offset0:8 offset1:9
	ds_read2st64_b32 v[144:145], v138 offset0:10 offset1:11
	s_waitcnt lgkmcnt(0)
	v_pk_mul_f32 v[132:133], v[132:133], v[4:5] op_sel_hi:[1,0]
	v_pk_mul_f32 v[130:131], v[130:131], v[4:5] op_sel_hi:[1,0]
	v_pk_mul_f32 v[128:129], v[128:129], v[4:5] op_sel_hi:[1,0]
	v_pk_mul_f32 v[126:127], v[126:127], v[4:5] op_sel_hi:[1,0]
	v_pk_mul_f32 v[124:125], v[124:125], v[4:5] op_sel_hi:[1,0]
	v_pk_mul_f32 v[122:123], v[122:123], v[4:5] op_sel_hi:[1,0]
	v_pk_mul_f32 v[120:121], v[120:121], v[4:5] op_sel_hi:[1,0]
	v_pk_mul_f32 v[118:119], v[118:119], v[4:5] op_sel_hi:[1,0]
	v_mov_b32_e32 v4, v5
	v_pk_mul_f32 v[116:117], v[116:117], v[4:5] op_sel_hi:[1,0]
	v_pk_mul_f32 v[114:115], v[114:115], v[4:5] op_sel_hi:[1,0]
	v_pk_mul_f32 v[112:113], v[112:113], v[4:5] op_sel_hi:[1,0]
	v_pk_mul_f32 v[110:111], v[110:111], v[4:5] op_sel_hi:[1,0]
	v_pk_mul_f32 v[108:109], v[108:109], v[4:5] op_sel_hi:[1,0]
	v_pk_mul_f32 v[106:107], v[106:107], v[4:5] op_sel_hi:[1,0]
	v_pk_mul_f32 v[104:105], v[104:105], v[4:5] op_sel_hi:[1,0]
	v_pk_mul_f32 v[102:103], v[102:103], v[4:5] op_sel_hi:[1,0]
	v_mov_b32_e32 v4, v141
	v_pk_mul_f32 v[84:85], v[84:85], v[4:5] op_sel_hi:[1,0]
	v_pk_mul_f32 v[82:83], v[82:83], v[4:5] op_sel_hi:[1,0]
	v_pk_mul_f32 v[80:81], v[80:81], v[4:5] op_sel_hi:[1,0]
	v_pk_mul_f32 v[78:79], v[78:79], v[4:5] op_sel_hi:[1,0]
	v_pk_mul_f32 v[76:77], v[76:77], v[4:5] op_sel_hi:[1,0]
	v_pk_mul_f32 v[74:75], v[74:75], v[4:5] op_sel_hi:[1,0]
	v_pk_mul_f32 v[72:73], v[72:73], v[4:5] op_sel_hi:[1,0]
	v_pk_mul_f32 v[70:71], v[70:71], v[4:5] op_sel_hi:[1,0]
	v_mov_b32_e32 v4, v143
	v_pk_mul_f32 v[52:53], v[52:53], v[4:5] op_sel_hi:[1,0]
	v_pk_mul_f32 v[50:51], v[50:51], v[4:5] op_sel_hi:[1,0]
	v_pk_mul_f32 v[48:49], v[48:49], v[4:5] op_sel_hi:[1,0]
	v_pk_mul_f32 v[46:47], v[46:47], v[4:5] op_sel_hi:[1,0]
	v_pk_mul_f32 v[44:45], v[44:45], v[4:5] op_sel_hi:[1,0]
	v_pk_mul_f32 v[42:43], v[42:43], v[4:5] op_sel_hi:[1,0]
	v_pk_mul_f32 v[40:41], v[40:41], v[4:5] op_sel_hi:[1,0]
	v_pk_mul_f32 v[38:39], v[38:39], v[4:5] op_sel_hi:[1,0]
	v_mov_b32_e32 v4, v145
	v_pk_mul_f32 v[100:101], v[100:101], v[140:141] op_sel_hi:[1,0]
	v_pk_mul_f32 v[98:99], v[98:99], v[140:141] op_sel_hi:[1,0]
	v_pk_mul_f32 v[96:97], v[96:97], v[140:141] op_sel_hi:[1,0]
	v_pk_mul_f32 v[94:95], v[94:95], v[140:141] op_sel_hi:[1,0]
	v_pk_mul_f32 v[92:93], v[92:93], v[140:141] op_sel_hi:[1,0]
	v_pk_mul_f32 v[90:91], v[90:91], v[140:141] op_sel_hi:[1,0]
	v_pk_mul_f32 v[88:89], v[88:89], v[140:141] op_sel_hi:[1,0]
	v_pk_mul_f32 v[86:87], v[86:87], v[140:141] op_sel_hi:[1,0]
	v_pk_mul_f32 v[68:69], v[68:69], v[142:143] op_sel_hi:[1,0]
	v_pk_mul_f32 v[66:67], v[66:67], v[142:143] op_sel_hi:[1,0]
	v_pk_mul_f32 v[64:65], v[64:65], v[142:143] op_sel_hi:[1,0]
	v_pk_mul_f32 v[62:63], v[62:63], v[142:143] op_sel_hi:[1,0]
	v_pk_mul_f32 v[60:61], v[60:61], v[142:143] op_sel_hi:[1,0]
	v_pk_mul_f32 v[58:59], v[58:59], v[142:143] op_sel_hi:[1,0]
	v_pk_mul_f32 v[56:57], v[56:57], v[142:143] op_sel_hi:[1,0]
	v_pk_mul_f32 v[54:55], v[54:55], v[142:143] op_sel_hi:[1,0]
	v_pk_mul_f32 v[36:37], v[36:37], v[144:145] op_sel_hi:[1,0]
	v_pk_mul_f32 v[34:35], v[34:35], v[144:145] op_sel_hi:[1,0]
	v_pk_mul_f32 v[32:33], v[32:33], v[144:145] op_sel_hi:[1,0]
	v_pk_mul_f32 v[30:31], v[30:31], v[144:145] op_sel_hi:[1,0]
	v_pk_mul_f32 v[28:29], v[28:29], v[144:145] op_sel_hi:[1,0]
	v_pk_mul_f32 v[26:27], v[26:27], v[144:145] op_sel_hi:[1,0]
	v_pk_mul_f32 v[24:25], v[24:25], v[144:145] op_sel_hi:[1,0]
	v_pk_mul_f32 v[22:23], v[22:23], v[144:145] op_sel_hi:[1,0]
	v_pk_mul_f32 v[20:21], v[20:21], v[4:5] op_sel_hi:[1,0]
	v_pk_mul_f32 v[18:19], v[18:19], v[4:5] op_sel_hi:[1,0]
	v_pk_mul_f32 v[16:17], v[16:17], v[4:5] op_sel_hi:[1,0]
	v_pk_mul_f32 v[14:15], v[14:15], v[4:5] op_sel_hi:[1,0]
	v_pk_mul_f32 v[12:13], v[12:13], v[4:5] op_sel_hi:[1,0]
	v_pk_mul_f32 v[10:11], v[10:11], v[4:5] op_sel_hi:[1,0]
	v_pk_mul_f32 v[8:9], v[8:9], v[4:5] op_sel_hi:[1,0]
	v_pk_mul_f32 v[6:7], v[6:7], v[4:5] op_sel_hi:[1,0]
	s_branch .LBB0_711

.LBB0_810:
.LBB0_811:
	s_waitcnt lgkmcnt(0)
	v_mfma_f32_16x16x32_bf16 v[58:61], v[66:69], v[106:109], v[58:61]
	v_mfma_f32_16x16x32_bf16 v[50:53], v[74:77], v[106:109], v[50:53]
	v_mfma_f32_16x16x32_bf16 v[34:37], v[66:69], v[98:101], v[34:37]
	v_mfma_f32_16x16x32_bf16 v[26:29], v[74:77], v[98:101], v[26:29]
	v_mfma_f32_16x16x32_bf16 v[14:17], v[66:69], v[90:93], v[14:17]
	v_mfma_f32_16x16x32_bf16 v[10:13], v[74:77], v[90:93], v[10:13]
	v_mfma_f32_16x16x32_bf16 v[6:9], v[66:69], v[82:85], v[6:9]
	v_mfma_f32_16x16x32_bf16 v[2:5], v[74:77], v[82:85], v[2:5]
	v_mfma_f32_16x16x32_bf16 v[58:61], v[70:73], v[110:113], v[58:61]
	v_mfma_f32_16x16x32_bf16 v[50:53], v[78:81], v[110:113], v[50:53]
	v_mfma_f32_16x16x32_bf16 v[34:37], v[70:73], v[102:105], v[34:37]
	v_mfma_f32_16x16x32_bf16 v[26:29], v[78:81], v[102:105], v[26:29]
	v_mfma_f32_16x16x32_bf16 v[14:17], v[70:73], v[94:97], v[14:17]
	v_mfma_f32_16x16x32_bf16 v[10:13], v[78:81], v[94:97], v[10:13]
	v_mfma_f32_16x16x32_bf16 v[6:9], v[70:73], v[86:89], v[6:9]
	v_mfma_f32_16x16x32_bf16 v[2:5], v[78:81], v[86:89], v[2:5]
	s_barrier
	s_add_i32 s73, s73, 2
	s_cmp_gt_u32 s73, 13
	s_cbranch_scc1 .LBB0_815
.LBB0_812:
	s_mov_b64 s[56:57], s[38:39]
	s_add_u32 s74, s71, s56
	s_addc_u32 s75, s72, s57
	s_add_u32 s38, s56, 0x100
	s_addc_u32 s39, s57, 0
	s_cmp_eq_u32 s73, 12
	s_cselect_b64 s[40:41], -1, 0
	s_and_b64 s[54:55], s[40:41], exec
	s_cselect_b32 s75, s27, s75
	s_cselect_b32 s74, s29, s74
	s_cselect_b32 s54, 0, s38
	s_add_i32 s81, s68, s43
	s_add_i32 m0, s48, 0xc000
	s_add_i32 s80, s48, 0xe000
	s_add_i32 s82, s81, 0x2000
	s_add_u32 s76, s74, 0x80000
	s_addc_u32 s77, s75, 0
	s_and_b64 s[40:41], s[6:7], s[40:41]
	s_and_b64 s[40:41], s[40:41], exec
	s_cselect_b32 s41, s30, s14
	s_cselect_b32 s40, s31, s15
	s_add_u32 s78, s41, s54
	ds_read_b128 v[66:69], v135
	ds_read_b128 v[70:73], v135 offset:1024
	ds_read_b128 v[74:77], v135 offset:2048
	ds_read_b128 v[78:81], v135 offset:3072
	s_addc_u32 s79, s40, 0
	s_add_i32 s83, 0, 0x18000
	s_add_u32 s54, s78, 0x80000
	s_addc_u32 s55, s79, 0
	s_add_i32 s84, s83, s43
	s_add_i32 s85, s84, 0x2000
	s_add_u32 s40, s74, 0x80080
	s_addc_u32 s41, s75, 0
	s_cmp_lg_u32 s73, 12
	v_lshl_add_u64 v[138:139], v[128:129], 0, s[56:57]
	ds_read_b128 v[82:85], v136
	ds_read_b128 v[86:89], v136 offset:1024
	ds_read_b128 v[90:93], v136 offset:2048
	ds_read_b128 v[94:97], v136 offset:3072
	ds_read_b128 v[98:101], v136 offset:4096
	ds_read_b128 v[102:105], v136 offset:5120
	ds_read_b128 v[106:109], v136 offset:6144
	ds_read_b128 v[110:113], v136 offset:7168
	global_load_lds_dwordx4 v[138:139], off
	v_lshl_add_u64 v[138:139], v[130:131], 0, s[56:57]
	s_mov_b32 m0, s80
	s_nop 0
	global_load_lds_dwordx4 v[138:139], off
	s_waitcnt vmcnt(8)
	s_waitcnt lgkmcnt(0)
	s_barrier
	s_waitcnt lgkmcnt(0)
	v_mfma_f32_16x16x32_bf16 v[62:65], v[66:69], v[82:85], v[62:65]
	v_mfma_f32_16x16x32_bf16 v[54:57], v[74:77], v[82:85], v[54:57]
	v_mfma_f32_16x16x32_bf16 v[46:49], v[66:69], v[90:93], v[46:49]
	v_mfma_f32_16x16x32_bf16 v[42:45], v[74:77], v[90:93], v[42:45]
	v_mfma_f32_16x16x32_bf16 v[38:41], v[66:69], v[98:101], v[38:41]
	v_mfma_f32_16x16x32_bf16 v[30:33], v[74:77], v[98:101], v[30:33]
	v_mfma_f32_16x16x32_bf16 v[22:25], v[66:69], v[106:109], v[22:25]
	v_mfma_f32_16x16x32_bf16 v[18:21], v[74:77], v[106:109], v[18:21]
	v_mfma_f32_16x16x32_bf16 v[62:65], v[70:73], v[86:89], v[62:65]
	v_mfma_f32_16x16x32_bf16 v[54:57], v[78:81], v[86:89], v[54:57]
	v_mfma_f32_16x16x32_bf16 v[46:49], v[70:73], v[94:97], v[46:49]
	v_mfma_f32_16x16x32_bf16 v[42:45], v[78:81], v[94:97], v[42:45]
	v_mfma_f32_16x16x32_bf16 v[38:41], v[70:73], v[102:105], v[38:41]
	v_mfma_f32_16x16x32_bf16 v[30:33], v[78:81], v[102:105], v[30:33]
	v_mfma_f32_16x16x32_bf16 v[22:25], v[70:73], v[110:113], v[22:25]
	v_mfma_f32_16x16x32_bf16 v[18:21], v[78:81], v[110:113], v[18:21]
	s_barrier
	s_mov_b32 m0, s81
	v_lshl_add_u64 v[138:139], s[74:75], 0, v[114:115]
	ds_read_b128 v[82:85], v136 offset:16384
	ds_read_b128 v[86:89], v136 offset:17408
	ds_read_b128 v[90:93], v136 offset:18432
	ds_read_b128 v[94:97], v136 offset:19456
	ds_read_b128 v[98:101], v136 offset:20480
	ds_read_b128 v[102:105], v136 offset:21504
	ds_read_b128 v[106:109], v136 offset:22528
	ds_read_b128 v[110:113], v136 offset:23552
	global_load_lds_dwordx4 v[138:139], off
	v_lshl_add_u64 v[140:141], s[74:75], 0, v[116:117]
	s_mov_b32 m0, s82
	v_lshl_add_u64 v[142:143], s[76:77], 0, v[114:115]
	global_load_lds_dwordx4 v[140:141], off
	s_mov_b32 m0, s49
	v_lshl_add_u64 v[144:145], s[78:79], 0, v[116:117]
	global_load_lds_dwordx4 v[142:143], off
	v_lshl_add_u64 v[142:143], s[76:77], 0, v[116:117]
	s_mov_b32 m0, s50
	s_nop 0
	global_load_lds_dwordx4 v[142:143], off
	v_lshl_add_u64 v[142:143], s[78:79], 0, v[114:115]
	s_mov_b32 m0, s48
	s_nop 0
	global_load_lds_dwordx4 v[142:143], off
	s_mov_b32 m0, s51
	s_nop 0
	global_load_lds_dwordx4 v[144:145], off
	s_waitcnt vmcnt(8)
	s_waitcnt lgkmcnt(0)
	s_barrier
	s_waitcnt lgkmcnt(0)
	v_mfma_f32_16x16x32_bf16 v[58:61], v[66:69], v[82:85], v[58:61]
	v_mfma_f32_16x16x32_bf16 v[50:53], v[74:77], v[82:85], v[50:53]
	v_mfma_f32_16x16x32_bf16 v[34:37], v[66:69], v[90:93], v[34:37]
	v_mfma_f32_16x16x32_bf16 v[26:29], v[74:77], v[90:93], v[26:29]
	v_mfma_f32_16x16x32_bf16 v[14:17], v[66:69], v[98:101], v[14:17]
	v_mfma_f32_16x16x32_bf16 v[10:13], v[74:77], v[98:101], v[10:13]
	v_mfma_f32_16x16x32_bf16 v[6:9], v[66:69], v[106:109], v[6:9]
	v_mfma_f32_16x16x32_bf16 v[2:5], v[74:77], v[106:109], v[2:5]
	v_mfma_f32_16x16x32_bf16 v[58:61], v[70:73], v[86:89], v[58:61]
	v_mfma_f32_16x16x32_bf16 v[50:53], v[78:81], v[86:89], v[50:53]
	v_mfma_f32_16x16x32_bf16 v[34:37], v[70:73], v[94:97], v[34:37]
	v_mfma_f32_16x16x32_bf16 v[26:29], v[78:81], v[94:97], v[26:29]
	v_mfma_f32_16x16x32_bf16 v[14:17], v[70:73], v[102:105], v[14:17]
	v_mfma_f32_16x16x32_bf16 v[10:13], v[78:81], v[102:105], v[10:13]
	v_mfma_f32_16x16x32_bf16 v[6:9], v[70:73], v[110:113], v[6:9]
	v_mfma_f32_16x16x32_bf16 v[2:5], v[78:81], v[110:113], v[2:5]
	s_barrier
	v_add_u32_e32 v78, s83, v133
	ds_read_b128 v[66:69], v78
	ds_read_b128 v[70:73], v78 offset:1024
	ds_read_b128 v[74:77], v78 offset:2048
	ds_read_b128 v[78:81], v78 offset:3072
	s_mov_b32 m0, s52
	v_lshl_add_u64 v[146:147], s[54:55], 0, v[114:115]
	ds_read_b128 v[82:85], v136 offset:32768
	ds_read_b128 v[86:89], v136 offset:33792
	ds_read_b128 v[90:93], v136 offset:34816
	ds_read_b128 v[94:97], v136 offset:35840
	ds_read_b128 v[98:101], v136 offset:36864
	ds_read_b128 v[102:105], v136 offset:37888
	ds_read_b128 v[106:109], v136 offset:38912
	ds_read_b128 v[110:113], v136 offset:39936
	global_load_lds_dwordx4 v[146:147], off
	v_lshl_add_u64 v[146:147], s[54:55], 0, v[116:117]
	s_mov_b32 m0, s53
	s_nop 0
	global_load_lds_dwordx4 v[146:147], off
	s_waitcnt vmcnt(8)
	s_waitcnt lgkmcnt(0)
	s_barrier
	s_waitcnt lgkmcnt(0)
	v_mfma_f32_16x16x32_bf16 v[62:65], v[66:69], v[82:85], v[62:65]
	v_mfma_f32_16x16x32_bf16 v[54:57], v[74:77], v[82:85], v[54:57]
	v_mfma_f32_16x16x32_bf16 v[46:49], v[66:69], v[90:93], v[46:49]
	v_mfma_f32_16x16x32_bf16 v[42:45], v[74:77], v[90:93], v[42:45]
	v_mfma_f32_16x16x32_bf16 v[38:41], v[66:69], v[98:101], v[38:41]
	v_mfma_f32_16x16x32_bf16 v[30:33], v[74:77], v[98:101], v[30:33]
	v_mfma_f32_16x16x32_bf16 v[22:25], v[66:69], v[106:109], v[22:25]
	v_mfma_f32_16x16x32_bf16 v[18:21], v[74:77], v[106:109], v[18:21]
	v_mfma_f32_16x16x32_bf16 v[62:65], v[70:73], v[86:89], v[62:65]
	v_mfma_f32_16x16x32_bf16 v[54:57], v[78:81], v[86:89], v[54:57]
	v_mfma_f32_16x16x32_bf16 v[46:49], v[70:73], v[94:97], v[46:49]
	v_mfma_f32_16x16x32_bf16 v[42:45], v[78:81], v[94:97], v[42:45]
	v_mfma_f32_16x16x32_bf16 v[38:41], v[70:73], v[102:105], v[38:41]
	v_mfma_f32_16x16x32_bf16 v[30:33], v[78:81], v[102:105], v[30:33]
	v_mfma_f32_16x16x32_bf16 v[22:25], v[70:73], v[110:113], v[22:25]
	v_mfma_f32_16x16x32_bf16 v[18:21], v[78:81], v[110:113], v[18:21]
	s_barrier
	s_mov_b32 m0, s84
	v_lshl_add_u64 v[138:139], v[138:139], 0, s[12:13]
	ds_read_b128 v[106:109], v136 offset:49152
	ds_read_b128 v[110:113], v136 offset:50176
	ds_read_b128 v[98:101], v136 offset:51200
	ds_read_b128 v[102:105], v136 offset:52224
	ds_read_b128 v[90:93], v136 offset:53248
	ds_read_b128 v[94:97], v136 offset:54272
	ds_read_b128 v[82:85], v136 offset:55296
	ds_read_b128 v[86:89], v136 offset:56320
	global_load_lds_dwordx4 v[138:139], off
	v_lshl_add_u64 v[138:139], v[140:141], 0, s[12:13]
	s_mov_b32 m0, s85
	s_nop 0
	global_load_lds_dwordx4 v[138:139], off
	v_lshl_add_u64 v[138:139], s[40:41], 0, v[114:115]
	s_mov_b32 m0, s65
	s_nop 0
	global_load_lds_dwordx4 v[138:139], off
	v_lshl_add_u64 v[138:139], s[40:41], 0, v[116:117]
	s_mov_b32 m0, s66
	s_nop 0
	global_load_lds_dwordx4 v[138:139], off
	v_lshl_add_u64 v[138:139], v[142:143], 0, s[12:13]
	s_mov_b32 m0, s63
	s_nop 0
	global_load_lds_dwordx4 v[138:139], off
	v_lshl_add_u64 v[138:139], v[144:145], 0, s[12:13]
	s_mov_b32 m0, s64
	s_nop 0
	global_load_lds_dwordx4 v[138:139], off
	s_waitcnt vmcnt(8)
	s_waitcnt lgkmcnt(0)
	s_barrier
	s_cbranch_scc1 .LBB0_811
	v_mov_b32_e32 v137, v1
	v_mov_b32_e32 v138, v132
	s_andn2_b64 vcc, exec, s[16:17]
	s_cbranch_vccnz .LBB0_810
	v_add_u32_e32 v140, s70, v137
	v_ashrrev_i32_e32 v141, 31, v140
	v_lshl_add_u32 v138, v138, 2, s62
	v_lshlrev_b64 v[140:141], 8, v[140:141]
	v_ashrrev_i32_e32 v139, 31, v138
	v_lshl_add_u64 v[140:141], s[36:37], 0, v[140:141]
	v_lshl_add_u64 v[138:139], v[138:139], 2, v[140:141]
	v_add_co_u32_e32 v142, vcc, 0x1000, v138
	global_store_dwordx4 v[138:139], v[62:65], off
	global_store_dwordx4 v[138:139], v[54:57], off offset:64
	v_addc_co_u32_e32 v143, vcc, 0, v139, vcc
	v_lshl_add_u64 v[140:141], v[138:139], 0, s[20:21]
	global_store_dwordx4 v[142:143], v[46:49], off
	global_store_dwordx4 v[140:141], v[42:45], off offset:64
	v_add_co_u32_e32 v142, vcc, 0x2000, v138
	v_lshl_add_u64 v[140:141], v[138:139], 0, s[22:23]
	s_nop 0
	v_addc_co_u32_e32 v143, vcc, 0, v139, vcc
	global_store_dwordx4 v[142:143], v[38:41], off
	global_store_dwordx4 v[140:141], v[30:33], off offset:64
	v_lshl_add_u64 v[140:141], v[138:139], 0, s[24:25]
	v_add_co_u32_e32 v138, vcc, 0x3000, v138
	s_nop 1
	v_addc_co_u32_e32 v139, vcc, 0, v139, vcc
	global_store_dwordx4 v[138:139], v[22:25], off
	global_store_dwordx4 v[140:141], v[18:21], off offset:64
	s_branch .LBB0_810

.LBB0_1005:
	ds_read_b128 v[152:155], v158
	ds_read_b128 v[166:169], v158 offset:1024
	ds_read_b128 v[170:173], v158 offset:2048
	ds_read_b128 v[174:177], v158 offset:3072
	ds_read_b128 v[178:181], v159
	ds_read_b128 v[182:185], v159 offset:1024
	ds_read_b128 v[186:189], v159 offset:2048
	ds_read_b128 v[190:193], v159 offset:3072
	s_add_u32 s40, s64, s10
	s_addc_u32 s41, s65, s11
	s_add_u32 s38, s10, 0x100
	s_addc_u32 s39, s11, 0
	s_cmpk_eq_i32 s10, 0xf00
	s_cselect_b64 vcc, -1, 0
	s_and_b64 s[2:3], vcc, exec
	s_cselect_b32 s41, s31, s41
	s_cselect_b32 s40, s37, s40
	s_cselect_b32 s67, 0, s38
	v_lshl_add_u64 v[226:227], v[146:147], 0, s[10:11]
	s_add_i32 m0, s49, 0xc000
	ds_read_b128 v[194:197], v160
	ds_read_b128 v[198:201], v160 offset:1024
	ds_read_b128 v[202:205], v160 offset:2048
	ds_read_b128 v[206:209], v160 offset:3072
	ds_read_b128 v[210:213], v160 offset:4096
	ds_read_b128 v[214:217], v160 offset:5120
	ds_read_b128 v[218:221], v160 offset:6144
	ds_read_b128 v[222:225], v160 offset:7168
	global_load_lds_dwordx4 v[226:227], off
	v_lshl_add_u64 v[226:227], v[144:145], 0, s[10:11]
	s_add_i32 m0, s49, 0xe000
	s_nop 0
	global_load_lds_dwordx4 v[226:227], off
	s_waitcnt vmcnt(8)
	s_waitcnt lgkmcnt(0)
	s_barrier
	s_waitcnt lgkmcnt(0)
	v_mfma_f32_16x16x32_bf16 v[126:129], v[152:155], v[194:197], v[126:129]
	v_mfma_f32_16x16x32_bf16 v[122:125], v[170:173], v[194:197], v[122:125]
	v_mfma_f32_16x16x32_bf16 v[110:113], v[152:155], v[202:205], v[110:113]
	v_mfma_f32_16x16x32_bf16 v[106:109], v[170:173], v[202:205], v[106:109]
	v_mfma_f32_16x16x32_bf16 v[94:97], v[152:155], v[210:213], v[94:97]
	v_mfma_f32_16x16x32_bf16 v[90:93], v[170:173], v[210:213], v[90:93]
	v_mfma_f32_16x16x32_bf16 v[78:81], v[152:155], v[218:221], v[78:81]
	v_mfma_f32_16x16x32_bf16 v[74:77], v[170:173], v[218:221], v[74:77]
	v_mfma_f32_16x16x32_bf16 v[126:129], v[166:169], v[198:201], v[126:129]
	v_mfma_f32_16x16x32_bf16 v[122:125], v[174:177], v[198:201], v[122:125]
	v_mfma_f32_16x16x32_bf16 v[110:113], v[166:169], v[206:209], v[110:113]
	v_mfma_f32_16x16x32_bf16 v[106:109], v[174:177], v[206:209], v[106:109]
	v_mfma_f32_16x16x32_bf16 v[94:97], v[166:169], v[214:217], v[94:97]
	v_mfma_f32_16x16x32_bf16 v[90:93], v[174:177], v[214:217], v[90:93]
	v_mfma_f32_16x16x32_bf16 v[78:81], v[166:169], v[222:225], v[78:81]
	v_mfma_f32_16x16x32_bf16 v[74:77], v[174:177], v[222:225], v[74:77]
	v_mfma_f32_16x16x32_bf16 v[118:121], v[178:181], v[194:197], v[118:121]
	v_mfma_f32_16x16x32_bf16 v[114:117], v[186:189], v[194:197], v[114:117]
	v_mfma_f32_16x16x32_bf16 v[102:105], v[178:181], v[202:205], v[102:105]
	v_mfma_f32_16x16x32_bf16 v[98:101], v[186:189], v[202:205], v[98:101]
	v_mfma_f32_16x16x32_bf16 v[86:89], v[178:181], v[210:213], v[86:89]
	v_mfma_f32_16x16x32_bf16 v[82:85], v[186:189], v[210:213], v[82:85]
	v_mfma_f32_16x16x32_bf16 v[70:73], v[178:181], v[218:221], v[70:73]
	v_mfma_f32_16x16x32_bf16 v[66:69], v[186:189], v[218:221], v[66:69]
	v_mfma_f32_16x16x32_bf16 v[118:121], v[182:185], v[198:201], v[118:121]
	v_mfma_f32_16x16x32_bf16 v[114:117], v[190:193], v[198:201], v[114:117]
	v_mfma_f32_16x16x32_bf16 v[102:105], v[182:185], v[206:209], v[102:105]
	v_mfma_f32_16x16x32_bf16 v[98:101], v[190:193], v[206:209], v[98:101]
	v_mfma_f32_16x16x32_bf16 v[86:89], v[182:185], v[214:217], v[86:89]
	v_mfma_f32_16x16x32_bf16 v[82:85], v[190:193], v[214:217], v[82:85]
	v_mfma_f32_16x16x32_bf16 v[70:73], v[182:185], v[222:225], v[70:73]
	v_mfma_f32_16x16x32_bf16 v[66:69], v[190:193], v[222:225], v[66:69]
	s_barrier
	s_add_i32 s2, s61, s48
	v_lshl_add_u64 v[226:227], s[40:41], 0, v[132:133]
	s_mov_b32 m0, s2
	ds_read_b128 v[194:197], v160 offset:16384
	ds_read_b128 v[198:201], v160 offset:17408
	ds_read_b128 v[202:205], v160 offset:18432
	ds_read_b128 v[206:209], v160 offset:19456
	ds_read_b128 v[210:213], v160 offset:20480
	ds_read_b128 v[214:217], v160 offset:21504
	ds_read_b128 v[218:221], v160 offset:22528
	ds_read_b128 v[222:225], v160 offset:23552
	global_load_lds_dwordx4 v[226:227], off
	s_add_i32 m0, s2, 0x2000
	s_add_u32 s2, s40, 0x80000
	v_lshl_add_u64 v[228:229], s[40:41], 0, v[134:135]
	s_addc_u32 s3, s41, 0
	s_add_i32 s10, s62, s48
	global_load_lds_dwordx4 v[228:229], off
	v_lshl_add_u64 v[230:231], s[2:3], 0, v[132:133]
	s_mov_b32 m0, s10
	v_cndmask_b32_e32 v130, v148, v164, vcc
	global_load_lds_dwordx4 v[230:231], off
	s_add_i32 m0, s10, 0x2000
	v_lshl_add_u64 v[230:231], s[2:3], 0, v[134:135]
	s_add_u32 s2, s16, s67
	global_load_lds_dwordx4 v[230:231], off
	s_addc_u32 s3, s17, 0
	s_mov_b32 m0, s49
	v_lshl_add_u64 v[230:231], s[2:3], 0, v[130:131]
	global_load_lds_dwordx4 v130, s[2:3]
	v_cndmask_b32_e32 v130, v140, v163, vcc
	s_mov_b32 m0, s50
	v_lshl_add_u64 v[232:233], s[2:3], 0, v[130:131]
	global_load_lds_dwordx4 v130, s[2:3]
	s_waitcnt vmcnt(8)
	s_waitcnt lgkmcnt(0)
	s_barrier
	s_waitcnt lgkmcnt(0)
	v_mfma_f32_16x16x32_bf16 v[62:65], v[152:155], v[194:197], v[62:65]
	v_mfma_f32_16x16x32_bf16 v[58:61], v[170:173], v[194:197], v[58:61]
	v_mfma_f32_16x16x32_bf16 v[46:49], v[152:155], v[202:205], v[46:49]
	v_mfma_f32_16x16x32_bf16 v[42:45], v[170:173], v[202:205], v[42:45]
	v_mfma_f32_16x16x32_bf16 v[30:33], v[152:155], v[210:213], v[30:33]
	v_mfma_f32_16x16x32_bf16 v[26:29], v[170:173], v[210:213], v[26:29]
	v_mfma_f32_16x16x32_bf16 v[14:17], v[152:155], v[218:221], v[14:17]
	v_mfma_f32_16x16x32_bf16 v[10:13], v[170:173], v[218:221], v[10:13]
	v_mfma_f32_16x16x32_bf16 v[62:65], v[166:169], v[198:201], v[62:65]
	v_mfma_f32_16x16x32_bf16 v[58:61], v[174:177], v[198:201], v[58:61]
	v_mfma_f32_16x16x32_bf16 v[46:49], v[166:169], v[206:209], v[46:49]
	v_mfma_f32_16x16x32_bf16 v[42:45], v[174:177], v[206:209], v[42:45]
	v_mfma_f32_16x16x32_bf16 v[30:33], v[166:169], v[214:217], v[30:33]
	v_mfma_f32_16x16x32_bf16 v[26:29], v[174:177], v[214:217], v[26:29]
	v_mfma_f32_16x16x32_bf16 v[14:17], v[166:169], v[222:225], v[14:17]
	v_mfma_f32_16x16x32_bf16 v[10:13], v[174:177], v[222:225], v[10:13]
	v_mfma_f32_16x16x32_bf16 v[54:57], v[178:181], v[194:197], v[54:57]
	v_mfma_f32_16x16x32_bf16 v[50:53], v[186:189], v[194:197], v[50:53]
	v_mfma_f32_16x16x32_bf16 v[38:41], v[178:181], v[202:205], v[38:41]
	v_mfma_f32_16x16x32_bf16 v[34:37], v[186:189], v[202:205], v[34:37]
	v_mfma_f32_16x16x32_bf16 v[22:25], v[178:181], v[210:213], v[22:25]
	v_mfma_f32_16x16x32_bf16 v[18:21], v[186:189], v[210:213], v[18:21]
	v_mfma_f32_16x16x32_bf16 v[6:9], v[178:181], v[218:221], v[6:9]
	v_mfma_f32_16x16x32_bf16 v[2:5], v[186:189], v[218:221], v[2:5]
	v_mfma_f32_16x16x32_bf16 v[54:57], v[182:185], v[198:201], v[54:57]
	v_mfma_f32_16x16x32_bf16 v[50:53], v[190:193], v[198:201], v[50:53]
	v_mfma_f32_16x16x32_bf16 v[38:41], v[182:185], v[206:209], v[38:41]
	v_mfma_f32_16x16x32_bf16 v[34:37], v[190:193], v[206:209], v[34:37]
	v_mfma_f32_16x16x32_bf16 v[22:25], v[182:185], v[214:217], v[22:25]
	v_mfma_f32_16x16x32_bf16 v[18:21], v[190:193], v[214:217], v[18:21]
	v_mfma_f32_16x16x32_bf16 v[6:9], v[182:185], v[222:225], v[6:9]
	v_mfma_f32_16x16x32_bf16 v[2:5], v[190:193], v[222:225], v[2:5]
	s_barrier
	s_add_i32 s10, 0, 0x18000
	v_add_u32_e32 v130, s10, v156
	s_add_i32 s11, 0, 0x1c000
	ds_read_b128 v[152:155], v130
	ds_read_b128 v[166:169], v130 offset:1024
	ds_read_b128 v[170:173], v130 offset:2048
	ds_read_b128 v[174:177], v130 offset:3072
	v_add_u32_e32 v130, s11, v156
	ds_read_b128 v[178:181], v130
	ds_read_b128 v[182:185], v130 offset:1024
	ds_read_b128 v[186:189], v130 offset:2048
	ds_read_b128 v[190:193], v130 offset:3072
	s_mov_b32 m0, s51
	v_cndmask_b32_e32 v130, v138, v161, vcc
	ds_read_b128 v[194:197], v160 offset:32768
	ds_read_b128 v[198:201], v160 offset:33792
	ds_read_b128 v[202:205], v160 offset:34816
	ds_read_b128 v[206:209], v160 offset:35840
	ds_read_b128 v[210:213], v160 offset:36864
	ds_read_b128 v[214:217], v160 offset:37888
	ds_read_b128 v[218:221], v160 offset:38912
	ds_read_b128 v[222:225], v160 offset:39936
	global_load_lds_dwordx4 v130, s[2:3]
	v_cndmask_b32_e32 v130, v142, v162, vcc
	s_mov_b32 m0, s52
	s_nop 0
	global_load_lds_dwordx4 v130, s[2:3]
	s_waitcnt vmcnt(8)
	s_waitcnt lgkmcnt(0)
	s_barrier
	s_waitcnt lgkmcnt(0)
	v_mfma_f32_16x16x32_bf16 v[126:129], v[152:155], v[194:197], v[126:129]
	v_mfma_f32_16x16x32_bf16 v[122:125], v[170:173], v[194:197], v[122:125]
	v_mfma_f32_16x16x32_bf16 v[110:113], v[152:155], v[202:205], v[110:113]
	v_mfma_f32_16x16x32_bf16 v[106:109], v[170:173], v[202:205], v[106:109]
	v_mfma_f32_16x16x32_bf16 v[94:97], v[152:155], v[210:213], v[94:97]
	v_mfma_f32_16x16x32_bf16 v[90:93], v[170:173], v[210:213], v[90:93]
	v_mfma_f32_16x16x32_bf16 v[78:81], v[152:155], v[218:221], v[78:81]
	v_mfma_f32_16x16x32_bf16 v[74:77], v[170:173], v[218:221], v[74:77]
	v_mfma_f32_16x16x32_bf16 v[126:129], v[166:169], v[198:201], v[126:129]
	v_mfma_f32_16x16x32_bf16 v[122:125], v[174:177], v[198:201], v[122:125]
	v_mfma_f32_16x16x32_bf16 v[110:113], v[166:169], v[206:209], v[110:113]
	v_mfma_f32_16x16x32_bf16 v[106:109], v[174:177], v[206:209], v[106:109]
	v_mfma_f32_16x16x32_bf16 v[94:97], v[166:169], v[214:217], v[94:97]
	v_mfma_f32_16x16x32_bf16 v[90:93], v[174:177], v[214:217], v[90:93]
	v_mfma_f32_16x16x32_bf16 v[78:81], v[166:169], v[222:225], v[78:81]
	v_mfma_f32_16x16x32_bf16 v[74:77], v[174:177], v[222:225], v[74:77]
	v_mfma_f32_16x16x32_bf16 v[118:121], v[178:181], v[194:197], v[118:121]
	v_mfma_f32_16x16x32_bf16 v[114:117], v[186:189], v[194:197], v[114:117]
	v_mfma_f32_16x16x32_bf16 v[102:105], v[178:181], v[202:205], v[102:105]
	v_mfma_f32_16x16x32_bf16 v[98:101], v[186:189], v[202:205], v[98:101]
	v_mfma_f32_16x16x32_bf16 v[86:89], v[178:181], v[210:213], v[86:89]
	v_mfma_f32_16x16x32_bf16 v[82:85], v[186:189], v[210:213], v[82:85]
	v_mfma_f32_16x16x32_bf16 v[70:73], v[178:181], v[218:221], v[70:73]
	v_mfma_f32_16x16x32_bf16 v[66:69], v[186:189], v[218:221], v[66:69]
	v_mfma_f32_16x16x32_bf16 v[118:121], v[182:185], v[198:201], v[118:121]
	v_mfma_f32_16x16x32_bf16 v[114:117], v[190:193], v[198:201], v[114:117]
	v_mfma_f32_16x16x32_bf16 v[102:105], v[182:185], v[206:209], v[102:105]
	v_mfma_f32_16x16x32_bf16 v[98:101], v[190:193], v[206:209], v[98:101]
	v_mfma_f32_16x16x32_bf16 v[86:89], v[182:185], v[214:217], v[86:89]
	v_mfma_f32_16x16x32_bf16 v[82:85], v[190:193], v[214:217], v[82:85]
	v_mfma_f32_16x16x32_bf16 v[70:73], v[182:185], v[222:225], v[70:73]
	v_mfma_f32_16x16x32_bf16 v[66:69], v[190:193], v[222:225], v[66:69]
	s_barrier
	s_add_i32 s2, s10, s48
	v_lshl_add_u64 v[226:227], v[226:227], 0, s[20:21]
	s_mov_b32 m0, s2
	ds_read_b128 v[194:197], v160 offset:49152
	ds_read_b128 v[198:201], v160 offset:50176
	ds_read_b128 v[202:205], v160 offset:51200
	ds_read_b128 v[206:209], v160 offset:52224
	ds_read_b128 v[210:213], v160 offset:53248
	ds_read_b128 v[214:217], v160 offset:54272
	ds_read_b128 v[218:221], v160 offset:55296
	ds_read_b128 v[222:225], v160 offset:56320
	global_load_lds_dwordx4 v[226:227], off
	s_add_i32 m0, s2, 0x2000
	s_add_u32 s2, s40, 0x80080
	v_lshl_add_u64 v[226:227], v[228:229], 0, s[20:21]
	s_addc_u32 s3, s41, 0
	s_add_i32 s10, s11, s48
	global_load_lds_dwordx4 v[226:227], off
	v_lshl_add_u64 v[226:227], s[2:3], 0, v[132:133]
	s_mov_b32 m0, s10
	s_nop 0
	global_load_lds_dwordx4 v[226:227], off
	v_lshl_add_u64 v[226:227], s[2:3], 0, v[134:135]
	s_add_i32 m0, s10, 0x2000
	s_nop 0
	global_load_lds_dwordx4 v[226:227], off
	v_lshl_add_u64 v[226:227], v[230:231], 0, s[20:21]
	s_mov_b32 m0, s58
	s_nop 0
	global_load_lds_dwordx4 v[226:227], off
	v_lshl_add_u64 v[226:227], v[232:233], 0, s[20:21]
	s_mov_b32 m0, s59
	s_nop 0
	global_load_lds_dwordx4 v[226:227], off
	s_waitcnt vmcnt(8)
	s_waitcnt lgkmcnt(0)
	s_barrier
	s_waitcnt lgkmcnt(0)
	v_mfma_f32_16x16x32_bf16 v[62:65], v[152:155], v[194:197], v[62:65]
	v_mfma_f32_16x16x32_bf16 v[58:61], v[170:173], v[194:197], v[58:61]
	v_mfma_f32_16x16x32_bf16 v[46:49], v[152:155], v[202:205], v[46:49]
	v_mfma_f32_16x16x32_bf16 v[42:45], v[170:173], v[202:205], v[42:45]
	v_mfma_f32_16x16x32_bf16 v[30:33], v[152:155], v[210:213], v[30:33]
	v_mfma_f32_16x16x32_bf16 v[26:29], v[170:173], v[210:213], v[26:29]
	v_mfma_f32_16x16x32_bf16 v[14:17], v[152:155], v[218:221], v[14:17]
	v_mfma_f32_16x16x32_bf16 v[10:13], v[170:173], v[218:221], v[10:13]
	v_mfma_f32_16x16x32_bf16 v[62:65], v[166:169], v[198:201], v[62:65]
	v_mfma_f32_16x16x32_bf16 v[58:61], v[174:177], v[198:201], v[58:61]
	v_mfma_f32_16x16x32_bf16 v[46:49], v[166:169], v[206:209], v[46:49]
	v_mfma_f32_16x16x32_bf16 v[42:45], v[174:177], v[206:209], v[42:45]
	v_mfma_f32_16x16x32_bf16 v[30:33], v[166:169], v[214:217], v[30:33]
	v_mfma_f32_16x16x32_bf16 v[26:29], v[174:177], v[214:217], v[26:29]
	v_mfma_f32_16x16x32_bf16 v[14:17], v[166:169], v[222:225], v[14:17]
	v_mfma_f32_16x16x32_bf16 v[10:13], v[174:177], v[222:225], v[10:13]
	v_mfma_f32_16x16x32_bf16 v[54:57], v[178:181], v[194:197], v[54:57]
	v_mfma_f32_16x16x32_bf16 v[50:53], v[186:189], v[194:197], v[50:53]
	v_mfma_f32_16x16x32_bf16 v[38:41], v[178:181], v[202:205], v[38:41]
	v_mfma_f32_16x16x32_bf16 v[34:37], v[186:189], v[202:205], v[34:37]
	v_mfma_f32_16x16x32_bf16 v[22:25], v[178:181], v[210:213], v[22:25]
	v_mfma_f32_16x16x32_bf16 v[18:21], v[186:189], v[210:213], v[18:21]
	v_mfma_f32_16x16x32_bf16 v[6:9], v[178:181], v[218:221], v[6:9]
	v_mfma_f32_16x16x32_bf16 v[2:5], v[186:189], v[218:221], v[2:5]
	v_mfma_f32_16x16x32_bf16 v[54:57], v[182:185], v[198:201], v[54:57]
	v_mfma_f32_16x16x32_bf16 v[50:53], v[190:193], v[198:201], v[50:53]
	v_mfma_f32_16x16x32_bf16 v[38:41], v[182:185], v[206:209], v[38:41]
	v_mfma_f32_16x16x32_bf16 v[34:37], v[190:193], v[206:209], v[34:37]
	v_mfma_f32_16x16x32_bf16 v[22:25], v[182:185], v[214:217], v[22:25]
	v_mfma_f32_16x16x32_bf16 v[18:21], v[190:193], v[214:217], v[18:21]
	v_mfma_f32_16x16x32_bf16 v[6:9], v[182:185], v[222:225], v[6:9]
	v_mfma_f32_16x16x32_bf16 v[2:5], v[190:193], v[222:225], v[2:5]
	s_barrier
	s_add_i32 s66, s66, 2
	s_cmp_gt_u32 s66, 29
	s_mov_b64 s[10:11], s[38:39]
	s_cbranch_scc0 .LBB0_1005
	s_and_b64 vcc, exec, s[24:25]
	s_cbranch_vccz .LBB0_1008
	s_barrier

.LBB0_1104:
	s_waitcnt lgkmcnt(0)
	v_mfma_f32_16x16x32_bf16 v[126:129], v[146:149], v[186:189], v[126:129]
	v_mfma_f32_16x16x32_bf16 v[122:125], v[154:157], v[186:189], v[122:125]
	v_mfma_f32_16x16x32_bf16 v[110:113], v[146:149], v[178:181], v[110:113]
	v_mfma_f32_16x16x32_bf16 v[106:109], v[154:157], v[178:181], v[106:109]
	v_mfma_f32_16x16x32_bf16 v[94:97], v[146:149], v[170:173], v[94:97]
	v_mfma_f32_16x16x32_bf16 v[90:93], v[154:157], v[170:173], v[90:93]
	v_mfma_f32_16x16x32_bf16 v[22:25], v[146:149], v[162:165], v[22:25]
	v_mfma_f32_16x16x32_bf16 v[14:17], v[154:157], v[162:165], v[14:17]
	v_mfma_f32_16x16x32_bf16 v[126:129], v[150:153], v[190:193], v[126:129]
	v_mfma_f32_16x16x32_bf16 v[122:125], v[158:161], v[190:193], v[122:125]
	v_mfma_f32_16x16x32_bf16 v[110:113], v[150:153], v[182:185], v[110:113]
	v_mfma_f32_16x16x32_bf16 v[106:109], v[158:161], v[182:185], v[106:109]
	v_mfma_f32_16x16x32_bf16 v[94:97], v[150:153], v[174:177], v[94:97]
	v_mfma_f32_16x16x32_bf16 v[90:93], v[158:161], v[174:177], v[90:93]
	v_mfma_f32_16x16x32_bf16 v[22:25], v[150:153], v[166:169], v[22:25]
	v_mfma_f32_16x16x32_bf16 v[14:17], v[158:161], v[166:169], v[14:17]
	v_mfma_f32_16x16x32_bf16 v[118:121], v[130:133], v[186:189], v[118:121]
	v_mfma_f32_16x16x32_bf16 v[114:117], v[138:141], v[186:189], v[114:117]
	v_mfma_f32_16x16x32_bf16 v[102:105], v[130:133], v[178:181], v[102:105]
	v_mfma_f32_16x16x32_bf16 v[98:101], v[138:141], v[178:181], v[98:101]
	v_mfma_f32_16x16x32_bf16 v[38:41], v[130:133], v[170:173], v[38:41]
	v_mfma_f32_16x16x32_bf16 v[30:33], v[138:141], v[170:173], v[30:33]
	v_mfma_f32_16x16x32_bf16 v[6:9], v[130:133], v[162:165], v[6:9]
	v_mfma_f32_16x16x32_bf16 v[2:5], v[138:141], v[162:165], v[2:5]
	v_mfma_f32_16x16x32_bf16 v[118:121], v[134:137], v[190:193], v[118:121]
	v_mfma_f32_16x16x32_bf16 v[114:117], v[142:145], v[190:193], v[114:117]
	v_mfma_f32_16x16x32_bf16 v[102:105], v[134:137], v[182:185], v[102:105]
	v_mfma_f32_16x16x32_bf16 v[98:101], v[142:145], v[182:185], v[98:101]
	v_mfma_f32_16x16x32_bf16 v[38:41], v[134:137], v[174:177], v[38:41]
	v_mfma_f32_16x16x32_bf16 v[30:33], v[142:145], v[174:177], v[30:33]
	v_mfma_f32_16x16x32_bf16 v[6:9], v[134:137], v[166:169], v[6:9]
	v_mfma_f32_16x16x32_bf16 v[2:5], v[142:145], v[166:169], v[2:5]
	s_barrier
	s_add_i32 s2, s87, 2
	s_cmp_gt_u32 s87, 5
	s_mov_b32 s87, s2
	s_cbranch_scc1 .LBB0_1124

.LBB0_1122:
	s_lshl_b32 s2, s87, 7
	v_add_u32_e32 v142, s80, v205
	v_add_u32_e32 v158, s81, v205
	s_add_u32 s64, s38, s2
	ds_read_b128 v[130:133], v142
	ds_read_b128 v[134:137], v142 offset:1024
	ds_read_b128 v[138:141], v142 offset:2048
	ds_read_b128 v[142:145], v142 offset:3072
	ds_read_b128 v[146:149], v158
	ds_read_b128 v[150:153], v158 offset:1024
	ds_read_b128 v[154:157], v158 offset:2048
	ds_read_b128 v[158:161], v158 offset:3072
	s_addc_u32 s65, s39, 0
	s_add_u32 s66, s64, 0x100
	s_addc_u32 s67, s65, 0
	s_and_b64 s[64:65], s[60:61], exec
	s_cselect_b32 s65, s35, s67
	s_cselect_b32 s64, s83, s66
	s_add_i32 s68, s2, 0x100
	s_and_b64 s[66:67], s[60:61], exec
	s_cselect_b32 s68, 0, s68
	s_add_u32 s2, s36, s2
	s_addc_u32 s67, s37, 0
	s_add_u32 s66, s2, 0x20080
	s_addc_u32 s67, s67, 0
	v_lshl_add_u64 v[210:211], s[66:67], 0, v[194:195]
	s_add_i32 m0, s50, 0xc000
	ds_read_b128 v[162:165], v209
	ds_read_b128 v[166:169], v209 offset:1024
	ds_read_b128 v[170:173], v209 offset:2048
	ds_read_b128 v[174:177], v209 offset:3072
	ds_read_b128 v[178:181], v209 offset:4096
	ds_read_b128 v[182:185], v209 offset:5120
	ds_read_b128 v[186:189], v209 offset:6144
	ds_read_b128 v[190:193], v209 offset:7168
	global_load_lds_dwordx4 v[210:211], off
	v_lshl_add_u64 v[210:211], s[66:67], 0, v[198:199]
	s_add_i32 m0, s50, 0xe000
	s_nop 0
	global_load_lds_dwordx4 v[210:211], off
	s_waitcnt vmcnt(8)
	s_waitcnt lgkmcnt(0)
	s_barrier
	s_waitcnt lgkmcnt(0)
	v_mfma_f32_16x16x32_bf16 v[86:89], v[130:133], v[162:165], v[86:89]
	v_mfma_f32_16x16x32_bf16 v[82:85], v[138:141], v[162:165], v[82:85]
	v_mfma_f32_16x16x32_bf16 v[78:81], v[130:133], v[170:173], v[78:81]
	v_mfma_f32_16x16x32_bf16 v[74:77], v[138:141], v[170:173], v[74:77]
	v_mfma_f32_16x16x32_bf16 v[70:73], v[130:133], v[178:181], v[70:73]
	v_mfma_f32_16x16x32_bf16 v[66:69], v[138:141], v[178:181], v[66:69]
	v_mfma_f32_16x16x32_bf16 v[62:65], v[130:133], v[186:189], v[62:65]
	v_mfma_f32_16x16x32_bf16 v[58:61], v[138:141], v[186:189], v[58:61]
	v_mfma_f32_16x16x32_bf16 v[86:89], v[134:137], v[166:169], v[86:89]
	v_mfma_f32_16x16x32_bf16 v[82:85], v[142:145], v[166:169], v[82:85]
	v_mfma_f32_16x16x32_bf16 v[78:81], v[134:137], v[174:177], v[78:81]
	v_mfma_f32_16x16x32_bf16 v[74:77], v[142:145], v[174:177], v[74:77]
	v_mfma_f32_16x16x32_bf16 v[70:73], v[134:137], v[182:185], v[70:73]
	v_mfma_f32_16x16x32_bf16 v[66:69], v[142:145], v[182:185], v[66:69]
	v_mfma_f32_16x16x32_bf16 v[62:65], v[134:137], v[190:193], v[62:65]
	v_mfma_f32_16x16x32_bf16 v[58:61], v[142:145], v[190:193], v[58:61]
	v_mfma_f32_16x16x32_bf16 v[54:57], v[146:149], v[162:165], v[54:57]
	v_mfma_f32_16x16x32_bf16 v[50:53], v[154:157], v[162:165], v[50:53]
	v_mfma_f32_16x16x32_bf16 v[46:49], v[146:149], v[170:173], v[46:49]
	v_mfma_f32_16x16x32_bf16 v[42:45], v[154:157], v[170:173], v[42:45]
	v_mfma_f32_16x16x32_bf16 v[34:37], v[146:149], v[178:181], v[34:37]
	v_mfma_f32_16x16x32_bf16 v[26:29], v[154:157], v[178:181], v[26:29]
	v_mfma_f32_16x16x32_bf16 v[18:21], v[146:149], v[186:189], v[18:21]
	v_mfma_f32_16x16x32_bf16 v[10:13], v[154:157], v[186:189], v[10:13]
	v_mfma_f32_16x16x32_bf16 v[54:57], v[150:153], v[166:169], v[54:57]
	v_mfma_f32_16x16x32_bf16 v[50:53], v[158:161], v[166:169], v[50:53]
	v_mfma_f32_16x16x32_bf16 v[46:49], v[150:153], v[174:177], v[46:49]
	v_mfma_f32_16x16x32_bf16 v[42:45], v[158:161], v[174:177], v[42:45]
	v_mfma_f32_16x16x32_bf16 v[34:37], v[150:153], v[182:185], v[34:37]
	v_mfma_f32_16x16x32_bf16 v[26:29], v[158:161], v[182:185], v[26:29]
	v_mfma_f32_16x16x32_bf16 v[18:21], v[150:153], v[190:193], v[18:21]
	v_mfma_f32_16x16x32_bf16 v[10:13], v[158:161], v[190:193], v[10:13]
	s_barrier
	s_add_i32 s2, s80, s49
	v_lshl_add_u64 v[210:211], s[64:65], 0, v[196:197]
	s_mov_b32 m0, s2
	ds_read_b128 v[162:165], v209 offset:16384
	ds_read_b128 v[166:169], v209 offset:17408
	ds_read_b128 v[170:173], v209 offset:18432
	ds_read_b128 v[174:177], v209 offset:19456
	ds_read_b128 v[178:181], v209 offset:20480
	ds_read_b128 v[182:185], v209 offset:21504
	ds_read_b128 v[186:189], v209 offset:22528
	ds_read_b128 v[190:193], v209 offset:23552
	global_load_lds_dwordx4 v[210:211], off
	s_add_i32 m0, s2, 0x2000
	s_add_u32 s66, s64, 0x20000
	v_lshl_add_u64 v[212:213], s[64:65], 0, v[200:201]
	s_addc_u32 s67, s65, 0
	s_add_i32 s2, s81, s49
	global_load_lds_dwordx4 v[212:213], off
	v_lshl_add_u64 v[214:215], s[66:67], 0, v[196:197]
	s_mov_b32 m0, s2
	s_nop 0
	global_load_lds_dwordx4 v[214:215], off
	s_add_i32 m0, s2, 0x2000
	s_add_u32 s62, s62, s68
	v_lshl_add_u64 v[214:215], s[66:67], 0, v[200:201]
	s_addc_u32 s63, s63, 0
	global_load_lds_dwordx4 v[214:215], off
	v_lshl_add_u64 v[214:215], s[62:63], 0, v[194:195]
	s_mov_b32 m0, s50
	v_lshl_add_u64 v[216:217], s[62:63], 0, v[198:199]
	global_load_lds_dwordx4 v[214:215], off
	s_mov_b32 m0, s51
	s_nop 0
	global_load_lds_dwordx4 v[216:217], off
	s_waitcnt vmcnt(8)
	s_waitcnt lgkmcnt(0)
	s_barrier
	s_waitcnt lgkmcnt(0)
	v_mfma_f32_16x16x32_bf16 v[126:129], v[130:133], v[162:165], v[126:129]
	v_mfma_f32_16x16x32_bf16 v[122:125], v[138:141], v[162:165], v[122:125]
	v_mfma_f32_16x16x32_bf16 v[110:113], v[130:133], v[170:173], v[110:113]
	v_mfma_f32_16x16x32_bf16 v[106:109], v[138:141], v[170:173], v[106:109]
	v_mfma_f32_16x16x32_bf16 v[94:97], v[130:133], v[178:181], v[94:97]
	v_mfma_f32_16x16x32_bf16 v[90:93], v[138:141], v[178:181], v[90:93]
	v_mfma_f32_16x16x32_bf16 v[22:25], v[130:133], v[186:189], v[22:25]
	v_mfma_f32_16x16x32_bf16 v[14:17], v[138:141], v[186:189], v[14:17]
	v_mfma_f32_16x16x32_bf16 v[126:129], v[134:137], v[166:169], v[126:129]
	v_mfma_f32_16x16x32_bf16 v[122:125], v[142:145], v[166:169], v[122:125]
	v_mfma_f32_16x16x32_bf16 v[110:113], v[134:137], v[174:177], v[110:113]
	v_mfma_f32_16x16x32_bf16 v[106:109], v[142:145], v[174:177], v[106:109]
	v_mfma_f32_16x16x32_bf16 v[94:97], v[134:137], v[182:185], v[94:97]
	v_mfma_f32_16x16x32_bf16 v[90:93], v[142:145], v[182:185], v[90:93]
	v_mfma_f32_16x16x32_bf16 v[22:25], v[134:137], v[190:193], v[22:25]
	v_mfma_f32_16x16x32_bf16 v[14:17], v[142:145], v[190:193], v[14:17]
	v_mfma_f32_16x16x32_bf16 v[118:121], v[146:149], v[162:165], v[118:121]
	v_mfma_f32_16x16x32_bf16 v[114:117], v[154:157], v[162:165], v[114:117]
	v_mfma_f32_16x16x32_bf16 v[102:105], v[146:149], v[170:173], v[102:105]
	v_mfma_f32_16x16x32_bf16 v[98:101], v[154:157], v[170:173], v[98:101]
	v_mfma_f32_16x16x32_bf16 v[38:41], v[146:149], v[178:181], v[38:41]
	v_mfma_f32_16x16x32_bf16 v[30:33], v[154:157], v[178:181], v[30:33]
	v_mfma_f32_16x16x32_bf16 v[6:9], v[146:149], v[186:189], v[6:9]
	v_mfma_f32_16x16x32_bf16 v[2:5], v[154:157], v[186:189], v[2:5]
	v_mfma_f32_16x16x32_bf16 v[118:121], v[150:153], v[166:169], v[118:121]
	v_mfma_f32_16x16x32_bf16 v[114:117], v[158:161], v[166:169], v[114:117]
	v_mfma_f32_16x16x32_bf16 v[102:105], v[150:153], v[174:177], v[102:105]
	v_mfma_f32_16x16x32_bf16 v[98:101], v[158:161], v[174:177], v[98:101]
	v_mfma_f32_16x16x32_bf16 v[38:41], v[150:153], v[182:185], v[38:41]
	v_mfma_f32_16x16x32_bf16 v[30:33], v[158:161], v[182:185], v[30:33]
	v_mfma_f32_16x16x32_bf16 v[6:9], v[150:153], v[190:193], v[6:9]
	v_mfma_f32_16x16x32_bf16 v[2:5], v[158:161], v[190:193], v[2:5]
	s_barrier
	s_add_i32 s2, 0, 0x18000
	s_add_i32 s66, 0, 0x1c000
	v_add_u32_e32 v130, s2, v205
	v_add_u32_e32 v142, s66, v205
	ds_read_b128 v[146:149], v130
	ds_read_b128 v[150:153], v130 offset:1024
	ds_read_b128 v[154:157], v130 offset:2048
	ds_read_b128 v[158:161], v130 offset:3072
	ds_read_b128 v[130:133], v142
	ds_read_b128 v[134:137], v142 offset:1024
	ds_read_b128 v[138:141], v142 offset:2048
	ds_read_b128 v[142:145], v142 offset:3072
	s_add_u32 s62, s62, 0x20000
	s_addc_u32 s63, s63, 0
	s_mov_b32 m0, s52
	v_lshl_add_u64 v[218:219], s[62:63], 0, v[194:195]
	ds_read_b128 v[162:165], v209 offset:32768
	ds_read_b128 v[166:169], v209 offset:33792
	ds_read_b128 v[170:173], v209 offset:34816
	ds_read_b128 v[174:177], v209 offset:35840
	ds_read_b128 v[178:181], v209 offset:36864
	ds_read_b128 v[182:185], v209 offset:37888
	ds_read_b128 v[186:189], v209 offset:38912
	ds_read_b128 v[190:193], v209 offset:39936
	global_load_lds_dwordx4 v[218:219], off
	v_lshl_add_u64 v[218:219], s[62:63], 0, v[198:199]
	s_mov_b32 m0, s53
	s_nop 0
	global_load_lds_dwordx4 v[218:219], off
	s_waitcnt vmcnt(8)
	s_waitcnt lgkmcnt(0)
	s_barrier
	s_waitcnt lgkmcnt(0)
	v_mfma_f32_16x16x32_bf16 v[86:89], v[146:149], v[162:165], v[86:89]
	v_mfma_f32_16x16x32_bf16 v[82:85], v[154:157], v[162:165], v[82:85]
	v_mfma_f32_16x16x32_bf16 v[78:81], v[146:149], v[170:173], v[78:81]
	v_mfma_f32_16x16x32_bf16 v[74:77], v[154:157], v[170:173], v[74:77]
	v_mfma_f32_16x16x32_bf16 v[70:73], v[146:149], v[178:181], v[70:73]
	v_mfma_f32_16x16x32_bf16 v[66:69], v[154:157], v[178:181], v[66:69]
	v_mfma_f32_16x16x32_bf16 v[62:65], v[146:149], v[186:189], v[62:65]
	v_mfma_f32_16x16x32_bf16 v[58:61], v[154:157], v[186:189], v[58:61]
	v_mfma_f32_16x16x32_bf16 v[86:89], v[150:153], v[166:169], v[86:89]
	v_mfma_f32_16x16x32_bf16 v[82:85], v[158:161], v[166:169], v[82:85]
	v_mfma_f32_16x16x32_bf16 v[78:81], v[150:153], v[174:177], v[78:81]
	v_mfma_f32_16x16x32_bf16 v[74:77], v[158:161], v[174:177], v[74:77]
	v_mfma_f32_16x16x32_bf16 v[70:73], v[150:153], v[182:185], v[70:73]
	v_mfma_f32_16x16x32_bf16 v[66:69], v[158:161], v[182:185], v[66:69]
	v_mfma_f32_16x16x32_bf16 v[62:65], v[150:153], v[190:193], v[62:65]
	v_mfma_f32_16x16x32_bf16 v[58:61], v[158:161], v[190:193], v[58:61]
	v_mfma_f32_16x16x32_bf16 v[54:57], v[130:133], v[162:165], v[54:57]
	v_mfma_f32_16x16x32_bf16 v[50:53], v[138:141], v[162:165], v[50:53]
	v_mfma_f32_16x16x32_bf16 v[46:49], v[130:133], v[170:173], v[46:49]
	v_mfma_f32_16x16x32_bf16 v[42:45], v[138:141], v[170:173], v[42:45]
	v_mfma_f32_16x16x32_bf16 v[34:37], v[130:133], v[178:181], v[34:37]
	v_mfma_f32_16x16x32_bf16 v[26:29], v[138:141], v[178:181], v[26:29]
	v_mfma_f32_16x16x32_bf16 v[18:21], v[130:133], v[186:189], v[18:21]
	v_mfma_f32_16x16x32_bf16 v[10:13], v[138:141], v[186:189], v[10:13]
	v_mfma_f32_16x16x32_bf16 v[54:57], v[134:137], v[166:169], v[54:57]
	v_mfma_f32_16x16x32_bf16 v[50:53], v[142:145], v[166:169], v[50:53]
	v_mfma_f32_16x16x32_bf16 v[46:49], v[134:137], v[174:177], v[46:49]
	v_mfma_f32_16x16x32_bf16 v[42:45], v[142:145], v[174:177], v[42:45]
	v_mfma_f32_16x16x32_bf16 v[34:37], v[134:137], v[182:185], v[34:37]
	v_mfma_f32_16x16x32_bf16 v[26:29], v[142:145], v[182:185], v[26:29]
	v_mfma_f32_16x16x32_bf16 v[18:21], v[134:137], v[190:193], v[18:21]
	v_mfma_f32_16x16x32_bf16 v[10:13], v[142:145], v[190:193], v[10:13]
	s_barrier
	s_add_i32 s2, s2, s49
	v_lshl_add_u64 v[210:211], v[210:211], 0, s[12:13]
	s_mov_b32 m0, s2
	ds_read_b128 v[186:189], v209 offset:49152
	ds_read_b128 v[190:193], v209 offset:50176
	ds_read_b128 v[178:181], v209 offset:51200
	ds_read_b128 v[182:185], v209 offset:52224
	ds_read_b128 v[170:173], v209 offset:53248
	ds_read_b128 v[174:177], v209 offset:54272
	ds_read_b128 v[162:165], v209 offset:55296
	ds_read_b128 v[166:169], v209 offset:56320
	global_load_lds_dwordx4 v[210:211], off
	s_add_i32 m0, s2, 0x2000
	s_add_u32 s62, s64, 0x20080
	v_lshl_add_u64 v[210:211], v[212:213], 0, s[12:13]
	s_addc_u32 s63, s65, 0
	s_add_i32 s2, s66, s49
	global_load_lds_dwordx4 v[210:211], off
	v_lshl_add_u64 v[210:211], s[62:63], 0, v[196:197]
	s_mov_b32 m0, s2
	s_andn2_b64 vcc, exec, s[60:61]
	global_load_lds_dwordx4 v[210:211], off
	v_lshl_add_u64 v[210:211], s[62:63], 0, v[200:201]
	s_add_i32 m0, s2, 0x2000
	s_nop 0
	global_load_lds_dwordx4 v[210:211], off
	v_lshl_add_u64 v[210:211], v[214:215], 0, s[12:13]
	s_mov_b32 m0, s73
	s_nop 0
	global_load_lds_dwordx4 v[210:211], off
	v_lshl_add_u64 v[210:211], v[216:217], 0, s[12:13]
	s_mov_b32 m0, s74
	s_nop 0
	global_load_lds_dwordx4 v[210:211], off
	s_waitcnt vmcnt(8)
	s_waitcnt lgkmcnt(0)
	s_barrier
	s_cbranch_vccnz .LBB0_1104
	v_pk_mul_f32 v[214:215], v[86:87], s[20:21] op_sel_hi:[1,0]
	v_pk_mul_f32 v[216:217], v[82:83], s[20:21] op_sel_hi:[1,0]
	v_mov_b32_e32 v218, 0
	v_mov_b32_e32 v219, 0
	v_cvt_pk_fp8_f32 v218, v214, v215
	v_cvt_pk_fp8_f32 v219, v216, v217
	v_pk_mul_f32 v[214:215], v[88:89], s[20:21] op_sel_hi:[1,0]
	v_pk_mul_f32 v[216:217], v[84:85], s[20:21] op_sel_hi:[1,0]
	v_cvt_pk_fp8_f32 v218, v214, v215 op_sel:[0,0,1]
	v_cvt_pk_fp8_f32 v219, v216, v217 op_sel:[0,0,1]
	v_pk_mul_f32 v[214:215], v[54:55], s[20:21] op_sel_hi:[1,0]
	v_pk_mul_f32 v[216:217], v[50:51], s[20:21] op_sel_hi:[1,0]
	v_mov_b32_e32 v220, 0
	v_mov_b32_e32 v221, 0
	v_mov_b32_e32 v210, v1
	v_mov_b32_e32 v211, v204
	v_cvt_pk_fp8_f32 v220, v214, v215
	v_cvt_pk_fp8_f32 v221, v216, v217
	v_pk_mul_f32 v[214:215], v[56:57], s[20:21] op_sel_hi:[1,0]
	v_add_u32_e32 v210, s85, v210
	v_lshl_add_u32 v212, v211, 3, s86
	v_ashrrev_i32_e32 v211, 31, v210
	v_pk_mul_f32 v[216:217], v[52:53], s[20:21] op_sel_hi:[1,0]
	v_lshlrev_b64 v[210:211], 11, v[210:211]
	v_cvt_pk_fp8_f32 v220, v214, v215 op_sel:[0,0,1]
	v_cvt_pk_fp8_f32 v221, v216, v217 op_sel:[0,0,1]
	v_ashrrev_i32_e32 v213, 31, v212
	v_lshl_add_u64 v[210:211], s[10:11], 0, v[210:211]
	v_lshl_add_u64 v[210:211], v[210:211], 0, v[212:213]
	global_store_dwordx2 v[210:211], v[218:219], off
	global_store_dwordx2 v[210:211], v[220:221], off offset:128
	v_pk_mul_f32 v[214:215], v[78:79], s[20:21] op_sel_hi:[1,0]
	v_pk_mul_f32 v[216:217], v[74:75], s[20:21] op_sel_hi:[1,0]
	v_mov_b32_e32 v218, 0
	v_mov_b32_e32 v219, 0
	v_cvt_pk_fp8_f32 v218, v214, v215
	v_cvt_pk_fp8_f32 v219, v216, v217
	v_pk_mul_f32 v[214:215], v[80:81], s[20:21] op_sel_hi:[1,0]
	v_pk_mul_f32 v[216:217], v[76:77], s[20:21] op_sel_hi:[1,0]
	v_cvt_pk_fp8_f32 v218, v214, v215 op_sel:[0,0,1]
	v_cvt_pk_fp8_f32 v219, v216, v217 op_sel:[0,0,1]
	v_pk_mul_f32 v[214:215], v[46:47], s[20:21] op_sel_hi:[1,0]
	v_pk_mul_f32 v[216:217], v[42:43], s[20:21] op_sel_hi:[1,0]
	v_mov_b32_e32 v220, 0
	v_mov_b32_e32 v221, 0
	v_cvt_pk_fp8_f32 v220, v214, v215
	v_cvt_pk_fp8_f32 v221, v216, v217
	v_pk_mul_f32 v[214:215], v[48:49], s[20:21] op_sel_hi:[1,0]
	v_pk_mul_f32 v[216:217], v[44:45], s[20:21] op_sel_hi:[1,0]
	v_cvt_pk_fp8_f32 v220, v214, v215 op_sel:[0,0,1]
	v_cvt_pk_fp8_f32 v221, v216, v217 op_sel:[0,0,1]
	s_mov_b32 s2, 0x8000
	v_add_co_u32_e32 v214, vcc, s2, v210
	s_mov_b64 s[60:61], 0x8000
	s_nop 0
	v_addc_co_u32_e32 v215, vcc, 0, v211, vcc
	v_lshl_add_u64 v[212:213], v[210:211], 0, s[60:61]
	global_store_dwordx2 v[214:215], v[218:219], off
	global_store_dwordx2 v[212:213], v[220:221], off offset:128
	v_pk_mul_f32 v[214:215], v[70:71], s[20:21] op_sel_hi:[1,0]
	v_pk_mul_f32 v[216:217], v[66:67], s[20:21] op_sel_hi:[1,0]
	v_mov_b32_e32 v218, 0
	v_mov_b32_e32 v219, 0
	v_cvt_pk_fp8_f32 v218, v214, v215
	v_cvt_pk_fp8_f32 v219, v216, v217
	v_pk_mul_f32 v[214:215], v[72:73], s[20:21] op_sel_hi:[1,0]
	v_pk_mul_f32 v[216:217], v[68:69], s[20:21] op_sel_hi:[1,0]
	v_cvt_pk_fp8_f32 v218, v214, v215 op_sel:[0,0,1]
	v_cvt_pk_fp8_f32 v219, v216, v217 op_sel:[0,0,1]
	v_pk_mul_f32 v[214:215], v[34:35], s[20:21] op_sel_hi:[1,0]
	v_pk_mul_f32 v[216:217], v[26:27], s[20:21] op_sel_hi:[1,0]
	v_mov_b32_e32 v220, 0
	v_mov_b32_e32 v221, 0
	v_cvt_pk_fp8_f32 v220, v214, v215
	v_cvt_pk_fp8_f32 v221, v216, v217
	v_pk_mul_f32 v[214:215], v[36:37], s[20:21] op_sel_hi:[1,0]
	v_pk_mul_f32 v[216:217], v[28:29], s[20:21] op_sel_hi:[1,0]
	v_cvt_pk_fp8_f32 v220, v214, v215 op_sel:[0,0,1]
	v_cvt_pk_fp8_f32 v221, v216, v217 op_sel:[0,0,1]
	s_mov_b32 s2, 0x10000
	v_add_co_u32_e32 v214, vcc, s2, v210
	v_lshl_add_u64 v[212:213], v[210:211], 0, s[24:25]
	s_nop 0
	v_addc_co_u32_e32 v215, vcc, 0, v211, vcc
	global_store_dwordx2 v[214:215], v[218:219], off
	global_store_dwordx2 v[212:213], v[220:221], off offset:128
	v_pk_mul_f32 v[214:215], v[62:63], s[20:21] op_sel_hi:[1,0]
	v_pk_mul_f32 v[216:217], v[58:59], s[20:21] op_sel_hi:[1,0]
	v_mov_b32_e32 v218, 0
	v_mov_b32_e32 v219, 0
	v_cvt_pk_fp8_f32 v218, v214, v215
	v_cvt_pk_fp8_f32 v219, v216, v217
	v_pk_mul_f32 v[214:215], v[64:65], s[20:21] op_sel_hi:[1,0]
	v_pk_mul_f32 v[216:217], v[60:61], s[20:21] op_sel_hi:[1,0]
	v_cvt_pk_fp8_f32 v218, v214, v215 op_sel:[0,0,1]
	v_cvt_pk_fp8_f32 v219, v216, v217 op_sel:[0,0,1]
	v_pk_mul_f32 v[214:215], v[18:19], s[20:21] op_sel_hi:[1,0]
	v_pk_mul_f32 v[216:217], v[10:11], s[20:21] op_sel_hi:[1,0]
	v_mov_b32_e32 v220, 0
	v_mov_b32_e32 v221, 0
	v_cvt_pk_fp8_f32 v220, v214, v215
	v_cvt_pk_fp8_f32 v221, v216, v217
	v_pk_mul_f32 v[214:215], v[20:21], s[20:21] op_sel_hi:[1,0]
	v_pk_mul_f32 v[216:217], v[12:13], s[20:21] op_sel_hi:[1,0]
	v_cvt_pk_fp8_f32 v220, v214, v215 op_sel:[0,0,1]
	v_cvt_pk_fp8_f32 v221, v216, v217 op_sel:[0,0,1]
	s_mov_b32 s2, 0x18000
	v_lshl_add_u64 v[212:213], v[210:211], 0, s[28:29]
	v_add_co_u32_e32 v210, vcc, s2, v210
	s_nop 1
	v_addc_co_u32_e32 v211, vcc, 0, v211, vcc
	global_store_dwordx2 v[210:211], v[218:219], off
	global_store_dwordx2 v[212:213], v[220:221], off offset:128
	s_branch .LBB0_1104

.LBB0_1292:
.LBB0_1293:
	s_waitcnt lgkmcnt(0)
	v_mfma_f32_16x16x32_bf16 v[126:129], v[146:149], v[186:189], v[126:129]
	v_mfma_f32_16x16x32_bf16 v[122:125], v[154:157], v[186:189], v[122:125]
	v_mfma_f32_16x16x32_bf16 v[114:117], v[146:149], v[178:181], v[114:117]
	v_mfma_f32_16x16x32_bf16 v[106:109], v[154:157], v[178:181], v[106:109]
	v_mfma_f32_16x16x32_bf16 v[102:105], v[146:149], v[170:173], v[102:105]
	v_mfma_f32_16x16x32_bf16 v[94:97], v[154:157], v[170:173], v[94:97]
	v_mfma_f32_16x16x32_bf16 v[86:89], v[146:149], v[162:165], v[86:89]
	v_mfma_f32_16x16x32_bf16 v[78:81], v[154:157], v[162:165], v[78:81]
	v_mfma_f32_16x16x32_bf16 v[126:129], v[150:153], v[190:193], v[126:129]
	v_mfma_f32_16x16x32_bf16 v[122:125], v[158:161], v[190:193], v[122:125]
	v_mfma_f32_16x16x32_bf16 v[114:117], v[150:153], v[182:185], v[114:117]
	v_mfma_f32_16x16x32_bf16 v[106:109], v[158:161], v[182:185], v[106:109]
	v_mfma_f32_16x16x32_bf16 v[102:105], v[150:153], v[174:177], v[102:105]
	v_mfma_f32_16x16x32_bf16 v[94:97], v[158:161], v[174:177], v[94:97]
	v_mfma_f32_16x16x32_bf16 v[86:89], v[150:153], v[166:169], v[86:89]
	v_mfma_f32_16x16x32_bf16 v[78:81], v[158:161], v[166:169], v[78:81]
	v_mfma_f32_16x16x32_bf16 v[118:121], v[130:133], v[186:189], v[118:121]
	v_mfma_f32_16x16x32_bf16 v[110:113], v[138:141], v[186:189], v[110:113]
	v_mfma_f32_16x16x32_bf16 v[98:101], v[130:133], v[178:181], v[98:101]
	v_mfma_f32_16x16x32_bf16 v[90:93], v[138:141], v[178:181], v[90:93]
	v_mfma_f32_16x16x32_bf16 v[82:85], v[130:133], v[170:173], v[82:85]
	v_mfma_f32_16x16x32_bf16 v[74:77], v[138:141], v[170:173], v[74:77]
	v_mfma_f32_16x16x32_bf16 v[70:73], v[130:133], v[162:165], v[70:73]
	v_mfma_f32_16x16x32_bf16 v[66:69], v[138:141], v[162:165], v[66:69]
	v_mfma_f32_16x16x32_bf16 v[118:121], v[134:137], v[190:193], v[118:121]
	v_mfma_f32_16x16x32_bf16 v[110:113], v[142:145], v[190:193], v[110:113]
	v_mfma_f32_16x16x32_bf16 v[98:101], v[134:137], v[182:185], v[98:101]
	v_mfma_f32_16x16x32_bf16 v[90:93], v[142:145], v[182:185], v[90:93]
	v_mfma_f32_16x16x32_bf16 v[82:85], v[134:137], v[174:177], v[82:85]
	v_mfma_f32_16x16x32_bf16 v[74:77], v[142:145], v[174:177], v[74:77]
	v_mfma_f32_16x16x32_bf16 v[70:73], v[134:137], v[166:169], v[70:73]
	v_mfma_f32_16x16x32_bf16 v[66:69], v[142:145], v[166:169], v[66:69]
	s_barrier
	s_add_i32 s73, s73, 2
	s_cmp_gt_u32 s73, 29
	s_cbranch_scc1 .LBB0_1299
.LBB0_1294:
	s_mov_b64 s[56:57], s[40:41]
	s_add_u32 s2, s71, s56
	s_addc_u32 s22, s72, s57
	s_add_u32 s40, s56, 0x100
	s_addc_u32 s41, s57, 0
	s_cmp_eq_u32 s73, 28
	s_cselect_b64 s[8:9], -1, 0
	s_and_b64 s[12:13], s[8:9], exec
	s_cselect_b32 s61, s67, s22
	s_cselect_b32 s60, s68, s2
	s_cselect_b32 s2, 0, s40
	s_add_i32 s22, s86, s42
	s_add_i32 m0, s51, 0xc000
	s_add_i32 s13, s51, 0xe000
	s_add_i32 s23, s22, 0x2000
	s_add_u32 s62, s60, 0x80000
	s_addc_u32 s63, s61, 0
	s_add_i32 s24, s87, s42
	s_add_i32 s25, s24, 0x2000
	s_and_b64 s[8:9], s[6:7], s[8:9]
	ds_read_b128 v[130:133], v229
	ds_read_b128 v[134:137], v229 offset:1024
	ds_read_b128 v[138:141], v229 offset:2048
	ds_read_b128 v[142:145], v229 offset:3072
	ds_read_b128 v[146:149], v230
	ds_read_b128 v[150:153], v230 offset:1024
	ds_read_b128 v[154:157], v230 offset:2048
	ds_read_b128 v[158:161], v230 offset:3072
	s_and_b64 s[8:9], s[8:9], exec
	s_cselect_b32 s9, s30, s36
	s_cselect_b32 s8, s31, s37
	s_add_u32 s64, s9, s2
	s_addc_u32 s65, s8, 0
	s_add_i32 s82, 0, 0x18000
	s_add_i32 s83, 0, 0x1c000
	s_add_u32 s58, s64, 0x80000
	s_addc_u32 s59, s65, 0
	s_add_i32 s8, s82, s42
	s_add_i32 s2, s8, 0x2000
	s_add_u32 s54, s60, 0x80080
	s_addc_u32 s55, s61, 0
	s_add_i32 s12, s83, s42
	s_add_i32 s9, s12, 0x2000
	s_cmp_lg_u32 s73, 28
	v_lshl_add_u64 v[224:225], v[220:221], 0, s[56:57]
	ds_read_b128 v[162:165], v231
	ds_read_b128 v[166:169], v231 offset:1024
	ds_read_b128 v[170:173], v231 offset:2048
	ds_read_b128 v[174:177], v231 offset:3072
	ds_read_b128 v[178:181], v231 offset:4096
	ds_read_b128 v[182:185], v231 offset:5120
	ds_read_b128 v[186:189], v231 offset:6144
	ds_read_b128 v[190:193], v231 offset:7168
	global_load_lds_dwordx4 v[224:225], off
	v_lshl_add_u64 v[224:225], v[222:223], 0, s[56:57]
	s_mov_b32 m0, s13
	s_nop 0
	global_load_lds_dwordx4 v[224:225], off
	s_waitcnt vmcnt(8)
	s_waitcnt lgkmcnt(0)
	s_barrier
	s_waitcnt lgkmcnt(0)
	v_mfma_f32_16x16x32_bf16 v[62:65], v[130:133], v[162:165], v[62:65]
	v_mfma_f32_16x16x32_bf16 v[58:61], v[138:141], v[162:165], v[58:61]
	v_mfma_f32_16x16x32_bf16 v[54:57], v[130:133], v[170:173], v[54:57]
	v_mfma_f32_16x16x32_bf16 v[50:53], v[138:141], v[170:173], v[50:53]
	v_mfma_f32_16x16x32_bf16 v[46:49], v[130:133], v[178:181], v[46:49]
	v_mfma_f32_16x16x32_bf16 v[42:45], v[138:141], v[178:181], v[42:45]
	v_mfma_f32_16x16x32_bf16 v[38:41], v[130:133], v[186:189], v[38:41]
	v_mfma_f32_16x16x32_bf16 v[34:37], v[138:141], v[186:189], v[34:37]
	v_mfma_f32_16x16x32_bf16 v[62:65], v[134:137], v[166:169], v[62:65]
	v_mfma_f32_16x16x32_bf16 v[58:61], v[142:145], v[166:169], v[58:61]
	v_mfma_f32_16x16x32_bf16 v[54:57], v[134:137], v[174:177], v[54:57]
	v_mfma_f32_16x16x32_bf16 v[50:53], v[142:145], v[174:177], v[50:53]
	v_mfma_f32_16x16x32_bf16 v[46:49], v[134:137], v[182:185], v[46:49]
	v_mfma_f32_16x16x32_bf16 v[42:45], v[142:145], v[182:185], v[42:45]
	v_mfma_f32_16x16x32_bf16 v[38:41], v[134:137], v[190:193], v[38:41]
	v_mfma_f32_16x16x32_bf16 v[34:37], v[142:145], v[190:193], v[34:37]
	v_mfma_f32_16x16x32_bf16 v[30:33], v[146:149], v[162:165], v[30:33]
	v_mfma_f32_16x16x32_bf16 v[26:29], v[154:157], v[162:165], v[26:29]
	v_mfma_f32_16x16x32_bf16 v[22:25], v[146:149], v[170:173], v[22:25]
	v_mfma_f32_16x16x32_bf16 v[18:21], v[154:157], v[170:173], v[18:21]
	v_mfma_f32_16x16x32_bf16 v[14:17], v[146:149], v[178:181], v[14:17]
	v_mfma_f32_16x16x32_bf16 v[10:13], v[154:157], v[178:181], v[10:13]
	v_mfma_f32_16x16x32_bf16 v[6:9], v[146:149], v[186:189], v[6:9]
	v_mfma_f32_16x16x32_bf16 v[2:5], v[154:157], v[186:189], v[2:5]
	v_mfma_f32_16x16x32_bf16 v[30:33], v[150:153], v[166:169], v[30:33]
	v_mfma_f32_16x16x32_bf16 v[26:29], v[158:161], v[166:169], v[26:29]
	v_mfma_f32_16x16x32_bf16 v[22:25], v[150:153], v[174:177], v[22:25]
	v_mfma_f32_16x16x32_bf16 v[18:21], v[158:161], v[174:177], v[18:21]
	v_mfma_f32_16x16x32_bf16 v[14:17], v[150:153], v[182:185], v[14:17]
	v_mfma_f32_16x16x32_bf16 v[10:13], v[158:161], v[182:185], v[10:13]
	v_mfma_f32_16x16x32_bf16 v[6:9], v[150:153], v[190:193], v[6:9]
	v_mfma_f32_16x16x32_bf16 v[2:5], v[158:161], v[190:193], v[2:5]
	s_barrier
	s_mov_b32 m0, s22
	v_lshl_add_u64 v[224:225], s[60:61], 0, v[196:197]
	ds_read_b128 v[162:165], v231 offset:16384
	ds_read_b128 v[166:169], v231 offset:17408
	ds_read_b128 v[170:173], v231 offset:18432
	ds_read_b128 v[174:177], v231 offset:19456
	ds_read_b128 v[178:181], v231 offset:20480
	ds_read_b128 v[182:185], v231 offset:21504
	ds_read_b128 v[186:189], v231 offset:22528
	ds_read_b128 v[190:193], v231 offset:23552
	global_load_lds_dwordx4 v[224:225], off
	v_lshl_add_u64 v[232:233], s[60:61], 0, v[200:201]
	s_mov_b32 m0, s23
	v_lshl_add_u64 v[234:235], s[62:63], 0, v[196:197]
	global_load_lds_dwordx4 v[232:233], off
	s_mov_b32 m0, s24
	v_lshl_add_u64 v[236:237], s[64:65], 0, v[198:199]
	global_load_lds_dwordx4 v[234:235], off
	v_lshl_add_u64 v[234:235], s[62:63], 0, v[200:201]
	s_mov_b32 m0, s25
	s_nop 0
	global_load_lds_dwordx4 v[234:235], off
	v_lshl_add_u64 v[234:235], s[64:65], 0, v[194:195]
	s_mov_b32 m0, s51
	s_nop 0
	global_load_lds_dwordx4 v[234:235], off
	s_mov_b32 m0, s52
	s_nop 0
	global_load_lds_dwordx4 v[236:237], off
	s_waitcnt vmcnt(8)
	s_waitcnt lgkmcnt(0)
	s_barrier
	s_waitcnt lgkmcnt(0)
	v_mfma_f32_16x16x32_bf16 v[126:129], v[130:133], v[162:165], v[126:129]
	v_mfma_f32_16x16x32_bf16 v[122:125], v[138:141], v[162:165], v[122:125]
	v_mfma_f32_16x16x32_bf16 v[114:117], v[130:133], v[170:173], v[114:117]
	v_mfma_f32_16x16x32_bf16 v[106:109], v[138:141], v[170:173], v[106:109]
	v_mfma_f32_16x16x32_bf16 v[102:105], v[130:133], v[178:181], v[102:105]
	v_mfma_f32_16x16x32_bf16 v[94:97], v[138:141], v[178:181], v[94:97]
	v_mfma_f32_16x16x32_bf16 v[86:89], v[130:133], v[186:189], v[86:89]
	v_mfma_f32_16x16x32_bf16 v[78:81], v[138:141], v[186:189], v[78:81]
	v_mfma_f32_16x16x32_bf16 v[126:129], v[134:137], v[166:169], v[126:129]
	v_mfma_f32_16x16x32_bf16 v[122:125], v[142:145], v[166:169], v[122:125]
	v_mfma_f32_16x16x32_bf16 v[114:117], v[134:137], v[174:177], v[114:117]
	v_mfma_f32_16x16x32_bf16 v[106:109], v[142:145], v[174:177], v[106:109]
	v_mfma_f32_16x16x32_bf16 v[102:105], v[134:137], v[182:185], v[102:105]
	v_mfma_f32_16x16x32_bf16 v[94:97], v[142:145], v[182:185], v[94:97]
	v_mfma_f32_16x16x32_bf16 v[86:89], v[134:137], v[190:193], v[86:89]
	v_mfma_f32_16x16x32_bf16 v[78:81], v[142:145], v[190:193], v[78:81]
	v_mfma_f32_16x16x32_bf16 v[118:121], v[146:149], v[162:165], v[118:121]
	v_mfma_f32_16x16x32_bf16 v[110:113], v[154:157], v[162:165], v[110:113]
	v_mfma_f32_16x16x32_bf16 v[98:101], v[146:149], v[170:173], v[98:101]
	v_mfma_f32_16x16x32_bf16 v[90:93], v[154:157], v[170:173], v[90:93]
	v_mfma_f32_16x16x32_bf16 v[82:85], v[146:149], v[178:181], v[82:85]
	v_mfma_f32_16x16x32_bf16 v[74:77], v[154:157], v[178:181], v[74:77]
	v_mfma_f32_16x16x32_bf16 v[70:73], v[146:149], v[186:189], v[70:73]
	v_mfma_f32_16x16x32_bf16 v[66:69], v[154:157], v[186:189], v[66:69]
	v_mfma_f32_16x16x32_bf16 v[118:121], v[150:153], v[166:169], v[118:121]
	v_mfma_f32_16x16x32_bf16 v[110:113], v[158:161], v[166:169], v[110:113]
	v_mfma_f32_16x16x32_bf16 v[98:101], v[150:153], v[174:177], v[98:101]
	v_mfma_f32_16x16x32_bf16 v[90:93], v[158:161], v[174:177], v[90:93]
	v_mfma_f32_16x16x32_bf16 v[82:85], v[150:153], v[182:185], v[82:85]
	v_mfma_f32_16x16x32_bf16 v[74:77], v[158:161], v[182:185], v[74:77]
	v_mfma_f32_16x16x32_bf16 v[70:73], v[150:153], v[190:193], v[70:73]
	v_mfma_f32_16x16x32_bf16 v[66:69], v[158:161], v[190:193], v[66:69]
	s_barrier
	v_add_u32_e32 v130, s82, v227
	v_add_u32_e32 v142, s83, v227
	ds_read_b128 v[146:149], v130
	ds_read_b128 v[150:153], v130 offset:1024
	ds_read_b128 v[154:157], v130 offset:2048
	ds_read_b128 v[158:161], v130 offset:3072
	ds_read_b128 v[130:133], v142
	ds_read_b128 v[134:137], v142 offset:1024
	ds_read_b128 v[138:141], v142 offset:2048
	ds_read_b128 v[142:145], v142 offset:3072
	s_mov_b32 m0, s53
	v_lshl_add_u64 v[238:239], s[58:59], 0, v[194:195]
	ds_read_b128 v[162:165], v231 offset:32768
	ds_read_b128 v[166:169], v231 offset:33792
	ds_read_b128 v[170:173], v231 offset:34816
	ds_read_b128 v[174:177], v231 offset:35840
	ds_read_b128 v[178:181], v231 offset:36864
	ds_read_b128 v[182:185], v231 offset:37888
	ds_read_b128 v[186:189], v231 offset:38912
	ds_read_b128 v[190:193], v231 offset:39936
	global_load_lds_dwordx4 v[238:239], off
	v_lshl_add_u64 v[238:239], s[58:59], 0, v[198:199]
	s_mov_b32 m0, s74
	s_nop 0
	global_load_lds_dwordx4 v[238:239], off
	s_waitcnt vmcnt(8)
	s_waitcnt lgkmcnt(0)
	s_barrier
	s_waitcnt lgkmcnt(0)
	v_mfma_f32_16x16x32_bf16 v[62:65], v[146:149], v[162:165], v[62:65]
	v_mfma_f32_16x16x32_bf16 v[58:61], v[154:157], v[162:165], v[58:61]
	v_mfma_f32_16x16x32_bf16 v[54:57], v[146:149], v[170:173], v[54:57]
	v_mfma_f32_16x16x32_bf16 v[50:53], v[154:157], v[170:173], v[50:53]
	v_mfma_f32_16x16x32_bf16 v[46:49], v[146:149], v[178:181], v[46:49]
	v_mfma_f32_16x16x32_bf16 v[42:45], v[154:157], v[178:181], v[42:45]
	v_mfma_f32_16x16x32_bf16 v[38:41], v[146:149], v[186:189], v[38:41]
	v_mfma_f32_16x16x32_bf16 v[34:37], v[154:157], v[186:189], v[34:37]
	v_mfma_f32_16x16x32_bf16 v[62:65], v[150:153], v[166:169], v[62:65]
	v_mfma_f32_16x16x32_bf16 v[58:61], v[158:161], v[166:169], v[58:61]
	v_mfma_f32_16x16x32_bf16 v[54:57], v[150:153], v[174:177], v[54:57]
	v_mfma_f32_16x16x32_bf16 v[50:53], v[158:161], v[174:177], v[50:53]
	v_mfma_f32_16x16x32_bf16 v[46:49], v[150:153], v[182:185], v[46:49]
	v_mfma_f32_16x16x32_bf16 v[42:45], v[158:161], v[182:185], v[42:45]
	v_mfma_f32_16x16x32_bf16 v[38:41], v[150:153], v[190:193], v[38:41]
	v_mfma_f32_16x16x32_bf16 v[34:37], v[158:161], v[190:193], v[34:37]
	v_mfma_f32_16x16x32_bf16 v[30:33], v[130:133], v[162:165], v[30:33]
	v_mfma_f32_16x16x32_bf16 v[26:29], v[138:141], v[162:165], v[26:29]
	v_mfma_f32_16x16x32_bf16 v[22:25], v[130:133], v[170:173], v[22:25]
	v_mfma_f32_16x16x32_bf16 v[18:21], v[138:141], v[170:173], v[18:21]
	v_mfma_f32_16x16x32_bf16 v[14:17], v[130:133], v[178:181], v[14:17]
	v_mfma_f32_16x16x32_bf16 v[10:13], v[138:141], v[178:181], v[10:13]
	v_mfma_f32_16x16x32_bf16 v[6:9], v[130:133], v[186:189], v[6:9]
	v_mfma_f32_16x16x32_bf16 v[2:5], v[138:141], v[186:189], v[2:5]
	v_mfma_f32_16x16x32_bf16 v[30:33], v[134:137], v[166:169], v[30:33]
	v_mfma_f32_16x16x32_bf16 v[26:29], v[142:145], v[166:169], v[26:29]
	v_mfma_f32_16x16x32_bf16 v[22:25], v[134:137], v[174:177], v[22:25]
	v_mfma_f32_16x16x32_bf16 v[18:21], v[142:145], v[174:177], v[18:21]
	v_mfma_f32_16x16x32_bf16 v[14:17], v[134:137], v[182:185], v[14:17]
	v_mfma_f32_16x16x32_bf16 v[10:13], v[142:145], v[182:185], v[10:13]
	v_mfma_f32_16x16x32_bf16 v[6:9], v[134:137], v[190:193], v[6:9]
	v_mfma_f32_16x16x32_bf16 v[2:5], v[142:145], v[190:193], v[2:5]
	s_barrier
	s_mov_b32 m0, s8
	v_lshl_add_u64 v[224:225], v[224:225], 0, s[18:19]
	ds_read_b128 v[186:189], v231 offset:49152
	ds_read_b128 v[190:193], v231 offset:50176
	ds_read_b128 v[178:181], v231 offset:51200
	ds_read_b128 v[182:185], v231 offset:52224
	ds_read_b128 v[170:173], v231 offset:53248
	ds_read_b128 v[174:177], v231 offset:54272
	ds_read_b128 v[162:165], v231 offset:55296
	ds_read_b128 v[166:169], v231 offset:56320
	global_load_lds_dwordx4 v[224:225], off
	v_lshl_add_u64 v[224:225], v[232:233], 0, s[18:19]
	s_mov_b32 m0, s2
	s_nop 0
	global_load_lds_dwordx4 v[224:225], off
	v_lshl_add_u64 v[224:225], s[54:55], 0, v[196:197]
	s_mov_b32 m0, s12
	s_nop 0
	global_load_lds_dwordx4 v[224:225], off
	v_lshl_add_u64 v[224:225], s[54:55], 0, v[200:201]
	s_mov_b32 m0, s9
	s_nop 0
	global_load_lds_dwordx4 v[224:225], off
	v_lshl_add_u64 v[224:225], v[234:235], 0, s[18:19]
	s_mov_b32 m0, s78
	s_nop 0
	global_load_lds_dwordx4 v[224:225], off
	v_lshl_add_u64 v[224:225], v[236:237], 0, s[18:19]
	s_mov_b32 m0, s79
	s_nop 0
	global_load_lds_dwordx4 v[224:225], off
	s_waitcnt vmcnt(8)
	s_waitcnt lgkmcnt(0)
	s_barrier
	s_cbranch_scc1 .LBB0_1293
	v_mov_b32_e32 v202, v1
	v_mov_b32_e32 v224, v209
	s_mov_b64 s[54:55], -1
	v_add_u32_e32 v202, s69, v202
	v_lshlrev_b32_e32 v224, 3, v224
	s_and_b64 vcc, exec, s[38:39]
	v_add_u32_e32 v234, 16, v202
	v_add_u32_e32 v233, 32, v202
	v_add_u32_e32 v232, 48, v202
	s_cbranch_vccz .LBB0_1297
	v_add_u32_e32 v236, s70, v224
	v_ashrrev_i32_e32 v237, 31, v236
	v_mov_b64_e32 v[240:241], s[14:15]
	v_mad_i64_i32 v[238:239], s[8:9], v202, s88, v[240:241]
	v_lshlrev_b64 v[244:245], 1, v[236:237]
	v_lshl_add_u64 v[246:247], v[238:239], 0, v[244:245]
	v_cvt_pk_bf16_f32 v236, v62, v63
	v_cvt_pk_bf16_f32 v237, v64, v65
	v_cvt_pk_bf16_f32 v238, v58, v59
	v_cvt_pk_bf16_f32 v239, v60, v61
	global_store_dwordx4 v[246:247], v[236:239], off
	s_mov_b64 s[54:55], 0
	s_nop 0
	v_cvt_pk_bf16_f32 v236, v30, v31
	v_cvt_pk_bf16_f32 v237, v32, v33
	v_cvt_pk_bf16_f32 v238, v26, v27
	v_cvt_pk_bf16_f32 v239, v28, v29
	global_store_dwordx4 v[246:247], v[236:239], off offset:256
	s_nop 1
	v_mad_i64_i32 v[236:237], s[8:9], v234, s88, v[240:241]
	v_lshl_add_u64 v[246:247], v[236:237], 0, v[244:245]
	v_cvt_pk_bf16_f32 v236, v54, v55
	v_cvt_pk_bf16_f32 v237, v56, v57
	v_cvt_pk_bf16_f32 v238, v50, v51
	v_cvt_pk_bf16_f32 v239, v52, v53
	global_store_dwordx4 v[246:247], v[236:239], off
	s_nop 1
	v_cvt_pk_bf16_f32 v236, v22, v23
	v_cvt_pk_bf16_f32 v237, v24, v25
	v_cvt_pk_bf16_f32 v238, v18, v19
	v_cvt_pk_bf16_f32 v239, v20, v21
	global_store_dwordx4 v[246:247], v[236:239], off offset:256
	s_nop 1
	v_mad_i64_i32 v[236:237], s[8:9], v233, s88, v[240:241]
	v_lshl_add_u64 v[246:247], v[236:237], 0, v[244:245]
	v_cvt_pk_bf16_f32 v236, v46, v47
	v_cvt_pk_bf16_f32 v237, v48, v49
	v_cvt_pk_bf16_f32 v238, v42, v43
	v_cvt_pk_bf16_f32 v239, v44, v45
	global_store_dwordx4 v[246:247], v[236:239], off
	s_nop 1
	v_cvt_pk_bf16_f32 v236, v14, v15
	v_cvt_pk_bf16_f32 v237, v16, v17
	v_cvt_pk_bf16_f32 v238, v10, v11
	v_cvt_pk_bf16_f32 v239, v12, v13
	global_store_dwordx4 v[246:247], v[236:239], off offset:256
	s_nop 1
	v_mad_i64_i32 v[236:237], s[8:9], v232, s88, v[240:241]
	v_lshl_add_u64 v[240:241], v[236:237], 0, v[244:245]
	v_cvt_pk_bf16_f32 v236, v38, v39
	v_cvt_pk_bf16_f32 v237, v40, v41
	v_cvt_pk_bf16_f32 v238, v34, v35
	v_cvt_pk_bf16_f32 v239, v36, v37
	global_store_dwordx4 v[240:241], v[236:239], off
	s_nop 1
	v_cvt_pk_bf16_f32 v236, v6, v7
	v_cvt_pk_bf16_f32 v237, v8, v9
	v_cvt_pk_bf16_f32 v238, v2, v3
	v_cvt_pk_bf16_f32 v239, v4, v5
	global_store_dwordx4 v[240:241], v[236:239], off offset:256

.LBB0_1415:
	s_waitcnt lgkmcnt(7)
	v_mfma_f32_16x16x32_bf16 v[76:79], v[74:77], v[38:41], 0
	v_mov_b32_e32 v75, s41
	v_or_b32_e32 v74, s40, v104
	s_waitcnt lgkmcnt(5)
	v_mfma_f32_16x16x32_bf16 v[66:69], v[66:69], v[38:41], 0
	v_mfma_f32_16x16x32_bf16 v[70:73], v[70:73], v[42:45], v[76:79]
	s_waitcnt lgkmcnt(3)
	v_mfma_f32_16x16x32_bf16 v[58:61], v[58:61], v[38:41], 0
	v_mfma_f32_16x16x32_bf16 v[62:65], v[62:65], v[42:45], v[66:69]
	s_nop 4
	v_add_f32_e32 v80, v143, v70
	v_add_f32_e32 v81, v142, v71
	v_max3_f32 v70, v88, v80, v81
	s_waitcnt lgkmcnt(1)
	v_mfma_f32_16x16x32_bf16 v[50:53], v[50:53], v[38:41], 0
	v_add_f32_e32 v82, v139, v72
	v_add_f32_e32 v83, v138, v73
	v_max3_f32 v70, v70, v82, v83
	v_mfma_f32_16x16x32_bf16 v[54:57], v[54:57], v[42:45], v[58:61]
	v_add_f32_e32 v84, v137, v62
	v_add_f32_e32 v85, v136, v63
	v_max3_f32 v62, v70, v84, v85
	s_waitcnt lgkmcnt(0)
	v_mfma_f32_16x16x32_bf16 v[46:49], v[46:49], v[42:45], v[50:53]
	v_add_f32_e32 v88, v135, v64
	v_add_f32_e32 v89, v134, v65
	v_max3_f32 v62, v62, v88, v89
	v_add_f32_e32 v90, v133, v54
	v_add_f32_e32 v91, v132, v55
	v_max3_f32 v54, v62, v90, v91
	v_add_f32_e32 v92, v131, v56
	v_add_f32_e32 v93, v130, v57
	v_max3_f32 v54, v54, v92, v93
	v_add_f32_e32 v109, v127, v46
	v_add_f32_e32 v126, v126, v47
	v_max3_f32 v46, v54, v109, v126
	v_add_f32_e32 v125, v125, v48
	v_add_f32_e32 v124, v124, v49
	v_max3_f32 v127, v46, v125, v124
	ds_read_b128 v[46:49], v21 offset:27648
	ds_read_b128 v[50:53], v21 offset:27712
	ds_read_b128 v[54:57], v21 offset:29952
	ds_read_b128 v[58:61], v21 offset:30016
	ds_read_b128 v[62:65], v21 offset:32256
	ds_read_b128 v[66:69], v21 offset:32320
	ds_read_b128 v[70:73], v21 offset:34560
	ds_read_b128 v[76:79], v21 offset:34624
	s_waitcnt lgkmcnt(7)
	v_mfma_f32_16x16x32_bf16 v[46:49], v[46:49], v[38:41], 0
	s_waitcnt lgkmcnt(6)
	v_mfma_f32_16x16x32_bf16 v[46:49], v[50:53], v[42:45], v[46:49]
	s_waitcnt lgkmcnt(5)
	v_mfma_f32_16x16x32_bf16 v[50:53], v[54:57], v[38:41], 0
	s_nop 5
	v_add_f32_e32 v21, v123, v46
	v_add_f32_e32 v122, v122, v47
	v_max3_f32 v46, v127, v21, v122
	v_add_f32_e32 v54, v121, v48
	v_add_f32_e32 v55, v120, v49
	v_max3_f32 v56, v46, v54, v55
	s_waitcnt lgkmcnt(4)
	v_mfma_f32_16x16x32_bf16 v[46:49], v[58:61], v[42:45], v[50:53]
	s_waitcnt lgkmcnt(3)
	v_mfma_f32_16x16x32_bf16 v[50:53], v[62:65], v[38:41], 0
	s_waitcnt lgkmcnt(1)
	v_mfma_f32_16x16x32_bf16 v[38:41], v[70:73], v[38:41], 0
	s_nop 3
	v_add_f32_e32 v57, v119, v46
	v_add_f32_e32 v58, v118, v47
	v_max3_f32 v46, v56, v57, v58
	v_add_f32_e32 v56, v117, v48
	v_add_f32_e32 v59, v116, v49
	v_max3_f32 v60, v46, v56, v59
	v_mfma_f32_16x16x32_bf16 v[46:49], v[66:69], v[42:45], v[50:53]
	s_waitcnt lgkmcnt(0)
	v_mfma_f32_16x16x32_bf16 v[38:41], v[76:79], v[42:45], v[38:41]
	s_nop 5
	v_add_f32_e32 v46, v115, v46
	v_add_f32_e32 v47, v114, v47
	v_max3_f32 v50, v60, v46, v47
	v_add_f32_e32 v48, v113, v48
	v_add_f32_e32 v49, v112, v49
	v_max3_f32 v50, v50, v48, v49
	v_add_f32_e32 v38, v206, v38
	v_add_f32_e32 v39, v205, v39
	v_max3_f32 v42, v50, v38, v39
	v_add_f32_e32 v40, v208, v40
	v_add_f32_e32 v41, v207, v41
	v_max3_f32 v42, v42, v40, v41
	ds_bpermute_b32 v43, v101, v42
	v_add_u32_e32 v142, 0xb000, v190
	v_add_u32_e32 v143, 0xd000, v190
	v_add_u32_e32 v144, 0xf000, v190
	s_waitcnt lgkmcnt(0)
	v_max_f32_e32 v43, v43, v43
	v_max_f32_e32 v42, v42, v43
	ds_bpermute_b32 v43, v105, v42
	s_waitcnt lgkmcnt(0)
	v_max_f32_e32 v43, v43, v43
	v_max_f32_e32 v42, v42, v43
	v_sub_f32_e32 v18, v18, v42
	v_sub_f32_e32 v19, v19, v42
	v_exp_f32_e32 v18, v18
	v_sub_f32_e32 v43, v86, v42
	v_exp_f32_e32 v19, v19
	v_sub_f32_e32 v44, v87, v42
	v_exp_f32_e32 v112, v43
	v_sub_f32_e32 v45, v80, v42
	v_exp_f32_e32 v113, v44
	v_sub_f32_e32 v50, v81, v42
	v_exp_f32_e32 v114, v45
	v_add_f32_e32 v43, 0, v18
	v_sub_f32_e32 v51, v82, v42
	v_exp_f32_e32 v115, v50
	v_add_f32_e32 v43, v19, v43
	v_add_f32_e32 v43, v112, v43
	v_exp_f32_e32 v116, v51
	v_sub_f32_e32 v44, v83, v42
	v_add_f32_e32 v43, v113, v43
	v_exp_f32_e32 v117, v44
	v_sub_f32_e32 v44, v84, v42
	v_add_f32_e32 v43, v114, v43
	v_exp_f32_e32 v118, v44
	v_sub_f32_e32 v44, v85, v42
	v_add_f32_e32 v43, v115, v43
	v_exp_f32_e32 v119, v44
	v_sub_f32_e32 v44, v88, v42
	v_add_f32_e32 v43, v116, v43
	v_exp_f32_e32 v120, v44
	v_sub_f32_e32 v44, v89, v42
	v_add_f32_e32 v43, v117, v43
	v_exp_f32_e32 v121, v44
	v_sub_f32_e32 v44, v90, v42
	v_add_f32_e32 v43, v118, v43
	v_exp_f32_e32 v123, v44
	v_sub_f32_e32 v44, v91, v42
	v_add_f32_e32 v43, v119, v43
	v_exp_f32_e32 v127, v44
	v_sub_f32_e32 v44, v92, v42
	v_add_f32_e32 v43, v120, v43
	v_exp_f32_e32 v92, v44
	v_sub_f32_e32 v44, v93, v42
	v_add_f32_e32 v43, v121, v43
	v_exp_f32_e32 v93, v44
	v_sub_f32_e32 v44, v109, v42
	v_add_f32_e32 v43, v123, v43
	v_exp_f32_e32 v109, v44
	v_sub_f32_e32 v44, v126, v42
	v_add_f32_e32 v43, v127, v43
	v_exp_f32_e32 v126, v44
	v_sub_f32_e32 v44, v125, v42
	v_add_f32_e32 v43, v92, v43
	v_exp_f32_e32 v125, v44
	v_sub_f32_e32 v44, v124, v42
	v_add_f32_e32 v43, v93, v43
	v_exp_f32_e32 v124, v44
	v_sub_f32_e32 v21, v21, v42
	v_add_f32_e32 v43, v109, v43
	v_exp_f32_e32 v21, v21
	v_sub_f32_e32 v44, v122, v42
	v_add_f32_e32 v43, v126, v43
	v_exp_f32_e32 v122, v44
	v_sub_f32_e32 v44, v54, v42
	v_add_f32_e32 v43, v125, v43
	v_exp_f32_e32 v128, v44
	v_sub_f32_e32 v44, v55, v42
	v_add_f32_e32 v43, v124, v43
	v_exp_f32_e32 v129, v44
	v_sub_f32_e32 v44, v57, v42
	v_add_f32_e32 v43, v21, v43
	v_exp_f32_e32 v130, v44
	v_sub_f32_e32 v44, v58, v42
	v_add_f32_e32 v43, v122, v43
	v_exp_f32_e32 v131, v44
	v_sub_f32_e32 v44, v56, v42
	v_add_f32_e32 v43, v128, v43
	v_exp_f32_e32 v132, v44
	v_sub_f32_e32 v44, v59, v42
	v_add_f32_e32 v43, v129, v43
	v_exp_f32_e32 v133, v44
	v_sub_f32_e32 v44, v46, v42
	v_add_f32_e32 v43, v130, v43
	v_exp_f32_e32 v134, v44
	v_sub_f32_e32 v44, v47, v42
	v_add_f32_e32 v43, v131, v43
	v_exp_f32_e32 v135, v44
	v_sub_f32_e32 v44, v48, v42
	v_add_f32_e32 v43, v132, v43
	v_exp_f32_e32 v136, v44
	v_sub_f32_e32 v44, v49, v42
	v_add_f32_e32 v43, v133, v43
	v_exp_f32_e32 v137, v44
	v_sub_f32_e32 v38, v38, v42
	v_add_f32_e32 v43, v134, v43
	v_exp_f32_e32 v138, v38
	v_sub_f32_e32 v38, v39, v42
	v_add_f32_e32 v43, v135, v43
	v_exp_f32_e32 v139, v38
	v_sub_f32_e32 v38, v40, v42
	v_add_f32_e32 v43, v136, v43
	v_exp_f32_e32 v140, v38
	v_sub_f32_e32 v38, v41, v42
	v_add_f32_e32 v43, v137, v43
	v_exp_f32_e32 v141, v38
	v_add_f32_e32 v38, v138, v43
	v_add_f32_e32 v38, v139, v38
	v_add_f32_e32 v38, v140, v38
	v_add_f32_e32 v38, v141, v38
	ds_bpermute_b32 v39, v101, v38
	ds_read2_b64 v[46:49], v143 offset0:92 offset1:96
	s_waitcnt lgkmcnt(1)
	v_add_f32_e32 v88, v38, v39
	v_sub_f32_e32 v38, v107, v42
	v_add_u32_e32 v107, 0x9000, v190
	v_exp_f32_e32 v90, v38
	ds_read2_b64 v[38:41], v107 offset0:28 offset1:32
	ds_read2_b64 v[42:45], v142 offset0:60 offset1:64
	ds_read2_b64 v[50:53], v144 offset0:124 offset1:128
	ds_read2_b64 v[54:57], v107 offset0:36 offset1:40
	ds_read2_b64 v[58:61], v142 offset0:68 offset1:72
	ds_read2_b64 v[62:65], v143 offset0:100 offset1:104
	ds_read2_b64 v[66:69], v144 offset0:132 offset1:136
	ds_read2_b64 v[70:73], v107 offset0:44 offset1:48
	ds_read2_b64 v[76:79], v142 offset0:76 offset1:80
	ds_read2_b64 v[80:83], v143 offset0:108 offset1:112
	ds_read2_b64 v[84:87], v144 offset0:140 offset1:144
	ds_bpermute_b32 v89, v105, v88
	s_waitcnt lgkmcnt(0)
	v_add_f32_e32 v88, v88, v89
	v_add_f32_e32 v145, v90, v88
	v_cvt_pk_bf16_f32 v88, v18, v19
	v_cvt_pk_bf16_f32 v89, v112, v113
	v_cvt_pk_bf16_f32 v90, v114, v115
	v_cvt_pk_bf16_f32 v91, v116, v117
	s_nop 0
	v_mfma_f32_16x16x32_bf16 v[38:41], v[38:41], v[88:91], 0
	v_mfma_f32_16x16x32_bf16 v[42:45], v[42:45], v[88:91], 0
	v_mfma_f32_16x16x32_bf16 v[46:49], v[46:49], v[88:91], 0
	v_mfma_f32_16x16x32_bf16 v[50:53], v[50:53], v[88:91], 0
	v_cvt_pk_bf16_f32 v88, v118, v119
	v_cvt_pk_bf16_f32 v89, v120, v121
	v_cvt_pk_bf16_f32 v90, v123, v127
	v_cvt_pk_bf16_f32 v91, v92, v93
	s_nop 0
	v_mfma_f32_16x16x32_bf16 v[38:41], v[54:57], v[88:91], v[38:41]
	v_cvt_pk_bf16_f32 v54, v109, v126
	v_cvt_pk_bf16_f32 v55, v125, v124
	v_cvt_pk_bf16_f32 v56, v21, v122
	v_mfma_f32_16x16x32_bf16 v[42:45], v[58:61], v[88:91], v[42:45]
	v_cvt_pk_bf16_f32 v57, v128, v129
	v_mfma_f32_16x16x32_bf16 v[46:49], v[62:65], v[88:91], v[46:49]
	ds_read2_b64 v[58:61], v107 offset0:52 offset1:56
	ds_read2_b64 v[62:65], v142 offset0:84 offset1:88
	v_mfma_f32_16x16x32_bf16 v[50:53], v[66:69], v[88:91], v[50:53]
	ds_read2_b64 v[66:69], v143 offset0:116 offset1:120
	ds_read2_b64 v[88:91], v144 offset0:148 offset1:152
	ds_read_b64 v[112:113], v190 offset:37344
	s_waitcnt lgkmcnt(0)
	v_mov_b32_e32 v114, v112
	v_mfma_f32_16x16x32_bf16 v[38:41], v[70:73], v[54:57], v[38:41]
	ds_read_b64 v[70:71], v190 offset:45792
	ds_read_b64 v[116:117], v190 offset:54240
	ds_read_b64 v[120:121], v190 offset:62688
	v_mov_b32_e32 v115, v113
	s_waitcnt lgkmcnt(2)
	v_mov_b32_e32 v72, v70
	v_mfma_f32_16x16x32_bf16 v[42:45], v[76:79], v[54:57], v[42:45]
	v_mov_b32_e32 v73, v71
	s_waitcnt lgkmcnt(1)
	v_mov_b32_e32 v118, v116
	v_mov_b32_e32 v119, v117
	v_mfma_f32_16x16x32_bf16 v[46:49], v[80:83], v[54:57], v[46:49]
	s_waitcnt lgkmcnt(0)
	v_mov_b32_e32 v122, v120
	v_mov_b32_e32 v123, v121
	v_mfma_f32_16x16x32_bf16 v[50:53], v[84:87], v[54:57], v[50:53]
	v_cvt_pk_bf16_f32 v54, v130, v131
	v_cvt_pk_bf16_f32 v55, v132, v133
	v_cvt_pk_bf16_f32 v56, v134, v135
	v_cvt_pk_bf16_f32 v57, v136, v137
	v_mov_b32_e32 v21, v20
	v_mfma_f32_16x16x32_bf16 v[38:41], v[58:61], v[54:57], v[38:41]
	v_div_scale_f32 v58, s[24:25], v145, v145, 1.0
	v_rcp_f32_e32 v59, v58
	v_mfma_f32_16x16x32_bf16 v[42:45], v[62:65], v[54:57], v[42:45]
	v_cvt_pk_bf16_f32 v18, v138, v139
	v_cvt_pk_bf16_f32 v19, v140, v141
	v_fma_f32 v60, -v58, v59, 1.0
	v_mfma_f32_16x16x32_bf16 v[46:49], v[66:69], v[54:57], v[46:49]
	v_fmac_f32_e32 v59, v60, v59
	s_mov_b32 s2, s42
	v_mfma_f32_16x16x32_bf16 v[50:53], v[88:91], v[54:57], v[50:53]
	v_div_scale_f32 v54, vcc, 1.0, v145, 1.0
	v_mul_f32_e32 v55, v54, v59
	v_fma_f32 v56, -v58, v55, v54
	v_mfma_f32_16x16x32_bf16 v[38:41], v[112:115], v[18:21], v[38:41]
	v_fmac_f32_e32 v55, v56, v59
	v_fma_f32 v54, -v58, v55, v54
	v_div_fmas_f32 v54, v54, v59, v55
	v_mfma_f32_16x16x32_bf16 v[42:45], v[70:73], v[18:21], v[42:45]
	v_div_fixup_f32 v56, v54, v145, 1.0
	v_lshlrev_b64 v[54:55], 12, v[74:75]
	v_lshl_add_u64 v[54:55], v[110:111], 0, v[54:55]
	v_mfma_f32_16x16x32_bf16 v[46:49], v[116:119], v[18:21], v[46:49]
	s_and_b64 vcc, exec, s[38:39]
	v_mfma_f32_16x16x32_bf16 v[50:53], v[120:123], v[18:21], v[50:53]
	v_mul_f32_e32 v18, v56, v38
	v_mul_f32_e32 v19, v56, v39
	v_cvt_pk_bf16_f32 v18, v18, v19
	v_mul_f32_e32 v19, v56, v40
	v_mul_f32_e32 v21, v56, v41
	v_cvt_pk_bf16_f32 v19, v19, v21
	global_store_dwordx2 v[54:55], v[18:19], off
	v_mul_f32_e32 v18, v56, v42
	v_mul_f32_e32 v19, v56, v43
	v_cvt_pk_bf16_f32 v18, v18, v19
	v_mul_f32_e32 v19, v56, v44
	v_mul_f32_e32 v21, v56, v45
	v_cvt_pk_bf16_f32 v19, v19, v21
	global_store_dwordx2 v[54:55], v[18:19], off offset:32
	v_mul_f32_e32 v18, v56, v46
	v_mul_f32_e32 v19, v56, v47
	v_cvt_pk_bf16_f32 v18, v18, v19
	v_mul_f32_e32 v19, v56, v48
	v_mul_f32_e32 v21, v56, v49
	v_cvt_pk_bf16_f32 v19, v19, v21
	global_store_dwordx2 v[54:55], v[18:19], off offset:64
	v_mul_f32_e32 v18, v56, v50
	v_mul_f32_e32 v19, v56, v51
	v_cvt_pk_bf16_f32 v18, v18, v19
	v_mul_f32_e32 v19, v56, v52
	v_mul_f32_e32 v21, v56, v53
	v_cvt_pk_bf16_f32 v19, v19, v21
	global_store_dwordx2 v[54:55], v[18:19], off offset:96
	s_cbranch_vccnz .LBB0_1473

.LBB0_1449:
	s_waitcnt lgkmcnt(1)
	v_mfma_f32_16x16x32_bf16 v[46:49], v[58:61], v[46:49], 0
	v_add_u32_e32 v209, 0x900, v209
	s_add_i32 s48, s48, 1
	s_waitcnt lgkmcnt(0)
	v_mfma_f32_16x16x32_bf16 v[46:49], v[54:57], v[50:53], v[46:49]
	s_nop 7
	v_add_f32_e32 v46, v206, v46
	v_add_f32_e32 v47, v205, v47
	v_add_f32_e32 v48, v208, v48
	v_max3_f32 v50, v210, v46, v47
	v_add_f32_e32 v49, v207, v49
	v_max3_f32 v50, v50, v48, v49
	ds_bpermute_b32 v51, v101, v50
	v_add_u32_e32 v235, 0x2000, v21
	v_add_u32_e32 v236, 0x4000, v21
	v_add_u32_e32 v237, 0x6000, v21
	s_waitcnt lgkmcnt(0)
	v_max_f32_e32 v51, v51, v51
	v_max_f32_e32 v50, v50, v51
	ds_bpermute_b32 v51, v105, v50
	s_waitcnt lgkmcnt(0)
	v_max_f32_e32 v51, v51, v51
	v_max_f32_e32 v50, v50, v51
	v_sub_f32_e32 v51, v176, v50
	v_sub_f32_e32 v52, v177, v50
	v_exp_f32_e32 v176, v51
	v_sub_f32_e32 v53, v178, v50
	v_exp_f32_e32 v177, v52
	v_sub_f32_e32 v54, v179, v50
	v_exp_f32_e32 v178, v53
	v_sub_f32_e32 v18, v18, v50
	v_exp_f32_e32 v179, v54
	v_sub_f32_e32 v19, v19, v50
	v_exp_f32_e32 v18, v18
	v_add_f32_e32 v51, 0, v176
	v_sub_f32_e32 v55, v88, v50
	v_exp_f32_e32 v19, v19
	v_add_f32_e32 v51, v177, v51
	v_add_f32_e32 v51, v178, v51
	v_exp_f32_e32 v210, v55
	v_sub_f32_e32 v52, v89, v50
	v_add_f32_e32 v51, v179, v51
	v_exp_f32_e32 v211, v52
	v_sub_f32_e32 v52, v90, v50
	v_add_f32_e32 v51, v18, v51
	v_exp_f32_e32 v212, v52
	v_sub_f32_e32 v52, v91, v50
	v_add_f32_e32 v51, v19, v51
	v_exp_f32_e32 v213, v52
	v_sub_f32_e32 v52, v92, v50
	v_add_f32_e32 v51, v210, v51
	v_exp_f32_e32 v214, v52
	v_sub_f32_e32 v52, v93, v50
	v_add_f32_e32 v51, v211, v51
	v_exp_f32_e32 v215, v52
	v_sub_f32_e32 v52, v86, v50
	v_add_f32_e32 v51, v212, v51
	v_exp_f32_e32 v216, v52
	v_sub_f32_e32 v52, v87, v50
	v_add_f32_e32 v51, v213, v51
	v_exp_f32_e32 v217, v52
	v_sub_f32_e32 v52, v182, v50
	v_add_f32_e32 v51, v214, v51
	v_exp_f32_e32 v182, v52
	v_sub_f32_e32 v52, v183, v50
	v_add_f32_e32 v51, v215, v51
	v_exp_f32_e32 v183, v52
	v_sub_f32_e32 v52, v184, v50
	v_add_f32_e32 v51, v216, v51
	v_exp_f32_e32 v184, v52
	v_sub_f32_e32 v52, v185, v50
	v_add_f32_e32 v51, v217, v51
	v_exp_f32_e32 v185, v52
	v_sub_f32_e32 v52, v186, v50
	v_add_f32_e32 v51, v182, v51
	v_exp_f32_e32 v186, v52
	v_sub_f32_e32 v52, v187, v50
	v_add_f32_e32 v51, v183, v51
	v_exp_f32_e32 v187, v52
	v_sub_f32_e32 v52, v180, v50
	v_add_f32_e32 v51, v184, v51
	v_exp_f32_e32 v180, v52
	v_sub_f32_e32 v52, v181, v50
	v_add_f32_e32 v51, v185, v51
	v_exp_f32_e32 v181, v52
	v_sub_f32_e32 v52, v80, v50
	v_add_f32_e32 v51, v186, v51
	v_exp_f32_e32 v218, v52
	v_sub_f32_e32 v52, v81, v50
	v_add_f32_e32 v51, v187, v51
	v_exp_f32_e32 v219, v52
	v_sub_f32_e32 v52, v70, v50
	v_add_f32_e32 v51, v180, v51
	v_exp_f32_e32 v220, v52
	v_sub_f32_e32 v52, v71, v50
	v_add_f32_e32 v51, v181, v51
	v_exp_f32_e32 v221, v52
	v_sub_f32_e32 v52, v72, v50
	v_add_f32_e32 v51, v218, v51
	v_exp_f32_e32 v222, v52
	v_sub_f32_e32 v52, v73, v50
	v_add_f32_e32 v51, v219, v51
	v_exp_f32_e32 v223, v52
	v_sub_f32_e32 v52, v78, v50
	v_add_f32_e32 v51, v220, v51
	v_exp_f32_e32 v224, v52
	v_sub_f32_e32 v52, v79, v50
	v_add_f32_e32 v51, v221, v51
	v_exp_f32_e32 v225, v52
	v_sub_f32_e32 v52, v62, v50
	v_add_f32_e32 v51, v222, v51
	v_exp_f32_e32 v226, v52
	v_sub_f32_e32 v52, v63, v50
	v_add_f32_e32 v51, v223, v51
	v_exp_f32_e32 v227, v52
	v_sub_f32_e32 v46, v46, v50
	v_add_f32_e32 v51, v224, v51
	v_exp_f32_e32 v228, v46
	v_sub_f32_e32 v46, v47, v50
	v_add_f32_e32 v51, v225, v51
	v_exp_f32_e32 v229, v46
	v_sub_f32_e32 v46, v48, v50
	v_add_f32_e32 v51, v226, v51
	v_exp_f32_e32 v230, v46
	v_sub_f32_e32 v46, v49, v50
	v_add_f32_e32 v51, v227, v51
	v_exp_f32_e32 v231, v46
	v_add_f32_e32 v46, v228, v51
	v_add_f32_e32 v46, v229, v46
	v_add_f32_e32 v46, v230, v46
	v_add_f32_e32 v46, v231, v46
	ds_bpermute_b32 v47, v101, v46
	ds_read2_b64 v[54:57], v236 offset0:64 offset1:68
	s_waitcnt lgkmcnt(1)
	v_add_f32_e32 v232, v46, v47
	v_sub_f32_e32 v46, v107, v50
	v_exp_f32_e32 v234, v46
	ds_read2_b64 v[46:49], v21 offset1:4
	ds_read2_b64 v[50:53], v235 offset0:32 offset1:36
	ds_read2_b64 v[58:61], v237 offset0:96 offset1:100
	ds_read2_b64 v[62:65], v21 offset0:8 offset1:12
	ds_read2_b64 v[66:69], v235 offset0:40 offset1:44
	ds_read2_b64 v[70:73], v236 offset0:72 offset1:76
	ds_read2_b64 v[74:77], v237 offset0:104 offset1:108
	ds_read2_b64 v[78:81], v21 offset0:16 offset1:20
	ds_read2_b64 v[82:85], v235 offset0:48 offset1:52
	ds_read2_b64 v[86:89], v236 offset0:80 offset1:84
	ds_read2_b64 v[90:93], v237 offset0:112 offset1:116
	ds_bpermute_b32 v233, v105, v232
	s_waitcnt lgkmcnt(0)
	v_add_f32_e32 v232, v232, v233
	v_add_f32_e32 v232, v234, v232
	v_add_u32_e32 v233, 32, v21
	v_cvt_pk_bf16_f32 v176, v176, v177
	v_cvt_pk_bf16_f32 v177, v178, v179
	v_cvt_pk_bf16_f32 v178, v18, v19
	v_cvt_pk_bf16_f32 v179, v210, v211
	s_nop 0
	v_mfma_f32_16x16x32_bf16 v[46:49], v[46:49], v[176:179], 0
	v_mfma_f32_16x16x32_bf16 v[50:53], v[50:53], v[176:179], 0
	v_mfma_f32_16x16x32_bf16 v[54:57], v[54:57], v[176:179], 0
	v_mfma_f32_16x16x32_bf16 v[58:61], v[58:61], v[176:179], 0
	v_cvt_pk_bf16_f32 v176, v212, v213
	v_cvt_pk_bf16_f32 v177, v214, v215
	v_cvt_pk_bf16_f32 v178, v216, v217
	v_cvt_pk_bf16_f32 v179, v182, v183
	s_nop 0
	v_mfma_f32_16x16x32_bf16 v[46:49], v[62:65], v[176:179], v[46:49]
	v_cvt_pk_bf16_f32 v62, v184, v185
	v_cvt_pk_bf16_f32 v63, v186, v187
	v_cvt_pk_bf16_f32 v64, v180, v181
	v_mfma_f32_16x16x32_bf16 v[50:53], v[66:69], v[176:179], v[50:53]
	v_cvt_pk_bf16_f32 v65, v218, v219
	ds_read2_b64 v[66:69], v21 offset0:24 offset1:28
	v_mfma_f32_16x16x32_bf16 v[54:57], v[70:73], v[176:179], v[54:57]
	v_mfma_f32_16x16x32_bf16 v[58:61], v[74:77], v[176:179], v[58:61]
	v_mfma_f32_16x16x32_bf16 v[46:49], v[78:81], v[62:65], v[46:49]
	ds_read2_b64 v[70:73], v235 offset0:56 offset1:60
	ds_read2_b64 v[74:77], v236 offset0:88 offset1:92
	ds_read2_b64 v[78:81], v237 offset0:120 offset1:124
	v_mfma_f32_16x16x32_bf16 v[50:53], v[82:85], v[62:65], v[50:53]
	v_mfma_f32_16x16x32_bf16 v[54:57], v[86:89], v[62:65], v[54:57]
	ds_read2_b64 v[82:85], v21 offset0:32 offset1:36
	ds_read2_b64 v[86:89], v235 offset0:64 offset1:68
	ds_read2_b64 v[176:179], v236 offset0:96 offset1:100
	ds_read2_b64 v[180:183], v237 offset0:128 offset1:132
	v_mfma_f32_16x16x32_bf16 v[58:61], v[90:93], v[62:65], v[58:61]
	v_cvt_pk_bf16_f32 v62, v220, v221
	v_cvt_pk_bf16_f32 v63, v222, v223
	v_cvt_pk_bf16_f32 v64, v224, v225
	v_cvt_pk_bf16_f32 v65, v226, v227
	v_mov_b32_e32 v21, v20
	s_waitcnt lgkmcnt(7)
	v_mfma_f32_16x16x32_bf16 v[46:49], v[66:69], v[62:65], v[46:49]
	v_div_scale_f32 v66, s[50:51], v232, v232, 1.0
	v_rcp_f32_e32 v67, v66
	s_waitcnt lgkmcnt(6)
	v_mfma_f32_16x16x32_bf16 v[50:53], v[70:73], v[62:65], v[50:53]
	v_cvt_pk_bf16_f32 v18, v228, v229
	v_cvt_pk_bf16_f32 v19, v230, v231
	v_fma_f32 v68, -v66, v67, 1.0
	s_waitcnt lgkmcnt(5)
	v_mfma_f32_16x16x32_bf16 v[54:57], v[74:77], v[62:65], v[54:57]
	v_fmac_f32_e32 v67, v68, v67
	v_lshl_add_u64 v[172:173], v[172:173], 0, 16
	s_cmp_eq_u32 s48, 7
	s_waitcnt lgkmcnt(4)
	v_mfma_f32_16x16x32_bf16 v[58:61], v[78:81], v[62:65], v[58:61]
	v_div_scale_f32 v62, vcc, 1.0, v232, 1.0
	v_mul_f32_e32 v63, v62, v67
	v_fma_f32 v64, -v66, v63, v62
	s_waitcnt lgkmcnt(3)
	v_mfma_f32_16x16x32_bf16 v[46:49], v[82:85], v[18:21], v[46:49]
	v_fmac_f32_e32 v63, v64, v67
	v_fma_f32 v62, -v66, v63, v62
	v_div_fmas_f32 v62, v62, v67, v63
	s_waitcnt lgkmcnt(2)
	v_mfma_f32_16x16x32_bf16 v[50:53], v[86:89], v[18:21], v[50:53]
	v_div_fixup_f32 v64, v62, v232, 1.0
	v_lshlrev_b64 v[62:63], 12, v[174:175]
	v_lshl_add_u64 v[62:63], v[110:111], 0, v[62:63]
	s_waitcnt lgkmcnt(1)
	v_mfma_f32_16x16x32_bf16 v[54:57], v[176:179], v[18:21], v[54:57]
	s_waitcnt lgkmcnt(0)
	v_mfma_f32_16x16x32_bf16 v[58:61], v[180:183], v[18:21], v[58:61]
	v_mul_f32_e32 v18, v64, v46
	v_mul_f32_e32 v19, v64, v47
	v_cvt_pk_bf16_f32 v18, v18, v19
	v_mul_f32_e32 v19, v64, v48
	v_mul_f32_e32 v21, v64, v49
	v_cvt_pk_bf16_f32 v19, v19, v21
	global_store_dwordx2 v[62:63], v[18:19], off
	v_mul_f32_e32 v18, v64, v50
	v_mul_f32_e32 v19, v64, v51
	v_cvt_pk_bf16_f32 v18, v18, v19
	v_mul_f32_e32 v19, v64, v52
	v_mul_f32_e32 v21, v64, v53
	v_cvt_pk_bf16_f32 v19, v19, v21
	global_store_dwordx2 v[62:63], v[18:19], off offset:32
	v_mul_f32_e32 v18, v64, v54
	v_mul_f32_e32 v19, v64, v55
	v_cvt_pk_bf16_f32 v18, v18, v19
	v_mul_f32_e32 v19, v64, v56
	v_mul_f32_e32 v21, v64, v57
	v_cvt_pk_bf16_f32 v19, v19, v21
	global_store_dwordx2 v[62:63], v[18:19], off offset:64
	v_mul_f32_e32 v18, v64, v58
	v_mul_f32_e32 v19, v64, v59
	v_cvt_pk_bf16_f32 v18, v18, v19
	v_mul_f32_e32 v19, v64, v60
	v_mul_f32_e32 v21, v64, v61
	s_waitcnt vmcnt(4)
	v_mov_b64_e32 v[52:53], v[44:45]
	s_waitcnt vmcnt(3)
	v_mov_b64_e32 v[48:49], v[40:41]
	v_cvt_pk_bf16_f32 v19, v19, v21
	v_mov_b32_e32 v21, v233
	v_mov_b64_e32 v[50:51], v[42:43]
	v_mov_b64_e32 v[46:47], v[38:39]
	global_store_dwordx2 v[62:63], v[18:19], off offset:96
	s_cbranch_scc1 .LBB0_1471
.LBB0_1450:
	v_or_b32_e32 v174, s40, v172
	v_mov_b64_e32 v[18:19], s[30:31]
	v_mad_u64_u32 v[18:19], s[24:25], v174, s5, v[18:19]
	v_or_b32_e32 v175, s41, v173
	v_mov_b32_e32 v38, v19
	v_mad_u64_u32 v[38:39], s[24:25], v175, s5, v[38:39]
	v_mov_b32_e32 v19, v38
	v_lshl_add_u64 v[18:19], v[18:19], 0, s[34:35]
	v_lshl_add_u64 v[18:19], v[18:19], 0, v[108:109]
	v_lshl_add_u64 v[38:39], v[18:19], 0, s[36:37]
	v_add_co_u32_e32 v18, vcc, s33, v18
	s_waitcnt vmcnt(1)
	v_and_b32_e32 v59, 0xffff0000, v50
	v_addc_co_u32_e32 v19, vcc, 0, v19, vcc
	global_load_dwordx4 v[42:45], v[18:19], off offset:1024
	s_nop 0
	global_load_dwordx4 v[38:41], v[38:39], off offset:64
	v_lshlrev_b32_e32 v58, 16, v50
	v_lshlrev_b32_e32 v62, 16, v52
	v_and_b32_e32 v63, 0xffff0000, v52
	v_mul_f32_e32 v52, v59, v59
	v_lshlrev_b32_e32 v60, 16, v51
	v_fmac_f32_e32 v52, v58, v58
	v_and_b32_e32 v61, 0xffff0000, v51
	v_fmac_f32_e32 v52, v60, v60
	v_fmac_f32_e32 v52, v61, v61
	v_fmac_f32_e32 v52, v62, v62
	v_lshlrev_b32_e32 v64, 16, v53
	v_fmac_f32_e32 v52, v63, v63
	v_and_b32_e32 v65, 0xffff0000, v53
	v_fmac_f32_e32 v52, v64, v64
	s_waitcnt vmcnt(2)
	v_and_b32_e32 v18, 0xffff0000, v46
	v_lshlrev_b32_e32 v19, 16, v46
	v_fmac_f32_e32 v52, v65, v65
	v_pk_mul_f32 v[50:51], v[18:19], v[18:19]
	v_lshlrev_b32_e32 v53, 16, v47
	v_add_f32_e32 v46, v51, v52
	v_and_b32_e32 v52, 0xffff0000, v47
	v_add_f32_e32 v50, v50, v46
	v_pk_mul_f32 v[46:47], v[52:53], v[52:53]
	v_and_b32_e32 v54, 0xffff0000, v48
	v_add_f32_e32 v47, v47, v50
	v_lshlrev_b32_e32 v55, 16, v48
	v_add_f32_e32 v50, v46, v47
	v_pk_mul_f32 v[46:47], v[54:55], v[54:55]
	v_and_b32_e32 v56, 0xffff0000, v49
	v_add_f32_e32 v47, v47, v50
	v_lshlrev_b32_e32 v57, 16, v49
	v_add_f32_e32 v48, v46, v47
	v_pk_mul_f32 v[46:47], v[56:57], v[56:57]
	s_nop 0
	v_add_f32_e32 v47, v47, v48
	v_add_f32_e32 v46, v46, v47
	ds_bpermute_b32 v47, v101, v46
	s_waitcnt lgkmcnt(0)
	v_add_f32_e32 v46, v46, v47
	ds_bpermute_b32 v47, v105, v46
	s_waitcnt lgkmcnt(0)
	v_add_f32_e32 v46, v46, v47
	v_fmamk_f32 v46, v46, 0x3c800000, v200
	v_mul_f32_e32 v47, 0x4b800000, v46
	v_cmp_gt_f32_e32 vcc, s4, v46
	s_nop 1
	v_cndmask_b32_e32 v46, v46, v47, vcc
	v_rsq_f32_e32 v46, v46
	s_nop 0
	v_mul_f32_e32 v47, 0x45800000, v46
	v_cndmask_b32_e32 v66, v46, v47, vcc
	v_mul_f32_e32 v46, v66, v58
	v_mul_f32_e32 v47, v66, v59
	v_cvt_pk_bf16_f32 v46, v46, v47
	v_mul_f32_e32 v47, v66, v60
	v_mul_f32_e32 v48, v66, v61
	v_cvt_pk_bf16_f32 v47, v47, v48
	v_mul_f32_e32 v48, v66, v62
	v_mul_f32_e32 v49, v66, v63
	v_cvt_pk_bf16_f32 v48, v48, v49
	v_mul_f32_e32 v49, v66, v64
	v_mul_f32_e32 v50, v66, v65
	v_mul_f32_e32 v19, v66, v19
	v_mul_f32_e32 v18, v66, v18
	v_cvt_pk_bf16_f32 v49, v49, v50
	v_cvt_pk_bf16_f32 v50, v19, v18
	v_mul_f32_e32 v18, v66, v53
	v_mul_f32_e32 v19, v66, v52
	v_cvt_pk_bf16_f32 v51, v18, v19
	v_mul_f32_e32 v18, v66, v55
	v_mul_f32_e32 v19, v66, v54
	v_cvt_pk_bf16_f32 v52, v18, v19
	v_mul_f32_e32 v18, v66, v57
	v_mul_f32_e32 v19, v66, v56
	v_cvt_pk_bf16_f32 v53, v18, v19
	ds_read_b128 v[86:89], v209
	ds_read_b128 v[90:93], v209 offset:64
	ds_read_b128 v[78:81], v209 offset:2304
	ds_read_b128 v[82:85], v209 offset:2368
	ds_read_b128 v[70:73], v209 offset:4608
	ds_read_b128 v[74:77], v209 offset:4672
	ds_read_b128 v[62:65], v209 offset:6912
	ds_read_b128 v[66:69], v209 offset:6976
	ds_read_b128 v[54:57], v209 offset:9216
	ds_read_b128 v[58:61], v209 offset:9280
	v_cndmask_b32_e64 v19, 0, 1, s[56:57]
	v_mov_b32_e32 v18, 0xff800000
	v_cmp_ne_u32_e64 s[24:25], 1, v19
	s_andn2_b64 vcc, exec, s[56:57]
	v_mov_b32_e32 v210, v107
	v_mov_b32_e32 v176, 0xff800000
	v_mov_b32_e32 v177, 0xff800000
	v_mov_b32_e32 v178, 0xff800000
	v_mov_b32_e32 v179, 0xff800000
	s_cbranch_vccnz .LBB0_1452
	s_waitcnt lgkmcnt(9)
	v_mfma_f32_16x16x32_bf16 v[86:89], v[86:89], v[46:49], 0
	s_waitcnt lgkmcnt(8)
	v_mfma_f32_16x16x32_bf16 v[86:89], v[90:93], v[50:53], v[86:89]
	s_nop 7
	v_pk_add_f32 v[176:177], v[128:129], v[86:87]
	v_pk_add_f32 v[178:179], v[140:141], v[88:89]
	v_max3_f32 v19, v107, v176, v177
	v_max3_f32 v210, v19, v178, v179

.LBB0_1464:
	s_waitcnt lgkmcnt(7)
	ds_read_b128 v[78:81], v209 offset:11520
	s_waitcnt lgkmcnt(7)
	ds_read_b128 v[82:85], v209 offset:11584
	s_waitcnt lgkmcnt(7)
	ds_read_b128 v[70:73], v209 offset:13824
	s_waitcnt lgkmcnt(7)
	ds_read_b128 v[74:77], v209 offset:13888
	s_waitcnt lgkmcnt(7)
	ds_read_b128 v[62:65], v209 offset:16128
	s_waitcnt lgkmcnt(7)
	ds_read_b128 v[66:69], v209 offset:16192
	s_waitcnt lgkmcnt(6)
	ds_read_b128 v[58:61], v209 offset:18432
	ds_read_b128 v[54:57], v209 offset:18496
	s_cmp_lt_u32 s48, 3
	s_cselect_b64 s[50:51], -1, 0
	s_and_b64 s[50:51], s[54:55], s[50:51]
	s_and_b64 vcc, exec, s[50:51]
	s_cbranch_vccnz .LBB0_1466
	s_waitcnt lgkmcnt(7)
	v_mfma_f32_16x16x32_bf16 v[78:81], v[78:81], v[46:49], 0
	s_waitcnt lgkmcnt(6)
	v_mfma_f32_16x16x32_bf16 v[78:81], v[82:85], v[50:53], v[78:81]
	s_nop 7
	v_pk_add_f32 v[180:181], v[160:161], v[78:79]
	v_pk_add_f32 v[80:81], v[162:163], v[80:81]
	v_max3_f32 v78, v210, v180, v181
	v_max3_f32 v210, v78, v80, v81
	s_branch .LBB0_1467

.LBB0_1471:
	v_and_b32_e32 v50, 0xffff0000, v42
	v_lshlrev_b32_e32 v21, 16, v42
	v_lshlrev_b32_e32 v53, 16, v44
	v_and_b32_e32 v54, 0xffff0000, v44
	v_mul_f32_e32 v44, v50, v50
	v_lshlrev_b32_e32 v51, 16, v43
	v_fmac_f32_e32 v44, v21, v21
	v_and_b32_e32 v52, 0xffff0000, v43
	v_fmac_f32_e32 v44, v51, v51
	v_fmac_f32_e32 v44, v52, v52
	v_fmac_f32_e32 v44, v53, v53
	v_lshlrev_b32_e32 v55, 16, v45
	v_fmac_f32_e32 v44, v54, v54
	v_and_b32_e32 v56, 0xffff0000, v45
	v_fmac_f32_e32 v44, v55, v55
	v_and_b32_e32 v18, 0xffff0000, v38
	v_lshlrev_b32_e32 v19, 16, v38
	v_fmac_f32_e32 v44, v56, v56
	v_pk_mul_f32 v[42:43], v[18:19], v[18:19]
	v_lshlrev_b32_e32 v45, 16, v39
	v_add_f32_e32 v38, v43, v44
	v_and_b32_e32 v44, 0xffff0000, v39
	v_add_f32_e32 v42, v42, v38
	v_pk_mul_f32 v[38:39], v[44:45], v[44:45]
	v_and_b32_e32 v46, 0xffff0000, v40
	v_add_f32_e32 v39, v39, v42
	v_lshlrev_b32_e32 v47, 16, v40
	v_add_f32_e32 v42, v38, v39
	v_pk_mul_f32 v[38:39], v[46:47], v[46:47]
	v_and_b32_e32 v48, 0xffff0000, v41
	v_add_f32_e32 v39, v39, v42
	v_lshlrev_b32_e32 v49, 16, v41
	v_add_f32_e32 v40, v38, v39
	v_pk_mul_f32 v[38:39], v[48:49], v[48:49]
	s_nop 0
	v_add_f32_e32 v39, v39, v40
	v_add_f32_e32 v38, v38, v39
	ds_bpermute_b32 v39, v101, v38
	s_waitcnt lgkmcnt(0)
	v_add_f32_e32 v38, v38, v39
	ds_bpermute_b32 v39, v105, v38
	s_waitcnt lgkmcnt(0)
	v_add_f32_e32 v38, v38, v39
	v_fmamk_f32 v38, v38, 0x3c800000, v200
	v_mul_f32_e32 v39, 0x4b800000, v38
	v_cmp_gt_f32_e32 vcc, s4, v38
	s_nop 1
	v_cndmask_b32_e32 v38, v38, v39, vcc
	v_rsq_f32_e32 v38, v38
	s_nop 0
	v_mul_f32_e32 v39, 0x45800000, v38
	v_cndmask_b32_e32 v57, v38, v39, vcc
	v_mul_f32_e32 v21, v57, v21
	v_mul_f32_e32 v38, v57, v50
	v_cvt_pk_bf16_f32 v38, v21, v38
	v_mul_f32_e32 v21, v57, v51
	v_mul_f32_e32 v39, v57, v52
	v_cvt_pk_bf16_f32 v39, v21, v39
	v_mul_f32_e32 v21, v57, v53
	v_mul_f32_e32 v40, v57, v54
	v_mul_f32_e32 v41, v57, v56
	v_mul_f32_e32 v19, v57, v19
	v_mul_f32_e32 v18, v57, v18
	v_cvt_pk_bf16_f32 v40, v21, v40
	v_mul_f32_e32 v21, v57, v55
	v_cvt_pk_bf16_f32 v41, v21, v41
	v_cvt_pk_bf16_f32 v42, v19, v18
	v_mul_f32_e32 v18, v57, v45
	v_mul_f32_e32 v19, v57, v44
	v_cvt_pk_bf16_f32 v43, v18, v19
	v_mul_f32_e32 v18, v57, v47
	v_mul_f32_e32 v19, v57, v46
	v_add_u32_e32 v21, v188, v191
	v_cvt_pk_bf16_f32 v44, v18, v19
	v_mul_f32_e32 v18, v57, v49
	v_mul_f32_e32 v19, v57, v48
	v_cvt_pk_bf16_f32 v45, v18, v19
	ds_read_b128 v[78:81], v203
	ds_read_b128 v[82:85], v203 offset:64
	ds_read_b128 v[74:77], v203 offset:2304
	ds_read_b128 v[70:73], v203 offset:2368
	ds_read_b128 v[66:69], v21 offset:20736
	ds_read_b128 v[62:65], v21 offset:20800
	ds_read_b128 v[58:61], v21 offset:23040
	ds_read_b128 v[54:57], v21 offset:23104
	ds_read_b128 v[50:53], v21 offset:25344
	ds_read_b128 v[46:49], v21 offset:25408
	v_mov_b32_e32 v18, 0xff800000
	s_and_b64 vcc, exec, s[24:25]
	v_mov_b32_e32 v88, v107
	v_mov_b32_e32 v19, 0xff800000
	v_mov_b32_e32 v86, 0xff800000
	v_mov_b32_e32 v87, 0xff800000
	s_cbranch_vccnz .LBB0_1415
	s_waitcnt lgkmcnt(9)
	v_mfma_f32_16x16x32_bf16 v[78:81], v[78:81], v[38:41], 0
	s_waitcnt lgkmcnt(8)
	v_mfma_f32_16x16x32_bf16 v[78:81], v[82:85], v[42:45], v[78:81]
	s_nop 7
	v_pk_add_f32 v[18:19], v[128:129], v[78:79]
	v_pk_add_f32 v[86:87], v[140:141], v[80:81]
	v_max3_f32 v78, v107, v18, v19
	v_max3_f32 v88, v78, v86, v87
	s_branch .LBB0_1415

.LBB0_1547:
	ds_read_b128 v[134:137], v189
	ds_read_b128 v[138:141], v189 offset:1024
	ds_read_b128 v[142:145], v189 offset:2048
	ds_read_b128 v[146:149], v189 offset:3072
	ds_read_b128 v[150:153], v190
	ds_read_b128 v[170:173], v190 offset:1024
	ds_read_b128 v[174:177], v190 offset:2048
	ds_read_b128 v[194:197], v190 offset:3072
	s_add_u32 s2, s66, s54
	s_addc_u32 s69, s67, s55
	s_add_u32 s56, s54, 0x100
	s_addc_u32 s57, s55, 0
	s_cmp_eq_u32 s68, 28
	s_cselect_b64 s[60:61], -1, 0
	s_and_b64 s[58:59], s[60:61], exec
	s_cselect_b32 s59, s31, s69
	s_cselect_b32 s58, s35, s2
	s_cselect_b32 s2, 0, s56
	v_lshl_add_u64 v[178:179], v[130:131], 0, s[54:55]
	s_add_i32 m0, s13, 0xc000
	ds_read_b128 v[198:201], v191
	ds_read_b128 v[202:205], v191 offset:1024
	ds_read_b128 v[206:209], v191 offset:2048
	ds_read_b128 v[210:213], v191 offset:3072
	ds_read_b128 v[214:217], v191 offset:4096
	ds_read_b128 v[218:221], v191 offset:5120
	ds_read_b128 v[222:225], v191 offset:6144
	ds_read_b128 v[226:229], v191 offset:7168
	global_load_lds_dwordx4 v[178:179], off
	v_lshl_add_u64 v[178:179], v[132:133], 0, s[54:55]
	s_add_i32 m0, s13, 0xe000
	s_nop 0
	global_load_lds_dwordx4 v[178:179], off
	s_waitcnt vmcnt(8)
	s_waitcnt lgkmcnt(0)
	s_barrier
	s_waitcnt lgkmcnt(0)
	v_mfma_f32_16x16x32_bf16 v[126:129], v[134:137], v[198:201], v[126:129]
	v_mfma_f32_16x16x32_bf16 v[122:125], v[142:145], v[198:201], v[122:125]
	v_mfma_f32_16x16x32_bf16 v[110:113], v[134:137], v[206:209], v[110:113]
	v_mfma_f32_16x16x32_bf16 v[106:109], v[142:145], v[206:209], v[106:109]
	v_mfma_f32_16x16x32_bf16 v[94:97], v[134:137], v[214:217], v[94:97]
	v_mfma_f32_16x16x32_bf16 v[90:93], v[142:145], v[214:217], v[90:93]
	v_mfma_f32_16x16x32_bf16 v[78:81], v[134:137], v[222:225], v[78:81]
	v_mfma_f32_16x16x32_bf16 v[74:77], v[142:145], v[222:225], v[74:77]
	v_mfma_f32_16x16x32_bf16 v[126:129], v[138:141], v[202:205], v[126:129]
	v_mfma_f32_16x16x32_bf16 v[122:125], v[146:149], v[202:205], v[122:125]
	v_mfma_f32_16x16x32_bf16 v[110:113], v[138:141], v[210:213], v[110:113]
	v_mfma_f32_16x16x32_bf16 v[106:109], v[146:149], v[210:213], v[106:109]
	v_mfma_f32_16x16x32_bf16 v[94:97], v[138:141], v[218:221], v[94:97]
	v_mfma_f32_16x16x32_bf16 v[90:93], v[146:149], v[218:221], v[90:93]
	v_mfma_f32_16x16x32_bf16 v[78:81], v[138:141], v[226:229], v[78:81]
	v_mfma_f32_16x16x32_bf16 v[74:77], v[146:149], v[226:229], v[74:77]
	v_mfma_f32_16x16x32_bf16 v[118:121], v[150:153], v[198:201], v[118:121]
	v_mfma_f32_16x16x32_bf16 v[114:117], v[174:177], v[198:201], v[114:117]
	v_mfma_f32_16x16x32_bf16 v[102:105], v[150:153], v[206:209], v[102:105]
	v_mfma_f32_16x16x32_bf16 v[98:101], v[174:177], v[206:209], v[98:101]
	v_mfma_f32_16x16x32_bf16 v[86:89], v[150:153], v[214:217], v[86:89]
	v_mfma_f32_16x16x32_bf16 v[82:85], v[174:177], v[214:217], v[82:85]
	v_mfma_f32_16x16x32_bf16 v[70:73], v[150:153], v[222:225], v[70:73]
	v_mfma_f32_16x16x32_bf16 v[66:69], v[174:177], v[222:225], v[66:69]
	v_mfma_f32_16x16x32_bf16 v[118:121], v[170:173], v[202:205], v[118:121]
	v_mfma_f32_16x16x32_bf16 v[114:117], v[194:197], v[202:205], v[114:117]
	v_mfma_f32_16x16x32_bf16 v[102:105], v[170:173], v[210:213], v[102:105]
	v_mfma_f32_16x16x32_bf16 v[98:101], v[194:197], v[210:213], v[98:101]
	v_mfma_f32_16x16x32_bf16 v[86:89], v[170:173], v[218:221], v[86:89]
	v_mfma_f32_16x16x32_bf16 v[82:85], v[194:197], v[218:221], v[82:85]
	v_mfma_f32_16x16x32_bf16 v[70:73], v[170:173], v[226:229], v[70:73]
	v_mfma_f32_16x16x32_bf16 v[66:69], v[194:197], v[226:229], v[66:69]
	s_barrier
	s_add_i32 s54, s63, s42
	v_lshl_add_u64 v[178:179], s[58:59], 0, v[156:157]
	s_mov_b32 m0, s54
	ds_read_b128 v[198:201], v191 offset:16384
	ds_read_b128 v[202:205], v191 offset:17408
	ds_read_b128 v[206:209], v191 offset:18432
	ds_read_b128 v[210:213], v191 offset:19456
	ds_read_b128 v[214:217], v191 offset:20480
	ds_read_b128 v[218:221], v191 offset:21504
	ds_read_b128 v[222:225], v191 offset:22528
	ds_read_b128 v[226:229], v191 offset:23552
	global_load_lds_dwordx4 v[178:179], off
	s_add_i32 m0, s54, 0x2000
	s_add_u32 s54, s58, 0x80000
	v_lshl_add_u64 v[182:183], s[58:59], 0, v[160:161]
	s_addc_u32 s55, s59, 0
	s_add_i32 s69, s64, s42
	global_load_lds_dwordx4 v[182:183], off
	v_lshl_add_u64 v[186:187], s[54:55], 0, v[156:157]
	s_mov_b32 m0, s69
	s_nop 0
	global_load_lds_dwordx4 v[186:187], off
	v_lshl_add_u64 v[186:187], s[54:55], 0, v[160:161]
	s_add_i32 m0, s69, 0x2000
	s_and_b64 s[54:55], s[8:9], s[60:61]
	s_and_b64 s[54:55], s[54:55], exec
	s_cselect_b32 s54, s36, s40
	s_cselect_b32 s55, s37, s41
	s_add_u32 s54, s54, s2
	s_addc_u32 s55, s55, 0
	global_load_lds_dwordx4 v[186:187], off
	v_lshl_add_u64 v[186:187], s[54:55], 0, v[154:155]
	s_mov_b32 m0, s13
	v_lshl_add_u64 v[230:231], s[54:55], 0, v[158:159]
	global_load_lds_dwordx4 v[186:187], off
	s_mov_b32 m0, s43
	s_nop 0
	global_load_lds_dwordx4 v[230:231], off
	s_waitcnt vmcnt(8)
	s_waitcnt lgkmcnt(0)
	s_barrier
	s_waitcnt lgkmcnt(0)
	v_mfma_f32_16x16x32_bf16 v[62:65], v[134:137], v[198:201], v[62:65]
	v_mfma_f32_16x16x32_bf16 v[58:61], v[142:145], v[198:201], v[58:61]
	v_mfma_f32_16x16x32_bf16 v[46:49], v[134:137], v[206:209], v[46:49]
	v_mfma_f32_16x16x32_bf16 v[42:45], v[142:145], v[206:209], v[42:45]
	v_mfma_f32_16x16x32_bf16 v[30:33], v[134:137], v[214:217], v[30:33]
	v_mfma_f32_16x16x32_bf16 v[26:29], v[142:145], v[214:217], v[26:29]
	v_mfma_f32_16x16x32_bf16 v[14:17], v[134:137], v[222:225], v[14:17]
	v_mfma_f32_16x16x32_bf16 v[10:13], v[142:145], v[222:225], v[10:13]
	v_mfma_f32_16x16x32_bf16 v[62:65], v[138:141], v[202:205], v[62:65]
	v_mfma_f32_16x16x32_bf16 v[58:61], v[146:149], v[202:205], v[58:61]
	v_mfma_f32_16x16x32_bf16 v[46:49], v[138:141], v[210:213], v[46:49]
	v_mfma_f32_16x16x32_bf16 v[42:45], v[146:149], v[210:213], v[42:45]
	v_mfma_f32_16x16x32_bf16 v[30:33], v[138:141], v[218:221], v[30:33]
	v_mfma_f32_16x16x32_bf16 v[26:29], v[146:149], v[218:221], v[26:29]
	v_mfma_f32_16x16x32_bf16 v[14:17], v[138:141], v[226:229], v[14:17]
	v_mfma_f32_16x16x32_bf16 v[10:13], v[146:149], v[226:229], v[10:13]
	v_mfma_f32_16x16x32_bf16 v[54:57], v[150:153], v[198:201], v[54:57]
	v_mfma_f32_16x16x32_bf16 v[50:53], v[174:177], v[198:201], v[50:53]
	v_mfma_f32_16x16x32_bf16 v[38:41], v[150:153], v[206:209], v[38:41]
	v_mfma_f32_16x16x32_bf16 v[34:37], v[174:177], v[206:209], v[34:37]
	v_mfma_f32_16x16x32_bf16 v[22:25], v[150:153], v[214:217], v[22:25]
	v_mfma_f32_16x16x32_bf16 v[18:21], v[174:177], v[214:217], v[18:21]
	v_mfma_f32_16x16x32_bf16 v[6:9], v[150:153], v[222:225], v[6:9]
	v_mfma_f32_16x16x32_bf16 v[2:5], v[174:177], v[222:225], v[2:5]
	v_mfma_f32_16x16x32_bf16 v[54:57], v[170:173], v[202:205], v[54:57]
	v_mfma_f32_16x16x32_bf16 v[50:53], v[194:197], v[202:205], v[50:53]
	v_mfma_f32_16x16x32_bf16 v[38:41], v[170:173], v[210:213], v[38:41]
	v_mfma_f32_16x16x32_bf16 v[34:37], v[194:197], v[210:213], v[34:37]
	v_mfma_f32_16x16x32_bf16 v[22:25], v[170:173], v[218:221], v[22:25]
	v_mfma_f32_16x16x32_bf16 v[18:21], v[194:197], v[218:221], v[18:21]
	v_mfma_f32_16x16x32_bf16 v[6:9], v[170:173], v[226:229], v[6:9]
	v_mfma_f32_16x16x32_bf16 v[2:5], v[194:197], v[226:229], v[2:5]
	s_barrier
	s_add_i32 s2, 0, 0x18000
	s_add_i32 s60, 0, 0x1c000
	v_add_u32_e32 v146, s2, v181
	v_add_u32_e32 v180, s60, v181
	ds_read_b128 v[134:137], v146
	ds_read_b128 v[138:141], v146 offset:1024
	ds_read_b128 v[142:145], v146 offset:2048
	ds_read_b128 v[146:149], v146 offset:3072
	ds_read_b128 v[150:153], v180
	ds_read_b128 v[170:173], v180 offset:1024
	ds_read_b128 v[174:177], v180 offset:2048
	ds_read_b128 v[194:197], v180 offset:3072
	s_add_u32 s54, s54, 0x80000
	s_addc_u32 s55, s55, 0
	s_mov_b32 m0, s48
	v_lshl_add_u64 v[232:233], s[54:55], 0, v[154:155]
	ds_read_b128 v[198:201], v191 offset:32768
	ds_read_b128 v[202:205], v191 offset:33792
	ds_read_b128 v[206:209], v191 offset:34816
	ds_read_b128 v[210:213], v191 offset:35840
	ds_read_b128 v[214:217], v191 offset:36864
	ds_read_b128 v[218:221], v191 offset:37888
	ds_read_b128 v[222:225], v191 offset:38912
	ds_read_b128 v[226:229], v191 offset:39936
	global_load_lds_dwordx4 v[232:233], off
	v_lshl_add_u64 v[232:233], s[54:55], 0, v[158:159]
	s_mov_b32 m0, s49
	s_nop 0
	global_load_lds_dwordx4 v[232:233], off
	s_waitcnt vmcnt(8)
	s_waitcnt lgkmcnt(0)
	s_barrier
	s_waitcnt lgkmcnt(0)
	v_mfma_f32_16x16x32_bf16 v[126:129], v[134:137], v[198:201], v[126:129]
	v_mfma_f32_16x16x32_bf16 v[122:125], v[142:145], v[198:201], v[122:125]
	v_mfma_f32_16x16x32_bf16 v[110:113], v[134:137], v[206:209], v[110:113]
	v_mfma_f32_16x16x32_bf16 v[106:109], v[142:145], v[206:209], v[106:109]
	v_mfma_f32_16x16x32_bf16 v[94:97], v[134:137], v[214:217], v[94:97]
	v_mfma_f32_16x16x32_bf16 v[90:93], v[142:145], v[214:217], v[90:93]
	v_mfma_f32_16x16x32_bf16 v[78:81], v[134:137], v[222:225], v[78:81]
	v_mfma_f32_16x16x32_bf16 v[74:77], v[142:145], v[222:225], v[74:77]
	v_mfma_f32_16x16x32_bf16 v[126:129], v[138:141], v[202:205], v[126:129]
	v_mfma_f32_16x16x32_bf16 v[122:125], v[146:149], v[202:205], v[122:125]
	v_mfma_f32_16x16x32_bf16 v[110:113], v[138:141], v[210:213], v[110:113]
	v_mfma_f32_16x16x32_bf16 v[106:109], v[146:149], v[210:213], v[106:109]
	v_mfma_f32_16x16x32_bf16 v[94:97], v[138:141], v[218:221], v[94:97]
	v_mfma_f32_16x16x32_bf16 v[90:93], v[146:149], v[218:221], v[90:93]
	v_mfma_f32_16x16x32_bf16 v[78:81], v[138:141], v[226:229], v[78:81]
	v_mfma_f32_16x16x32_bf16 v[74:77], v[146:149], v[226:229], v[74:77]
	v_mfma_f32_16x16x32_bf16 v[118:121], v[150:153], v[198:201], v[118:121]
	v_mfma_f32_16x16x32_bf16 v[114:117], v[174:177], v[198:201], v[114:117]
	v_mfma_f32_16x16x32_bf16 v[102:105], v[150:153], v[206:209], v[102:105]
	v_mfma_f32_16x16x32_bf16 v[98:101], v[174:177], v[206:209], v[98:101]
	v_mfma_f32_16x16x32_bf16 v[86:89], v[150:153], v[214:217], v[86:89]
	v_mfma_f32_16x16x32_bf16 v[82:85], v[174:177], v[214:217], v[82:85]
	v_mfma_f32_16x16x32_bf16 v[70:73], v[150:153], v[222:225], v[70:73]
	v_mfma_f32_16x16x32_bf16 v[66:69], v[174:177], v[222:225], v[66:69]
	v_mfma_f32_16x16x32_bf16 v[118:121], v[170:173], v[202:205], v[118:121]
	v_mfma_f32_16x16x32_bf16 v[114:117], v[194:197], v[202:205], v[114:117]
	v_mfma_f32_16x16x32_bf16 v[102:105], v[170:173], v[210:213], v[102:105]
	v_mfma_f32_16x16x32_bf16 v[98:101], v[194:197], v[210:213], v[98:101]
	v_mfma_f32_16x16x32_bf16 v[86:89], v[170:173], v[218:221], v[86:89]
	v_mfma_f32_16x16x32_bf16 v[82:85], v[194:197], v[218:221], v[82:85]
	v_mfma_f32_16x16x32_bf16 v[70:73], v[170:173], v[226:229], v[70:73]
	v_mfma_f32_16x16x32_bf16 v[66:69], v[194:197], v[226:229], v[66:69]
	s_barrier
	s_add_i32 s2, s2, s42
	v_lshl_add_u64 v[178:179], v[178:179], 0, s[26:27]
	s_mov_b32 m0, s2
	ds_read_b128 v[198:201], v191 offset:49152
	ds_read_b128 v[202:205], v191 offset:50176
	ds_read_b128 v[206:209], v191 offset:51200
	ds_read_b128 v[210:213], v191 offset:52224
	ds_read_b128 v[214:217], v191 offset:53248
	ds_read_b128 v[218:221], v191 offset:54272
	ds_read_b128 v[222:225], v191 offset:55296
	ds_read_b128 v[226:229], v191 offset:56320
	global_load_lds_dwordx4 v[178:179], off
	s_add_i32 m0, s2, 0x2000
	s_add_u32 s54, s58, 0x80080
	v_lshl_add_u64 v[178:179], v[182:183], 0, s[26:27]
	s_addc_u32 s55, s59, 0
	s_add_i32 s2, s60, s42
	global_load_lds_dwordx4 v[178:179], off
	v_lshl_add_u64 v[178:179], s[54:55], 0, v[156:157]
	s_mov_b32 m0, s2
	s_nop 0
	global_load_lds_dwordx4 v[178:179], off
	v_lshl_add_u64 v[178:179], s[54:55], 0, v[160:161]
	s_add_i32 m0, s2, 0x2000
	s_nop 0
	global_load_lds_dwordx4 v[178:179], off
	v_lshl_add_u64 v[178:179], v[186:187], 0, s[26:27]
	s_mov_b32 m0, s51
	s_nop 0
	global_load_lds_dwordx4 v[178:179], off
	v_lshl_add_u64 v[178:179], v[230:231], 0, s[26:27]
	s_mov_b32 m0, s52
	s_nop 0
	global_load_lds_dwordx4 v[178:179], off
	s_waitcnt vmcnt(8)
	s_waitcnt lgkmcnt(0)
	s_barrier
	s_waitcnt lgkmcnt(0)
	v_mfma_f32_16x16x32_bf16 v[62:65], v[134:137], v[198:201], v[62:65]
	v_mfma_f32_16x16x32_bf16 v[58:61], v[142:145], v[198:201], v[58:61]
	v_mfma_f32_16x16x32_bf16 v[46:49], v[134:137], v[206:209], v[46:49]
	v_mfma_f32_16x16x32_bf16 v[42:45], v[142:145], v[206:209], v[42:45]
	v_mfma_f32_16x16x32_bf16 v[30:33], v[134:137], v[214:217], v[30:33]
	v_mfma_f32_16x16x32_bf16 v[26:29], v[142:145], v[214:217], v[26:29]
	v_mfma_f32_16x16x32_bf16 v[14:17], v[134:137], v[222:225], v[14:17]
	v_mfma_f32_16x16x32_bf16 v[10:13], v[142:145], v[222:225], v[10:13]
	v_mfma_f32_16x16x32_bf16 v[62:65], v[138:141], v[202:205], v[62:65]
	v_mfma_f32_16x16x32_bf16 v[58:61], v[146:149], v[202:205], v[58:61]
	v_mfma_f32_16x16x32_bf16 v[46:49], v[138:141], v[210:213], v[46:49]
	v_mfma_f32_16x16x32_bf16 v[42:45], v[146:149], v[210:213], v[42:45]
	v_mfma_f32_16x16x32_bf16 v[30:33], v[138:141], v[218:221], v[30:33]
	v_mfma_f32_16x16x32_bf16 v[26:29], v[146:149], v[218:221], v[26:29]
	v_mfma_f32_16x16x32_bf16 v[14:17], v[138:141], v[226:229], v[14:17]
	v_mfma_f32_16x16x32_bf16 v[10:13], v[146:149], v[226:229], v[10:13]
	v_mfma_f32_16x16x32_bf16 v[54:57], v[150:153], v[198:201], v[54:57]
	v_mfma_f32_16x16x32_bf16 v[50:53], v[174:177], v[198:201], v[50:53]
	v_mfma_f32_16x16x32_bf16 v[38:41], v[150:153], v[206:209], v[38:41]
	v_mfma_f32_16x16x32_bf16 v[34:37], v[174:177], v[206:209], v[34:37]
	v_mfma_f32_16x16x32_bf16 v[22:25], v[150:153], v[214:217], v[22:25]
	v_mfma_f32_16x16x32_bf16 v[18:21], v[174:177], v[214:217], v[18:21]
	v_mfma_f32_16x16x32_bf16 v[6:9], v[150:153], v[222:225], v[6:9]
	v_mfma_f32_16x16x32_bf16 v[2:5], v[174:177], v[222:225], v[2:5]
	v_mfma_f32_16x16x32_bf16 v[54:57], v[170:173], v[202:205], v[54:57]
	v_mfma_f32_16x16x32_bf16 v[50:53], v[194:197], v[202:205], v[50:53]
	v_mfma_f32_16x16x32_bf16 v[38:41], v[170:173], v[210:213], v[38:41]
	v_mfma_f32_16x16x32_bf16 v[34:37], v[194:197], v[210:213], v[34:37]
	v_mfma_f32_16x16x32_bf16 v[22:25], v[170:173], v[218:221], v[22:25]
	v_mfma_f32_16x16x32_bf16 v[18:21], v[194:197], v[218:221], v[18:21]
	v_mfma_f32_16x16x32_bf16 v[6:9], v[170:173], v[226:229], v[6:9]
	v_mfma_f32_16x16x32_bf16 v[2:5], v[194:197], v[226:229], v[2:5]
	s_barrier
	s_add_i32 s68, s68, 2
	s_cmp_gt_u32 s68, 29
	s_mov_b64 s[54:55], s[56:57]
	s_cbranch_scc0 .LBB0_1547
	s_and_b64 vcc, exec, s[28:29]
	s_cbranch_vccz .LBB0_1550
	s_barrier

.LBB0_1936:
	s_waitcnt lgkmcnt(0)
	v_mfma_f32_16x16x32_bf16 v[126:129], v[146:149], v[186:189], v[126:129]
	v_mfma_f32_16x16x32_bf16 v[122:125], v[154:157], v[186:189], v[122:125]
	v_mfma_f32_16x16x32_bf16 v[110:113], v[146:149], v[178:181], v[110:113]
	v_mfma_f32_16x16x32_bf16 v[106:109], v[154:157], v[178:181], v[106:109]
	v_mfma_f32_16x16x32_bf16 v[94:97], v[146:149], v[170:173], v[94:97]
	v_mfma_f32_16x16x32_bf16 v[90:93], v[154:157], v[170:173], v[90:93]
	v_mfma_f32_16x16x32_bf16 v[22:25], v[146:149], v[162:165], v[22:25]
	v_mfma_f32_16x16x32_bf16 v[10:13], v[154:157], v[162:165], v[10:13]
	v_mfma_f32_16x16x32_bf16 v[126:129], v[150:153], v[190:193], v[126:129]
	v_mfma_f32_16x16x32_bf16 v[122:125], v[158:161], v[190:193], v[122:125]
	v_mfma_f32_16x16x32_bf16 v[110:113], v[150:153], v[182:185], v[110:113]
	v_mfma_f32_16x16x32_bf16 v[106:109], v[158:161], v[182:185], v[106:109]
	v_mfma_f32_16x16x32_bf16 v[94:97], v[150:153], v[174:177], v[94:97]
	v_mfma_f32_16x16x32_bf16 v[90:93], v[158:161], v[174:177], v[90:93]
	v_mfma_f32_16x16x32_bf16 v[22:25], v[150:153], v[166:169], v[22:25]
	v_mfma_f32_16x16x32_bf16 v[10:13], v[158:161], v[166:169], v[10:13]
	v_mfma_f32_16x16x32_bf16 v[118:121], v[130:133], v[186:189], v[118:121]
	v_mfma_f32_16x16x32_bf16 v[114:117], v[138:141], v[186:189], v[114:117]
	v_mfma_f32_16x16x32_bf16 v[102:105], v[130:133], v[178:181], v[102:105]
	v_mfma_f32_16x16x32_bf16 v[98:101], v[138:141], v[178:181], v[98:101]
	v_mfma_f32_16x16x32_bf16 v[38:41], v[130:133], v[170:173], v[38:41]
	v_mfma_f32_16x16x32_bf16 v[26:29], v[138:141], v[170:173], v[26:29]
	v_mfma_f32_16x16x32_bf16 v[6:9], v[130:133], v[162:165], v[6:9]
	v_mfma_f32_16x16x32_bf16 v[2:5], v[138:141], v[162:165], v[2:5]
	v_mfma_f32_16x16x32_bf16 v[118:121], v[134:137], v[190:193], v[118:121]
	v_mfma_f32_16x16x32_bf16 v[114:117], v[142:145], v[190:193], v[114:117]
	v_mfma_f32_16x16x32_bf16 v[102:105], v[134:137], v[182:185], v[102:105]
	v_mfma_f32_16x16x32_bf16 v[98:101], v[142:145], v[182:185], v[98:101]
	v_mfma_f32_16x16x32_bf16 v[38:41], v[134:137], v[174:177], v[38:41]
	v_mfma_f32_16x16x32_bf16 v[26:29], v[142:145], v[174:177], v[26:29]
	v_mfma_f32_16x16x32_bf16 v[6:9], v[134:137], v[166:169], v[6:9]
	v_mfma_f32_16x16x32_bf16 v[2:5], v[142:145], v[166:169], v[2:5]
	s_barrier
	s_add_i32 s2, s89, 2
	s_cmp_gt_u32 s89, 5
	s_mov_b32 s89, s2
	s_cbranch_scc1 .LBB0_1956

.LBB0_1954:
	s_lshl_b32 s2, s89, 7
	v_add_u32_e32 v142, s82, v205
	v_add_u32_e32 v158, s83, v205
	s_add_u32 s66, s40, s2
	ds_read_b128 v[130:133], v142
	ds_read_b128 v[134:137], v142 offset:1024
	ds_read_b128 v[138:141], v142 offset:2048
	ds_read_b128 v[142:145], v142 offset:3072
	ds_read_b128 v[146:149], v158
	ds_read_b128 v[150:153], v158 offset:1024
	ds_read_b128 v[154:157], v158 offset:2048
	ds_read_b128 v[158:161], v158 offset:3072
	s_addc_u32 s67, s41, 0
	s_add_u32 s68, s66, 0x100
	s_addc_u32 s69, s67, 0
	s_and_b64 s[66:67], s[62:63], exec
	s_cselect_b32 s67, s37, s69
	s_cselect_b32 s66, s85, s68
	s_add_i32 s70, s2, 0x100
	s_and_b64 s[68:69], s[62:63], exec
	s_cselect_b32 s70, 0, s70
	s_add_u32 s2, s38, s2
	s_addc_u32 s69, s39, 0
	s_add_u32 s68, s2, 0x20080
	s_addc_u32 s69, s69, 0
	v_lshl_add_u64 v[210:211], s[68:69], 0, v[194:195]
	s_add_i32 m0, s50, 0xc000
	ds_read_b128 v[162:165], v209
	ds_read_b128 v[166:169], v209 offset:1024
	ds_read_b128 v[170:173], v209 offset:2048
	ds_read_b128 v[174:177], v209 offset:3072
	ds_read_b128 v[178:181], v209 offset:4096
	ds_read_b128 v[182:185], v209 offset:5120
	ds_read_b128 v[186:189], v209 offset:6144
	ds_read_b128 v[190:193], v209 offset:7168
	global_load_lds_dwordx4 v[210:211], off
	v_lshl_add_u64 v[210:211], s[68:69], 0, v[198:199]
	s_add_i32 m0, s50, 0xe000
	s_nop 0
	global_load_lds_dwordx4 v[210:211], off
	s_waitcnt vmcnt(8)
	s_waitcnt lgkmcnt(0)
	s_barrier
	s_waitcnt lgkmcnt(0)
	v_mfma_f32_16x16x32_bf16 v[86:89], v[130:133], v[162:165], v[86:89]
	v_mfma_f32_16x16x32_bf16 v[82:85], v[138:141], v[162:165], v[82:85]
	v_mfma_f32_16x16x32_bf16 v[78:81], v[130:133], v[170:173], v[78:81]
	v_mfma_f32_16x16x32_bf16 v[74:77], v[138:141], v[170:173], v[74:77]
	v_mfma_f32_16x16x32_bf16 v[70:73], v[130:133], v[178:181], v[70:73]
	v_mfma_f32_16x16x32_bf16 v[66:69], v[138:141], v[178:181], v[66:69]
	v_mfma_f32_16x16x32_bf16 v[62:65], v[130:133], v[186:189], v[62:65]
	v_mfma_f32_16x16x32_bf16 v[58:61], v[138:141], v[186:189], v[58:61]
	v_mfma_f32_16x16x32_bf16 v[86:89], v[134:137], v[166:169], v[86:89]
	v_mfma_f32_16x16x32_bf16 v[82:85], v[142:145], v[166:169], v[82:85]
	v_mfma_f32_16x16x32_bf16 v[78:81], v[134:137], v[174:177], v[78:81]
	v_mfma_f32_16x16x32_bf16 v[74:77], v[142:145], v[174:177], v[74:77]
	v_mfma_f32_16x16x32_bf16 v[70:73], v[134:137], v[182:185], v[70:73]
	v_mfma_f32_16x16x32_bf16 v[66:69], v[142:145], v[182:185], v[66:69]
	v_mfma_f32_16x16x32_bf16 v[62:65], v[134:137], v[190:193], v[62:65]
	v_mfma_f32_16x16x32_bf16 v[58:61], v[142:145], v[190:193], v[58:61]
	v_mfma_f32_16x16x32_bf16 v[54:57], v[146:149], v[162:165], v[54:57]
	v_mfma_f32_16x16x32_bf16 v[50:53], v[154:157], v[162:165], v[50:53]
	v_mfma_f32_16x16x32_bf16 v[46:49], v[146:149], v[170:173], v[46:49]
	v_mfma_f32_16x16x32_bf16 v[42:45], v[154:157], v[170:173], v[42:45]
	v_mfma_f32_16x16x32_bf16 v[34:37], v[146:149], v[178:181], v[34:37]
	v_mfma_f32_16x16x32_bf16 v[30:33], v[154:157], v[178:181], v[30:33]
	v_mfma_f32_16x16x32_bf16 v[18:21], v[146:149], v[186:189], v[18:21]
	v_mfma_f32_16x16x32_bf16 v[14:17], v[154:157], v[186:189], v[14:17]
	v_mfma_f32_16x16x32_bf16 v[54:57], v[150:153], v[166:169], v[54:57]
	v_mfma_f32_16x16x32_bf16 v[50:53], v[158:161], v[166:169], v[50:53]
	v_mfma_f32_16x16x32_bf16 v[46:49], v[150:153], v[174:177], v[46:49]
	v_mfma_f32_16x16x32_bf16 v[42:45], v[158:161], v[174:177], v[42:45]
	v_mfma_f32_16x16x32_bf16 v[34:37], v[150:153], v[182:185], v[34:37]
	v_mfma_f32_16x16x32_bf16 v[30:33], v[158:161], v[182:185], v[30:33]
	v_mfma_f32_16x16x32_bf16 v[18:21], v[150:153], v[190:193], v[18:21]
	v_mfma_f32_16x16x32_bf16 v[14:17], v[158:161], v[190:193], v[14:17]
	s_barrier
	s_add_i32 s2, s82, s49
	v_lshl_add_u64 v[210:211], s[66:67], 0, v[196:197]
	s_mov_b32 m0, s2
	ds_read_b128 v[162:165], v209 offset:16384
	ds_read_b128 v[166:169], v209 offset:17408
	ds_read_b128 v[170:173], v209 offset:18432
	ds_read_b128 v[174:177], v209 offset:19456
	ds_read_b128 v[178:181], v209 offset:20480
	ds_read_b128 v[182:185], v209 offset:21504
	ds_read_b128 v[186:189], v209 offset:22528
	ds_read_b128 v[190:193], v209 offset:23552
	global_load_lds_dwordx4 v[210:211], off
	s_add_i32 m0, s2, 0x2000
	s_add_u32 s68, s66, 0x20000
	v_lshl_add_u64 v[212:213], s[66:67], 0, v[200:201]
	s_addc_u32 s69, s67, 0
	s_add_i32 s2, s83, s49
	global_load_lds_dwordx4 v[212:213], off
	v_lshl_add_u64 v[214:215], s[68:69], 0, v[196:197]
	s_mov_b32 m0, s2
	s_nop 0
	global_load_lds_dwordx4 v[214:215], off
	s_add_i32 m0, s2, 0x2000
	s_add_u32 s64, s64, s70
	v_lshl_add_u64 v[214:215], s[68:69], 0, v[200:201]
	s_addc_u32 s65, s65, 0
	global_load_lds_dwordx4 v[214:215], off
	v_lshl_add_u64 v[214:215], s[64:65], 0, v[194:195]
	s_mov_b32 m0, s50
	v_lshl_add_u64 v[216:217], s[64:65], 0, v[198:199]
	global_load_lds_dwordx4 v[214:215], off
	s_mov_b32 m0, s51
	s_nop 0
	global_load_lds_dwordx4 v[216:217], off
	s_waitcnt vmcnt(8)
	s_waitcnt lgkmcnt(0)
	s_barrier
	s_waitcnt lgkmcnt(0)
	v_mfma_f32_16x16x32_bf16 v[126:129], v[130:133], v[162:165], v[126:129]
	v_mfma_f32_16x16x32_bf16 v[122:125], v[138:141], v[162:165], v[122:125]
	v_mfma_f32_16x16x32_bf16 v[110:113], v[130:133], v[170:173], v[110:113]
	v_mfma_f32_16x16x32_bf16 v[106:109], v[138:141], v[170:173], v[106:109]
	v_mfma_f32_16x16x32_bf16 v[94:97], v[130:133], v[178:181], v[94:97]
	v_mfma_f32_16x16x32_bf16 v[90:93], v[138:141], v[178:181], v[90:93]
	v_mfma_f32_16x16x32_bf16 v[22:25], v[130:133], v[186:189], v[22:25]
	v_mfma_f32_16x16x32_bf16 v[10:13], v[138:141], v[186:189], v[10:13]
	v_mfma_f32_16x16x32_bf16 v[126:129], v[134:137], v[166:169], v[126:129]
	v_mfma_f32_16x16x32_bf16 v[122:125], v[142:145], v[166:169], v[122:125]
	v_mfma_f32_16x16x32_bf16 v[110:113], v[134:137], v[174:177], v[110:113]
	v_mfma_f32_16x16x32_bf16 v[106:109], v[142:145], v[174:177], v[106:109]
	v_mfma_f32_16x16x32_bf16 v[94:97], v[134:137], v[182:185], v[94:97]
	v_mfma_f32_16x16x32_bf16 v[90:93], v[142:145], v[182:185], v[90:93]
	v_mfma_f32_16x16x32_bf16 v[22:25], v[134:137], v[190:193], v[22:25]
	v_mfma_f32_16x16x32_bf16 v[10:13], v[142:145], v[190:193], v[10:13]
	v_mfma_f32_16x16x32_bf16 v[118:121], v[146:149], v[162:165], v[118:121]
	v_mfma_f32_16x16x32_bf16 v[114:117], v[154:157], v[162:165], v[114:117]
	v_mfma_f32_16x16x32_bf16 v[102:105], v[146:149], v[170:173], v[102:105]
	v_mfma_f32_16x16x32_bf16 v[98:101], v[154:157], v[170:173], v[98:101]
	v_mfma_f32_16x16x32_bf16 v[38:41], v[146:149], v[178:181], v[38:41]
	v_mfma_f32_16x16x32_bf16 v[26:29], v[154:157], v[178:181], v[26:29]
	v_mfma_f32_16x16x32_bf16 v[6:9], v[146:149], v[186:189], v[6:9]
	v_mfma_f32_16x16x32_bf16 v[2:5], v[154:157], v[186:189], v[2:5]
	v_mfma_f32_16x16x32_bf16 v[118:121], v[150:153], v[166:169], v[118:121]
	v_mfma_f32_16x16x32_bf16 v[114:117], v[158:161], v[166:169], v[114:117]
	v_mfma_f32_16x16x32_bf16 v[102:105], v[150:153], v[174:177], v[102:105]
	v_mfma_f32_16x16x32_bf16 v[98:101], v[158:161], v[174:177], v[98:101]
	v_mfma_f32_16x16x32_bf16 v[38:41], v[150:153], v[182:185], v[38:41]
	v_mfma_f32_16x16x32_bf16 v[26:29], v[158:161], v[182:185], v[26:29]
	v_mfma_f32_16x16x32_bf16 v[6:9], v[150:153], v[190:193], v[6:9]
	v_mfma_f32_16x16x32_bf16 v[2:5], v[158:161], v[190:193], v[2:5]
	s_barrier
	s_add_i32 s2, 0, 0x18000
	s_add_i32 s68, 0, 0x1c000
	v_add_u32_e32 v130, s2, v205
	v_add_u32_e32 v142, s68, v205
	ds_read_b128 v[146:149], v130
	ds_read_b128 v[150:153], v130 offset:1024
	ds_read_b128 v[154:157], v130 offset:2048
	ds_read_b128 v[158:161], v130 offset:3072
	ds_read_b128 v[130:133], v142
	ds_read_b128 v[134:137], v142 offset:1024
	ds_read_b128 v[138:141], v142 offset:2048
	ds_read_b128 v[142:145], v142 offset:3072
	s_add_u32 s64, s64, 0x20000
	s_addc_u32 s65, s65, 0
	s_mov_b32 m0, s52
	v_lshl_add_u64 v[218:219], s[64:65], 0, v[194:195]
	ds_read_b128 v[162:165], v209 offset:32768
	ds_read_b128 v[166:169], v209 offset:33792
	ds_read_b128 v[170:173], v209 offset:34816
	ds_read_b128 v[174:177], v209 offset:35840
	ds_read_b128 v[178:181], v209 offset:36864
	ds_read_b128 v[182:185], v209 offset:37888
	ds_read_b128 v[186:189], v209 offset:38912
	ds_read_b128 v[190:193], v209 offset:39936
	global_load_lds_dwordx4 v[218:219], off
	v_lshl_add_u64 v[218:219], s[64:65], 0, v[198:199]
	s_mov_b32 m0, s53
	s_nop 0
	global_load_lds_dwordx4 v[218:219], off
	s_waitcnt vmcnt(8)
	s_waitcnt lgkmcnt(0)
	s_barrier
	s_waitcnt lgkmcnt(0)
	v_mfma_f32_16x16x32_bf16 v[86:89], v[146:149], v[162:165], v[86:89]
	v_mfma_f32_16x16x32_bf16 v[82:85], v[154:157], v[162:165], v[82:85]
	v_mfma_f32_16x16x32_bf16 v[78:81], v[146:149], v[170:173], v[78:81]
	v_mfma_f32_16x16x32_bf16 v[74:77], v[154:157], v[170:173], v[74:77]
	v_mfma_f32_16x16x32_bf16 v[70:73], v[146:149], v[178:181], v[70:73]
	v_mfma_f32_16x16x32_bf16 v[66:69], v[154:157], v[178:181], v[66:69]
	v_mfma_f32_16x16x32_bf16 v[62:65], v[146:149], v[186:189], v[62:65]
	v_mfma_f32_16x16x32_bf16 v[58:61], v[154:157], v[186:189], v[58:61]
	v_mfma_f32_16x16x32_bf16 v[86:89], v[150:153], v[166:169], v[86:89]
	v_mfma_f32_16x16x32_bf16 v[82:85], v[158:161], v[166:169], v[82:85]
	v_mfma_f32_16x16x32_bf16 v[78:81], v[150:153], v[174:177], v[78:81]
	v_mfma_f32_16x16x32_bf16 v[74:77], v[158:161], v[174:177], v[74:77]
	v_mfma_f32_16x16x32_bf16 v[70:73], v[150:153], v[182:185], v[70:73]
	v_mfma_f32_16x16x32_bf16 v[66:69], v[158:161], v[182:185], v[66:69]
	v_mfma_f32_16x16x32_bf16 v[62:65], v[150:153], v[190:193], v[62:65]
	v_mfma_f32_16x16x32_bf16 v[58:61], v[158:161], v[190:193], v[58:61]
	v_mfma_f32_16x16x32_bf16 v[54:57], v[130:133], v[162:165], v[54:57]
	v_mfma_f32_16x16x32_bf16 v[50:53], v[138:141], v[162:165], v[50:53]
	v_mfma_f32_16x16x32_bf16 v[46:49], v[130:133], v[170:173], v[46:49]
	v_mfma_f32_16x16x32_bf16 v[42:45], v[138:141], v[170:173], v[42:45]
	v_mfma_f32_16x16x32_bf16 v[34:37], v[130:133], v[178:181], v[34:37]
	v_mfma_f32_16x16x32_bf16 v[30:33], v[138:141], v[178:181], v[30:33]
	v_mfma_f32_16x16x32_bf16 v[18:21], v[130:133], v[186:189], v[18:21]
	v_mfma_f32_16x16x32_bf16 v[14:17], v[138:141], v[186:189], v[14:17]
	v_mfma_f32_16x16x32_bf16 v[54:57], v[134:137], v[166:169], v[54:57]
	v_mfma_f32_16x16x32_bf16 v[50:53], v[142:145], v[166:169], v[50:53]
	v_mfma_f32_16x16x32_bf16 v[46:49], v[134:137], v[174:177], v[46:49]
	v_mfma_f32_16x16x32_bf16 v[42:45], v[142:145], v[174:177], v[42:45]
	v_mfma_f32_16x16x32_bf16 v[34:37], v[134:137], v[182:185], v[34:37]
	v_mfma_f32_16x16x32_bf16 v[30:33], v[142:145], v[182:185], v[30:33]
	v_mfma_f32_16x16x32_bf16 v[18:21], v[134:137], v[190:193], v[18:21]
	v_mfma_f32_16x16x32_bf16 v[14:17], v[142:145], v[190:193], v[14:17]
	s_barrier
	s_add_i32 s2, s2, s49
	v_lshl_add_u64 v[210:211], v[210:211], 0, s[12:13]
	s_mov_b32 m0, s2
	ds_read_b128 v[186:189], v209 offset:49152
	ds_read_b128 v[190:193], v209 offset:50176
	ds_read_b128 v[178:181], v209 offset:51200
	ds_read_b128 v[182:185], v209 offset:52224
	ds_read_b128 v[170:173], v209 offset:53248
	ds_read_b128 v[174:177], v209 offset:54272
	ds_read_b128 v[162:165], v209 offset:55296
	ds_read_b128 v[166:169], v209 offset:56320
	global_load_lds_dwordx4 v[210:211], off
	s_add_i32 m0, s2, 0x2000
	s_add_u32 s64, s66, 0x20080
	v_lshl_add_u64 v[210:211], v[212:213], 0, s[12:13]
	s_addc_u32 s65, s67, 0
	s_add_i32 s2, s68, s49
	global_load_lds_dwordx4 v[210:211], off
	v_lshl_add_u64 v[210:211], s[64:65], 0, v[196:197]
	s_mov_b32 m0, s2
	s_andn2_b64 vcc, exec, s[62:63]
	global_load_lds_dwordx4 v[210:211], off
	v_lshl_add_u64 v[210:211], s[64:65], 0, v[200:201]
	s_add_i32 m0, s2, 0x2000
	s_nop 0
	global_load_lds_dwordx4 v[210:211], off
	v_lshl_add_u64 v[210:211], v[214:215], 0, s[12:13]
	s_mov_b32 m0, s75
	s_nop 0
	global_load_lds_dwordx4 v[210:211], off
	v_lshl_add_u64 v[210:211], v[216:217], 0, s[12:13]
	s_mov_b32 m0, s76
	s_nop 0
	global_load_lds_dwordx4 v[210:211], off
	s_waitcnt vmcnt(8)
	s_waitcnt lgkmcnt(0)
	s_barrier
	s_cbranch_vccnz .LBB0_1936
	v_pk_mul_f32 v[214:215], v[86:87], s[20:21] op_sel_hi:[1,0]
	v_pk_mul_f32 v[216:217], v[82:83], s[20:21] op_sel_hi:[1,0]
	v_mov_b32_e32 v218, 0
	v_mov_b32_e32 v219, 0
	v_cvt_pk_fp8_f32 v218, v214, v215
	v_cvt_pk_fp8_f32 v219, v216, v217
	v_pk_mul_f32 v[214:215], v[88:89], s[20:21] op_sel_hi:[1,0]
	v_pk_mul_f32 v[216:217], v[84:85], s[20:21] op_sel_hi:[1,0]
	v_cvt_pk_fp8_f32 v218, v214, v215 op_sel:[0,0,1]
	v_cvt_pk_fp8_f32 v219, v216, v217 op_sel:[0,0,1]
	v_pk_mul_f32 v[214:215], v[54:55], s[20:21] op_sel_hi:[1,0]
	v_pk_mul_f32 v[216:217], v[50:51], s[20:21] op_sel_hi:[1,0]
	v_mov_b32_e32 v220, 0
	v_mov_b32_e32 v221, 0
	v_mov_b32_e32 v210, v1
	v_mov_b32_e32 v211, v204
	v_cvt_pk_fp8_f32 v220, v214, v215
	v_cvt_pk_fp8_f32 v221, v216, v217
	v_pk_mul_f32 v[214:215], v[56:57], s[20:21] op_sel_hi:[1,0]
	v_add_u32_e32 v210, s87, v210
	v_lshl_add_u32 v212, v211, 3, s88
	v_ashrrev_i32_e32 v211, 31, v210
	v_pk_mul_f32 v[216:217], v[52:53], s[20:21] op_sel_hi:[1,0]
	v_lshlrev_b64 v[210:211], 11, v[210:211]
	v_cvt_pk_fp8_f32 v220, v214, v215 op_sel:[0,0,1]
	v_cvt_pk_fp8_f32 v221, v216, v217 op_sel:[0,0,1]
	v_ashrrev_i32_e32 v213, 31, v212
	v_lshl_add_u64 v[210:211], s[10:11], 0, v[210:211]
	v_lshl_add_u64 v[210:211], v[210:211], 0, v[212:213]
	global_store_dwordx2 v[210:211], v[218:219], off
	global_store_dwordx2 v[210:211], v[220:221], off offset:128
	v_pk_mul_f32 v[214:215], v[78:79], s[20:21] op_sel_hi:[1,0]
	v_pk_mul_f32 v[216:217], v[74:75], s[20:21] op_sel_hi:[1,0]
	v_mov_b32_e32 v218, 0
	v_mov_b32_e32 v219, 0
	v_cvt_pk_fp8_f32 v218, v214, v215
	v_cvt_pk_fp8_f32 v219, v216, v217
	v_pk_mul_f32 v[214:215], v[80:81], s[20:21] op_sel_hi:[1,0]
	v_pk_mul_f32 v[216:217], v[76:77], s[20:21] op_sel_hi:[1,0]
	v_cvt_pk_fp8_f32 v218, v214, v215 op_sel:[0,0,1]
	v_cvt_pk_fp8_f32 v219, v216, v217 op_sel:[0,0,1]
	v_pk_mul_f32 v[214:215], v[46:47], s[20:21] op_sel_hi:[1,0]
	v_pk_mul_f32 v[216:217], v[42:43], s[20:21] op_sel_hi:[1,0]
	v_mov_b32_e32 v220, 0
	v_mov_b32_e32 v221, 0
	v_cvt_pk_fp8_f32 v220, v214, v215
	v_cvt_pk_fp8_f32 v221, v216, v217
	v_pk_mul_f32 v[214:215], v[48:49], s[20:21] op_sel_hi:[1,0]
	v_pk_mul_f32 v[216:217], v[44:45], s[20:21] op_sel_hi:[1,0]
	v_cvt_pk_fp8_f32 v220, v214, v215 op_sel:[0,0,1]
	v_cvt_pk_fp8_f32 v221, v216, v217 op_sel:[0,0,1]
	s_mov_b32 s2, 0x8000
	v_add_co_u32_e32 v214, vcc, s2, v210
	v_lshl_add_u64 v[212:213], v[210:211], 0, s[24:25]
	s_nop 0
	v_addc_co_u32_e32 v215, vcc, 0, v211, vcc
	global_store_dwordx2 v[214:215], v[218:219], off
	global_store_dwordx2 v[212:213], v[220:221], off offset:128
	v_pk_mul_f32 v[214:215], v[70:71], s[20:21] op_sel_hi:[1,0]
	v_pk_mul_f32 v[216:217], v[66:67], s[20:21] op_sel_hi:[1,0]
	v_mov_b32_e32 v218, 0
	v_mov_b32_e32 v219, 0
	v_cvt_pk_fp8_f32 v218, v214, v215
	v_cvt_pk_fp8_f32 v219, v216, v217
	v_pk_mul_f32 v[214:215], v[72:73], s[20:21] op_sel_hi:[1,0]
	v_pk_mul_f32 v[216:217], v[68:69], s[20:21] op_sel_hi:[1,0]
	v_cvt_pk_fp8_f32 v218, v214, v215 op_sel:[0,0,1]
	v_cvt_pk_fp8_f32 v219, v216, v217 op_sel:[0,0,1]
	v_pk_mul_f32 v[214:215], v[34:35], s[20:21] op_sel_hi:[1,0]
	v_pk_mul_f32 v[216:217], v[30:31], s[20:21] op_sel_hi:[1,0]
	v_mov_b32_e32 v220, 0
	v_mov_b32_e32 v221, 0
	v_cvt_pk_fp8_f32 v220, v214, v215
	v_cvt_pk_fp8_f32 v221, v216, v217
	v_pk_mul_f32 v[214:215], v[36:37], s[20:21] op_sel_hi:[1,0]
	v_pk_mul_f32 v[216:217], v[32:33], s[20:21] op_sel_hi:[1,0]
	v_cvt_pk_fp8_f32 v220, v214, v215 op_sel:[0,0,1]
	v_cvt_pk_fp8_f32 v221, v216, v217 op_sel:[0,0,1]
	s_mov_b32 s2, 0x10000
	v_add_co_u32_e32 v214, vcc, s2, v210
	v_lshl_add_u64 v[212:213], v[210:211], 0, s[28:29]
	s_nop 0
	v_addc_co_u32_e32 v215, vcc, 0, v211, vcc
	global_store_dwordx2 v[214:215], v[218:219], off
	global_store_dwordx2 v[212:213], v[220:221], off offset:128
	v_pk_mul_f32 v[214:215], v[62:63], s[20:21] op_sel_hi:[1,0]
	v_pk_mul_f32 v[216:217], v[58:59], s[20:21] op_sel_hi:[1,0]
	v_mov_b32_e32 v218, 0
	v_mov_b32_e32 v219, 0
	v_cvt_pk_fp8_f32 v218, v214, v215
	v_cvt_pk_fp8_f32 v219, v216, v217
	v_pk_mul_f32 v[214:215], v[64:65], s[20:21] op_sel_hi:[1,0]
	v_pk_mul_f32 v[216:217], v[60:61], s[20:21] op_sel_hi:[1,0]
	v_cvt_pk_fp8_f32 v218, v214, v215 op_sel:[0,0,1]
	v_cvt_pk_fp8_f32 v219, v216, v217 op_sel:[0,0,1]
	v_pk_mul_f32 v[214:215], v[18:19], s[20:21] op_sel_hi:[1,0]
	v_pk_mul_f32 v[216:217], v[14:15], s[20:21] op_sel_hi:[1,0]
	v_mov_b32_e32 v220, 0
	v_mov_b32_e32 v221, 0
	v_cvt_pk_fp8_f32 v220, v214, v215
	v_cvt_pk_fp8_f32 v221, v216, v217
	v_pk_mul_f32 v[214:215], v[20:21], s[20:21] op_sel_hi:[1,0]
	v_pk_mul_f32 v[216:217], v[16:17], s[20:21] op_sel_hi:[1,0]
	v_cvt_pk_fp8_f32 v220, v214, v215 op_sel:[0,0,1]
	v_cvt_pk_fp8_f32 v221, v216, v217 op_sel:[0,0,1]
	s_mov_b32 s2, 0x18000
	v_lshl_add_u64 v[212:213], v[210:211], 0, s[30:31]
	v_add_co_u32_e32 v210, vcc, s2, v210
	s_nop 1
	v_addc_co_u32_e32 v211, vcc, 0, v211, vcc
	global_store_dwordx2 v[210:211], v[218:219], off
	global_store_dwordx2 v[212:213], v[220:221], off offset:128
	s_branch .LBB0_1936
